# static priority raise: one s_setprio 1 for waves 4-7 at each GEMM phase entry (reset at exit), all per-segment s_setprio flips deleted
# baseline (speedup 1.0000x reference)
; #define PG8_STAGE_B(bufoff, gbase) do { _Pragma("unroll") for (int _i = 0; _i < 2; ++_i) \
;         __builtin_amdgcn_global_load_lds((const unsigned*)((const char*)(gbase) + voffB[_i]), (LAS unsigned*)(lds + (bufoff) + ldsw + _i * 8192), 16, 0, 0); } while (0)
; #define PG8_STAGE_A(bufoff, gbase, VO, h) do { _Pragma("unroll") for (int _i = 0; _i < 2; ++_i) \
;         __builtin_amdgcn_global_load_lds((const unsigned*)((const char*)(gbase) + (VO)[h][_i]), (LAS unsigned*)(lds + (bufoff) + ldsw + _i * 8192), 16, 0, 0); } while (0)
; #define PG8_BAR __builtin_amdgcn_s_barrier()
;     ...
;     for (int i = 0; i < 2; ++i) { int R, C; stage_rc(tid * 16 + i * 8192, R, C); const int Rb = (R & ~31) + perm32(R & 31);
;         Rr[i] = R; Cc[i] = C; voffB[i] = nB64 ? (unsigned)(Rb * 64 + ((C * 2) & 63) + ((C * 2) >> 6) * nB64 * 64) : (unsigned)(Rb * ldb + C) * 2u;
;         voffA[0][i] = (unsigned)(R * lda + C) * 2u; voffA[1][i] = (unsigned)((R + HALF) * lda + C) * 2u; voffN[0][i] = voffA[0][i]; voffN[1][i] = voffA[1][i]; }
;     const size_t kstep = (size_t)(BK * 2);
;     const size_t kstepB = kstepB_arg ? kstepB_arg : kstep;
;     const size_t hstepB = nB64 ? (size_t)HALF * 64 : (size_t)HALF * ldb * 2;
;     const unsigned ldsw = (unsigned)wid * 1024u;
;     const int aoff = lds_byte(wr * 64 + fr, fq * 8), boff = lds_byte(wc * 32 + fr, fq * 8);
;     ...
;     PG8_STAGE_B(PG8_SB(0, 0), cB); PG8_STAGE_B(PG8_SB(0, 1), cB + hstepB); PG8_STAGE_A(PG8_SA(0, 0), cA, voffA, 0); PG8_STAGE_A(PG8_SA(0, 1), cA, voffA, 1);
;     if (wr == 1) PG8_BAR;
.LBB0_362:
	s_and_b64 vcc, exec, s[0:1]
	s_cbranch_vccnz .LBB0_424
	v_readlane_b32 s0, v249, 40
	s_mov_b32 s1, 0x3ffffe0
	s_waitcnt lgkmcnt(0)
	v_mov_b32_e32 v14, 0x40000
	v_lshl_or_b32 v0, v12, 4, s0
	v_ashrrev_i32_e32 v1, 31, v0
	v_lshrrev_b32_e32 v1, 22, v1
	v_add_u32_e32 v1, v0, v1
	v_ashrrev_i32_e32 v4, 10, v1
	v_mul_i32_i24_e32 v1, 0x400, v4
	v_sub_u32_e32 v1, v0, v1
	v_lshrrev_b32_e32 v2, 4, v1
	v_bitop3_b32 v1, v2, v1, 32 bitop3:0x6c
	v_ashrrev_i32_e32 v3, 31, v1
	v_lshrrev_b32_e32 v3, 26, v3
	v_lshlrev_b32_e32 v2, 3, v4
	v_add_u32_e32 v3, v1, v3
	v_and_b32_e32 v2, -16, v2
	v_ashrrev_i32_e32 v5, 6, v3
	v_and_b32_e32 v3, 0xc0, v3
	v_add_u32_e32 v2, v5, v2
	v_lshlrev_b32_e32 v6, 5, v4
	v_sub_u32_e32 v1, v1, v3
	v_and_b32_e32 v6, 32, v6
	v_ashrrev_i16_sdwa v7, v222, sext(v1) dst_sel:DWORD dst_unused:UNUSED_PAD src0_sel:DWORD src1_sel:BYTE_0
	v_lshlrev_b32_e32 v3, 1, v2
	v_lshrrev_b32_e32 v8, 2, v2
	v_and_b32_e32 v9, 3, v5
	v_add_u32_sdwa v1, v6, sext(v7) dst_sel:DWORD dst_unused:UNUSED_PAD src0_sel:DWORD src1_sel:WORD_0
	v_and_b32_e32 v3, 24, v3
	v_and_b32_e32 v8, 4, v8
	v_and_or_b32 v9, v2, s1, v9
	v_or3_b32 v3, v9, v8, v3
	v_lshlrev_b32_e32 v8, 1, v1
	v_lshrrev_b32_e32 v9, 5, v1
	v_lshl_add_u32 v1, v2, 10, v1
	v_add_u32_e32 v0, 0x2000, v0
	v_lshl_add_u32 v196, v1, 1, v14
	v_ashrrev_i32_e32 v1, 31, v0
	v_lshrrev_b32_e32 v1, 22, v1
	v_mul_i32_i24_e32 v9, 0xc0000, v9
	v_add_u32_e32 v1, v0, v1
	v_and_or_b32 v9, v8, 62, v9
	v_lshl_add_u32 v64, v2, 11, v8
	v_ashrrev_i32_e32 v8, 10, v1
	v_mul_i32_i24_e32 v1, 0x400, v8
	v_sub_u32_e32 v0, v0, v1
	v_lshrrev_b32_e32 v1, 4, v0
	v_bitop3_b32 v0, v1, v0, 32 bitop3:0x6c
	v_ashrrev_i32_e32 v2, 31, v0
	v_lshrrev_b32_e32 v2, 26, v2
	v_add_u32_e32 v2, v0, v2
	v_lshl_add_u32 v194, v3, 6, v9
	v_ashrrev_i32_e32 v9, 6, v2
	v_and_b32_e32 v2, 0xffc0, v2
	v_sub_u32_e32 v0, v0, v2
	v_lshlrev_b32_e32 v1, 3, v8
	v_lshrrev_b16_e32 v2, 7, v0
	v_and_b32_e32 v1, -16, v1
	v_and_b32_e32 v2, 1, v2
	v_add_u32_e32 v1, v9, v1
	v_lshlrev_b32_e32 v3, 5, v8
	v_add_u16_e32 v0, v0, v2
	v_and_b32_e32 v10, 32, v3
	v_ashrrev_i16_sdwa v11, v222, sext(v0) dst_sel:DWORD dst_unused:UNUSED_PAD src0_sel:DWORD src1_sel:BYTE_0
	v_lshlrev_b32_e32 v2, 1, v1
	v_lshrrev_b32_e32 v3, 2, v1
	v_and_b32_e32 v13, 3, v9
	v_add_u32_sdwa v0, v10, sext(v11) dst_sel:DWORD dst_unused:UNUSED_PAD src0_sel:DWORD src1_sel:WORD_0
	v_and_b32_e32 v2, 24, v2
	v_and_b32_e32 v3, 4, v3
	v_and_or_b32 v13, v1, s1, v13
	v_or3_b32 v2, v13, v3, v2
	v_lshrrev_b32_e32 v13, 5, v0
	s_add_i32 s26, s0, 0
	v_lshlrev_b32_e32 v3, 1, v0
	v_mul_i32_i24_e32 v13, 0xc0000, v13
	s_add_i32 s27, s26, 0x10000
	s_add_i32 s28, s26, 0x12000
	v_and_or_b32 v13, v3, 62, v13
	s_mov_b32 m0, s27
	s_add_u32 s0, s2, 0x2000
	v_lshl_add_u32 v198, v2, 6, v13
	global_load_lds_dwordx4 v194, s[2:3]
	s_mov_b32 m0, s28
	s_addc_u32 s1, s3, 0
	s_add_i32 s29, s26, 0x14000
	global_load_lds_dwordx4 v198, s[2:3]
	s_mov_b32 m0, s29
	s_add_i32 s31, s26, 0x16000
	global_load_lds_dwordx4 v194, s[0:1]
	s_mov_b32 m0, s31
	s_add_i32 s34, s26, 0x2000
	global_load_lds_dwordx4 v198, s[0:1]
	s_mov_b32 m0, s26
	v_lshl_add_u32 v200, v1, 11, v3
	global_load_lds_dwordx4 v64, s[4:5]
	s_mov_b32 m0, s34
	s_add_i32 s35, s26, 0x4000
	v_lshl_add_u32 v0, v1, 10, v0
	global_load_lds_dwordx4 v200, s[4:5]
	s_mov_b32 m0, s35
	s_add_i32 s36, s26, 0x6000
	v_lshl_add_u32 v202, v0, 1, v14
	global_load_lds_dwordx4 v196, s[4:5]
	s_mov_b32 m0, s36
	v_readlane_b32 s8, v249, 47
	global_load_lds_dwordx4 v202, s[4:5]
	v_readlane_b32 s9, v249, 48
	v_mov_b32_e32 v201, v65
	v_lshl_add_u64 v[0:1], s[4:5], 0, v[64:65]
	v_cndmask_b32_e64 v13, 0, 1, s[8:9]
	v_lshl_add_u64 v[2:3], s[4:5], 0, v[200:201]
	v_cmp_ne_u32_e64 s[0:1], 1, v13
	s_andn2_b64 vcc, exec, s[8:9]
	s_cbranch_vccnz .LBB0_365
	s_barrier
	s_setprio 1

; #define PG8_STAGE_B(bufoff, gbase) do { _Pragma("unroll") for (int _i = 0; _i < 2; ++_i) \
;         __builtin_amdgcn_global_load_lds((const unsigned*)((const char*)(gbase) + voffB[_i]), (LAS unsigned*)(lds + (bufoff) + ldsw + _i * 8192), 16, 0, 0); } while (0)
; #define PG8_STAGE_A(bufoff, gbase, VO, h) do { _Pragma("unroll") for (int _i = 0; _i < 2; ++_i) \
;         __builtin_amdgcn_global_load_lds((const unsigned*)((const char*)(gbase) + (VO)[h][_i]), (LAS unsigned*)(lds + (bufoff) + ldsw + _i * 8192), 16, 0, 0); } while (0)
; #define PG8_WAIT_V(n) asm volatile("s_waitcnt vmcnt(" #n ")" ::: "memory")
; #define PG8_WAIT_L(n) asm volatile("s_waitcnt lgkmcnt(" #n ")" ::: "memory")
; #define PG8_WAIT_VX(rx) do { if (rx) asm volatile("s_waitcnt vmcnt(%0)" :: "n"(8 + Epi::NVM) : "memory"); else asm volatile("s_waitcnt vmcnt(8)" ::: "memory"); } while (0)
; #define PG8_BAR __builtin_amdgcn_s_barrier()
; #define PG8_SCHED __builtin_amdgcn_sched_barrier(0)
;     ...
;             PG8_WAIT_VX(rx); PG8_WAIT_L(0); PG8_BAR; PG8_MMA(0, 0, At, B0); PG8_MMA(0, 1, At, B1); PG8_BAR; PG8_SCHED;
;             PG8_LDA(At, 1, 1); PG8_STAGE_B(PG8_SB(1, 0), b3); PG8_STAGE_B(PG8_SB(1, 1), b3 + hstepB); PG8_STAGE_A(PG8_SA(1, 0), a3, vo2, 0);
;             PG8_WAIT_V(8); PG8_WAIT_L(0); PG8_BAR; PG8_MMA(1, 0, At, B0); PG8_MMA(1, 1, At, B1); PG8_BAR; PG8_SCHED;
.LBB0_371:
	s_waitcnt lgkmcnt(0)
	s_add_u32 s2, s20, 0x180000
	s_addc_u32 s3, s21, 0
	s_barrier
	s_waitcnt lgkmcnt(0)
	v_mfma_i32_16x16x64_i8 v[142:145], v[158:161], v[186:189], v[142:145]
	v_mfma_i32_16x16x64_i8 v[138:141], v[150:153], v[186:189], v[138:141]
	v_mfma_i32_16x16x64_i8 v[126:129], v[158:161], v[178:181], v[126:129]
	v_mfma_i32_16x16x64_i8 v[122:125], v[150:153], v[178:181], v[122:125]
	v_mfma_i32_16x16x64_i8 v[110:113], v[158:161], v[170:173], v[110:113]
	v_mfma_i32_16x16x64_i8 v[106:109], v[150:153], v[170:173], v[106:109]
	v_mfma_i32_16x16x64_i8 v[94:97], v[158:161], v[166:169], v[94:97]
	v_mfma_i32_16x16x64_i8 v[90:93], v[150:153], v[166:169], v[90:93]
	v_mfma_i32_16x16x64_i8 v[142:145], v[154:157], v[190:193], v[142:145]
	v_mfma_i32_16x16x64_i8 v[138:141], v[146:149], v[190:193], v[138:141]
	v_mfma_i32_16x16x64_i8 v[126:129], v[154:157], v[182:185], v[126:129]
	v_mfma_i32_16x16x64_i8 v[122:125], v[146:149], v[182:185], v[122:125]
	v_mfma_i32_16x16x64_i8 v[110:113], v[154:157], v[174:177], v[110:113]
	v_mfma_i32_16x16x64_i8 v[106:109], v[146:149], v[174:177], v[106:109]
	v_mfma_i32_16x16x64_i8 v[94:97], v[154:157], v[162:165], v[94:97]
	v_mfma_i32_16x16x64_i8 v[90:93], v[146:149], v[162:165], v[90:93]
	v_mfma_i32_16x16x64_i8 v[134:137], v[44:47], v[186:189], v[134:137]
	v_mfma_i32_16x16x64_i8 v[130:133], v[28:31], v[186:189], v[130:133]
	v_mfma_i32_16x16x64_i8 v[118:121], v[44:47], v[178:181], v[118:121]
	v_mfma_i32_16x16x64_i8 v[114:117], v[28:31], v[178:181], v[114:117]
	v_mfma_i32_16x16x64_i8 v[102:105], v[44:47], v[170:173], v[102:105]
	v_mfma_i32_16x16x64_i8 v[98:101], v[28:31], v[170:173], v[98:101]
	v_mfma_i32_16x16x64_i8 v[86:89], v[44:47], v[166:169], v[86:89]
	v_mfma_i32_16x16x64_i8 v[82:85], v[28:31], v[166:169], v[82:85]
	v_mfma_i32_16x16x64_i8 v[134:137], v[40:43], v[190:193], v[134:137]
	v_mfma_i32_16x16x64_i8 v[130:133], v[24:27], v[190:193], v[130:133]
	v_mfma_i32_16x16x64_i8 v[118:121], v[40:43], v[182:185], v[118:121]
	v_mfma_i32_16x16x64_i8 v[114:117], v[24:27], v[182:185], v[114:117]
	v_mfma_i32_16x16x64_i8 v[102:105], v[40:43], v[174:177], v[102:105]
	v_mfma_i32_16x16x64_i8 v[98:101], v[24:27], v[174:177], v[98:101]
	v_mfma_i32_16x16x64_i8 v[86:89], v[40:43], v[162:165], v[86:89]
	v_mfma_i32_16x16x64_i8 v[82:85], v[24:27], v[162:165], v[82:85]
	s_barrier
	s_mov_b32 m0, s37
	v_lshl_add_u64 v[220:221], s[2:3], 0, v[194:195]
	ds_read_b128 v[162:165], v219 offset:49152
	ds_read_b128 v[166:169], v219 offset:50176
	ds_read_b128 v[170:173], v219 offset:51200
	ds_read_b128 v[174:177], v219 offset:52224
	ds_read_b128 v[178:181], v219 offset:53248
	ds_read_b128 v[182:185], v219 offset:54272
	ds_read_b128 v[186:189], v219 offset:55296
	ds_read_b128 v[190:193], v219 offset:56320
	global_load_lds_dwordx4 v[220:221], off
	v_lshl_add_u64 v[220:221], s[2:3], 0, v[198:199]
	s_add_u32 s2, s20, 0x182000
	s_mov_b32 m0, s38
	s_addc_u32 s3, s21, 0
	global_load_lds_dwordx4 v[220:221], off
	v_lshl_add_u64 v[220:221], s[2:3], 0, v[194:195]
	s_mov_b32 m0, s41
	v_lshl_add_u64 v[212:213], v[212:213], 0, s[94:95]
	global_load_lds_dwordx4 v[220:221], off
	v_lshl_add_u64 v[220:221], s[2:3], 0, v[198:199]
	s_mov_b32 m0, s42
	s_nop 0
	global_load_lds_dwordx4 v[220:221], off
	s_mov_b32 m0, s39
	s_nop 0
	global_load_lds_dwordx4 v[212:213], off
	v_lshl_add_u64 v[212:213], v[214:215], 0, s[94:95]
	s_mov_b32 m0, s40
	s_nop 0
	global_load_lds_dwordx4 v[212:213], off
	s_waitcnt vmcnt(8)
	s_waitcnt lgkmcnt(0)
	s_barrier
	s_waitcnt lgkmcnt(0)
	v_mfma_i32_16x16x64_i8 v[78:81], v[158:161], v[162:165], v[78:81]
	v_mfma_i32_16x16x64_i8 v[74:77], v[150:153], v[162:165], v[74:77]
	v_mfma_i32_16x16x64_i8 v[60:63], v[158:161], v[170:173], v[60:63]
	v_mfma_i32_16x16x64_i8 v[56:59], v[150:153], v[170:173], v[56:59]
	v_mfma_i32_16x16x64_i8 v[36:39], v[158:161], v[178:181], v[36:39]
	v_mfma_i32_16x16x64_i8 v[32:35], v[150:153], v[178:181], v[32:35]
	v_mfma_i32_16x16x64_i8 v[12:15], v[158:161], v[186:189], v[12:15]
	v_mfma_i32_16x16x64_i8 v[8:11], v[150:153], v[186:189], v[8:11]
	v_mfma_i32_16x16x64_i8 v[78:81], v[154:157], v[166:169], v[78:81]
	v_mfma_i32_16x16x64_i8 v[74:77], v[146:149], v[166:169], v[74:77]
	v_mfma_i32_16x16x64_i8 v[60:63], v[154:157], v[174:177], v[60:63]
	v_mfma_i32_16x16x64_i8 v[56:59], v[146:149], v[174:177], v[56:59]
	v_mfma_i32_16x16x64_i8 v[36:39], v[154:157], v[182:185], v[36:39]
	v_mfma_i32_16x16x64_i8 v[32:35], v[146:149], v[182:185], v[32:35]
	v_mfma_i32_16x16x64_i8 v[12:15], v[154:157], v[190:193], v[12:15]
	v_mfma_i32_16x16x64_i8 v[8:11], v[146:149], v[190:193], v[8:11]
	v_mfma_i32_16x16x64_i8 v[70:73], v[44:47], v[162:165], v[70:73]
	v_mfma_i32_16x16x64_i8 v[66:69], v[28:31], v[162:165], v[66:69]
	v_mfma_i32_16x16x64_i8 v[52:55], v[44:47], v[170:173], v[52:55]
	v_mfma_i32_16x16x64_i8 v[48:51], v[28:31], v[170:173], v[48:51]
	v_mfma_i32_16x16x64_i8 v[20:23], v[44:47], v[178:181], v[20:23]
	v_mfma_i32_16x16x64_i8 v[16:19], v[28:31], v[178:181], v[16:19]
	v_mfma_i32_16x16x64_i8 v[4:7], v[44:47], v[186:189], v[4:7]
	v_mfma_i32_16x16x64_i8 v[0:3], v[28:31], v[186:189], v[0:3]
	v_mfma_i32_16x16x64_i8 v[70:73], v[40:43], v[166:169], v[70:73]
	v_mfma_i32_16x16x64_i8 v[66:69], v[24:27], v[166:169], v[66:69]
	v_mfma_i32_16x16x64_i8 v[52:55], v[40:43], v[174:177], v[52:55]
	v_mfma_i32_16x16x64_i8 v[48:51], v[24:27], v[174:177], v[48:51]
	v_mfma_i32_16x16x64_i8 v[20:23], v[40:43], v[182:185], v[20:23]
	v_mfma_i32_16x16x64_i8 v[16:19], v[24:27], v[182:185], v[16:19]
	v_mfma_i32_16x16x64_i8 v[4:7], v[40:43], v[190:193], v[4:7]
	v_mfma_i32_16x16x64_i8 v[0:3], v[24:27], v[190:193], v[0:3]
	s_barrier
	s_add_i32 s50, s50, 2
	s_add_u32 s48, s48, 0x300000
	s_addc_u32 s49, s49, 0
	s_add_u32 s18, s18, 0x100
	s_addc_u32 s19, s19, 0
	s_cmp_gt_u32 s50, 13
	s_cbranch_scc1 .LBB0_384

; #define PG8_STAGE_B(bufoff, gbase) do { _Pragma("unroll") for (int _i = 0; _i < 2; ++_i) \
;         __builtin_amdgcn_global_load_lds((const unsigned*)((const char*)(gbase) + voffB[_i]), (LAS unsigned*)(lds + (bufoff) + ldsw + _i * 8192), 16, 0, 0); } while (0)
; #define PG8_STAGE_A(bufoff, gbase, VO, h) do { _Pragma("unroll") for (int _i = 0; _i < 2; ++_i) \
;         __builtin_amdgcn_global_load_lds((const unsigned*)((const char*)(gbase) + (VO)[h][_i]), (LAS unsigned*)(lds + (bufoff) + ldsw + _i * 8192), 16, 0, 0); } while (0)
; #define PG8_WAIT_L(n) asm volatile("s_waitcnt lgkmcnt(" #n ")" ::: "memory")
; #define PG8_WAIT_VX(rx) do { if (rx) asm volatile("s_waitcnt vmcnt(%0)" :: "n"(8 + Epi::NVM) : "memory"); else asm volatile("s_waitcnt vmcnt(8)" ::: "memory"); } while (0)
; #define PG8_BAR __builtin_amdgcn_s_barrier()
; #define PG8_SCHED __builtin_amdgcn_sched_barrier(0)
;     ...
;             PG8_LDB(B0, 0, 0); PG8_LDB(B1, 0, 1); PG8_SCHED; PG8_LDA(At, 0, 0); if (!rx) PG8_STAGE_A(PG8_SA(1, 1), a1, voffA, 1);
;             PG8_WAIT_VX(rx); PG8_WAIT_L(0); PG8_BAR; PG8_MMA(0, 0, At, B0); PG8_MMA(0, 1, At, B1); PG8_BAR; PG8_SCHED;
;             PG8_LDA(At, 0, 1); PG8_STAGE_B(PG8_SB(0, 0), b2); PG8_STAGE_B(PG8_SB(0, 1), b2 + hstepB); PG8_STAGE_A(PG8_SA(0, 0), a2, vo2, 0);
.LBB0_375:
	s_add_u32 s2, s4, s18
	s_addc_u32 s3, s5, s19
	s_add_u32 s2, s2, 0x100
	s_addc_u32 s3, s3, 0
	s_waitcnt lgkmcnt(0)
	s_cmpk_eq_i32 s18, 0x700
	s_cselect_b32 s23, s11, s3
	s_cselect_b32 s22, s10, s2
	s_cselect_b32 s21, s13, s49
	s_cselect_b32 s20, s12, s48
	s_barrier
	s_waitcnt lgkmcnt(0)
	v_mfma_i32_16x16x64_i8 v[142:145], v[158:161], v[186:189], v[142:145]
	v_mfma_i32_16x16x64_i8 v[138:141], v[150:153], v[186:189], v[138:141]
	v_mfma_i32_16x16x64_i8 v[126:129], v[158:161], v[178:181], v[126:129]
	v_mfma_i32_16x16x64_i8 v[122:125], v[150:153], v[178:181], v[122:125]
	v_mfma_i32_16x16x64_i8 v[110:113], v[158:161], v[170:173], v[110:113]
	v_mfma_i32_16x16x64_i8 v[106:109], v[150:153], v[170:173], v[106:109]
	v_mfma_i32_16x16x64_i8 v[94:97], v[158:161], v[166:169], v[94:97]
	v_mfma_i32_16x16x64_i8 v[90:93], v[150:153], v[166:169], v[90:93]
	v_mfma_i32_16x16x64_i8 v[142:145], v[154:157], v[190:193], v[142:145]
	v_mfma_i32_16x16x64_i8 v[138:141], v[146:149], v[190:193], v[138:141]
	v_mfma_i32_16x16x64_i8 v[126:129], v[154:157], v[182:185], v[126:129]
	v_mfma_i32_16x16x64_i8 v[122:125], v[146:149], v[182:185], v[122:125]
	v_mfma_i32_16x16x64_i8 v[110:113], v[154:157], v[174:177], v[110:113]
	v_mfma_i32_16x16x64_i8 v[106:109], v[146:149], v[174:177], v[106:109]
	v_mfma_i32_16x16x64_i8 v[94:97], v[154:157], v[162:165], v[94:97]
	v_mfma_i32_16x16x64_i8 v[90:93], v[146:149], v[162:165], v[90:93]
	v_mfma_i32_16x16x64_i8 v[134:137], v[44:47], v[186:189], v[134:137]
	v_mfma_i32_16x16x64_i8 v[130:133], v[28:31], v[186:189], v[130:133]
	v_mfma_i32_16x16x64_i8 v[118:121], v[44:47], v[178:181], v[118:121]
	v_mfma_i32_16x16x64_i8 v[114:117], v[28:31], v[178:181], v[114:117]
	v_mfma_i32_16x16x64_i8 v[102:105], v[44:47], v[170:173], v[102:105]
	v_mfma_i32_16x16x64_i8 v[98:101], v[28:31], v[170:173], v[98:101]
	v_mfma_i32_16x16x64_i8 v[86:89], v[44:47], v[166:169], v[86:89]
	v_mfma_i32_16x16x64_i8 v[82:85], v[28:31], v[166:169], v[82:85]
	v_mfma_i32_16x16x64_i8 v[134:137], v[40:43], v[190:193], v[134:137]
	v_mfma_i32_16x16x64_i8 v[130:133], v[24:27], v[190:193], v[130:133]
	v_mfma_i32_16x16x64_i8 v[118:121], v[40:43], v[182:185], v[118:121]
	v_mfma_i32_16x16x64_i8 v[114:117], v[24:27], v[182:185], v[114:117]
	v_mfma_i32_16x16x64_i8 v[102:105], v[40:43], v[174:177], v[102:105]
	v_mfma_i32_16x16x64_i8 v[98:101], v[24:27], v[174:177], v[98:101]
	v_mfma_i32_16x16x64_i8 v[86:89], v[40:43], v[162:165], v[86:89]
	v_mfma_i32_16x16x64_i8 v[82:85], v[24:27], v[162:165], v[82:85]
	s_barrier
	s_mov_b32 m0, s27
	v_lshl_add_u64 v[212:213], s[20:21], 0, v[194:195]
	s_add_u32 s2, s20, 0x2000
	ds_read_b128 v[186:189], v219 offset:16384
	ds_read_b128 v[190:193], v219 offset:17408
	ds_read_b128 v[178:181], v219 offset:18432
	ds_read_b128 v[182:185], v219 offset:19456
	ds_read_b128 v[170:173], v219 offset:20480
	ds_read_b128 v[174:177], v219 offset:21504
	ds_read_b128 v[166:169], v219 offset:22528
	ds_read_b128 v[162:165], v219 offset:23552
	global_load_lds_dwordx4 v[212:213], off
	v_lshl_add_u64 v[212:213], s[20:21], 0, v[198:199]
	s_mov_b32 m0, s28
	s_addc_u32 s3, s21, 0
	global_load_lds_dwordx4 v[212:213], off
	v_lshl_add_u64 v[212:213], s[2:3], 0, v[194:195]
	s_mov_b32 m0, s29
	v_lshl_add_u64 v[214:215], s[22:23], 0, v[200:201]
	global_load_lds_dwordx4 v[212:213], off
	v_lshl_add_u64 v[212:213], s[2:3], 0, v[198:199]
	s_mov_b32 m0, s31
	v_cndmask_b32_e64 v220, 0, 1, s[24:25]
	global_load_lds_dwordx4 v[212:213], off
	v_lshl_add_u64 v[212:213], s[22:23], 0, v[64:65]
	s_mov_b32 m0, s26
	v_cmp_ne_u32_e64 s[2:3], 1, v220
	global_load_lds_dwordx4 v[212:213], off
	s_mov_b32 m0, s34
	s_andn2_b64 vcc, exec, s[24:25]
	global_load_lds_dwordx4 v[214:215], off
	s_cbranch_vccnz .LBB0_381
	s_waitcnt vmcnt(24)
	s_cbranch_execnz .LBB0_378

; #define PG8_STAGE_A(bufoff, gbase, VO, h) do { _Pragma("unroll") for (int _i = 0; _i < 2; ++_i) \
;         __builtin_amdgcn_global_load_lds((const unsigned*)((const char*)(gbase) + (VO)[h][_i]), (LAS unsigned*)(lds + (bufoff) + ldsw + _i * 8192), 16, 0, 0); } while (0)
; #define PG8_WAIT_L(n) asm volatile("s_waitcnt lgkmcnt(" #n ")" ::: "memory")
; #define PG8_WAIT_VX(rx) do { if (rx) asm volatile("s_waitcnt vmcnt(%0)" :: "n"(8 + Epi::NVM) : "memory"); else asm volatile("s_waitcnt vmcnt(8)" ::: "memory"); } while (0)
; #define PG8_BAR __builtin_amdgcn_s_barrier()
; #define PG8_SCHED __builtin_amdgcn_sched_barrier(0)
;     ...
;             PG8_WAIT_VX(rx); PG8_WAIT_L(0); PG8_BAR; PG8_MMA(1, 0, At, B0); PG8_MMA(1, 1, At, B1); PG8_BAR; PG8_SCHED;
;             PG8_LDB(B0, 1, 0); PG8_LDB(B1, 1, 1); PG8_SCHED; PG8_LDA(At, 1, 0); PG8_STAGE_A(PG8_SA(0, 1), a2, vo2, 1);
.LBB0_378:
	s_waitcnt lgkmcnt(0)
	s_barrier
	s_waitcnt lgkmcnt(0)
	v_mfma_i32_16x16x64_i8 v[78:81], v[158:161], v[186:189], v[78:81]
	v_mfma_i32_16x16x64_i8 v[74:77], v[150:153], v[186:189], v[74:77]
	v_mfma_i32_16x16x64_i8 v[60:63], v[158:161], v[178:181], v[60:63]
	v_mfma_i32_16x16x64_i8 v[56:59], v[150:153], v[178:181], v[56:59]
	v_mfma_i32_16x16x64_i8 v[36:39], v[158:161], v[170:173], v[36:39]
	v_mfma_i32_16x16x64_i8 v[32:35], v[150:153], v[170:173], v[32:35]
	v_mfma_i32_16x16x64_i8 v[12:15], v[158:161], v[166:169], v[12:15]
	v_mfma_i32_16x16x64_i8 v[8:11], v[150:153], v[166:169], v[8:11]
	v_mfma_i32_16x16x64_i8 v[78:81], v[154:157], v[190:193], v[78:81]
	v_mfma_i32_16x16x64_i8 v[74:77], v[146:149], v[190:193], v[74:77]
	v_mfma_i32_16x16x64_i8 v[60:63], v[154:157], v[182:185], v[60:63]
	v_mfma_i32_16x16x64_i8 v[56:59], v[146:149], v[182:185], v[56:59]
	v_mfma_i32_16x16x64_i8 v[36:39], v[154:157], v[174:177], v[36:39]
	v_mfma_i32_16x16x64_i8 v[32:35], v[146:149], v[174:177], v[32:35]
	v_mfma_i32_16x16x64_i8 v[12:15], v[154:157], v[162:165], v[12:15]
	v_mfma_i32_16x16x64_i8 v[8:11], v[146:149], v[162:165], v[8:11]
	v_mfma_i32_16x16x64_i8 v[70:73], v[44:47], v[186:189], v[70:73]
	v_mfma_i32_16x16x64_i8 v[66:69], v[28:31], v[186:189], v[66:69]
	v_mfma_i32_16x16x64_i8 v[52:55], v[44:47], v[178:181], v[52:55]
	v_mfma_i32_16x16x64_i8 v[48:51], v[28:31], v[178:181], v[48:51]
	v_mfma_i32_16x16x64_i8 v[20:23], v[44:47], v[170:173], v[20:23]
	v_mfma_i32_16x16x64_i8 v[16:19], v[28:31], v[170:173], v[16:19]
	v_mfma_i32_16x16x64_i8 v[4:7], v[44:47], v[166:169], v[4:7]
	v_mfma_i32_16x16x64_i8 v[0:3], v[28:31], v[166:169], v[0:3]
	v_mfma_i32_16x16x64_i8 v[70:73], v[40:43], v[190:193], v[70:73]
	v_mfma_i32_16x16x64_i8 v[66:69], v[24:27], v[190:193], v[66:69]
	v_mfma_i32_16x16x64_i8 v[52:55], v[40:43], v[182:185], v[52:55]
	v_mfma_i32_16x16x64_i8 v[48:51], v[24:27], v[182:185], v[48:51]
	v_mfma_i32_16x16x64_i8 v[20:23], v[40:43], v[174:177], v[20:23]
	v_mfma_i32_16x16x64_i8 v[16:19], v[24:27], v[174:177], v[16:19]
	v_mfma_i32_16x16x64_i8 v[4:7], v[40:43], v[162:165], v[4:7]
	v_mfma_i32_16x16x64_i8 v[0:3], v[24:27], v[162:165], v[0:3]
	s_barrier
	v_add_u32_e32 v24, 0x18000, v218
	ds_read_b128 v[158:161], v24
	ds_read_b128 v[154:157], v24 offset:1024
	ds_read_b128 v[150:153], v24 offset:2048
	ds_read_b128 v[146:149], v24 offset:3072
	v_add_u32_e32 v24, 0x1c000, v218
	ds_read_b128 v[44:47], v24
	ds_read_b128 v[40:43], v24 offset:1024
	ds_read_b128 v[28:31], v24 offset:2048
	ds_read_b128 v[24:27], v24 offset:3072
	s_mov_b32 m0, s35
	v_lshl_add_u64 v[220:221], s[22:23], 0, v[196:197]
	ds_read_b128 v[186:189], v219 offset:32768
	ds_read_b128 v[190:193], v219 offset:33792
	ds_read_b128 v[178:181], v219 offset:34816
	ds_read_b128 v[182:185], v219 offset:35840
	ds_read_b128 v[170:173], v219 offset:36864
	ds_read_b128 v[174:177], v219 offset:37888
	ds_read_b128 v[166:169], v219 offset:38912
	ds_read_b128 v[162:165], v219 offset:39936
	global_load_lds_dwordx4 v[220:221], off
	v_lshl_add_u64 v[220:221], s[22:23], 0, v[202:203]
	s_mov_b32 m0, s36
	s_and_b64 vcc, exec, s[2:3]
	global_load_lds_dwordx4 v[220:221], off
	s_cbranch_vccnz .LBB0_382
	s_waitcnt vmcnt(24)
	s_cbranch_execnz .LBB0_371
	s_branch .LBB0_383

; #define PG8_STAGE_A(bufoff, gbase, VO, h) do { _Pragma("unroll") for (int _i = 0; _i < 2; ++_i) \
;         __builtin_amdgcn_global_load_lds((const unsigned*)((const char*)(gbase) + (VO)[h][_i]), (LAS unsigned*)(lds + (bufoff) + ldsw + _i * 8192), 16, 0, 0); } while (0)
; #define PG8_BAR __builtin_amdgcn_s_barrier()
;     ...
;         }
;         if (ALIGN_EPI) { if (wr == 0) PG8_BAR; }
;         if (ALIGN_EPI && has_next) { if constexpr (GATHER) PG8_STAGE_A(PG8_SA(1, 1), nA + kstep, voffN, 1); else PG8_STAGE_A(PG8_SA(1, 1), nA + kstep, voffA, 1); }
.LBB0_384:
	s_setprio 0
	v_readlane_b32 s2, v249, 49
	v_readlane_b32 s3, v249, 50
	s_and_b64 vcc, exec, s[2:3]
	s_cbranch_vccz .LBB0_386
	s_barrier

; #define PG8_STAGE_B(bufoff, gbase) do { _Pragma("unroll") for (int _i = 0; _i < 2; ++_i) \
;         __builtin_amdgcn_global_load_lds((const unsigned*)((const char*)(gbase) + voffB[_i]), (LAS unsigned*)(lds + (bufoff) + ldsw + _i * 8192), 16, 0, 0); } while (0)
; #define PG8_STAGE_A(bufoff, gbase, VO, h) do { _Pragma("unroll") for (int _i = 0; _i < 2; ++_i) \
;         __builtin_amdgcn_global_load_lds((const unsigned*)((const char*)(gbase) + (VO)[h][_i]), (LAS unsigned*)(lds + (bufoff) + ldsw + _i * 8192), 16, 0, 0); } while (0)
; #define PG8_BAR __builtin_amdgcn_s_barrier()
;     ...
;     for (int i = 0; i < 2; ++i) { int R, C; stage_rc(tid * 16 + i * 8192, R, C); const int Rb = (R & ~31) + perm32(R & 31);
;         Rr[i] = R; Cc[i] = C; voffB[i] = nB64 ? (unsigned)(Rb * 64 + ((C * 2) & 63) + ((C * 2) >> 6) * nB64 * 64) : (unsigned)(Rb * ldb + C) * 2u;
;         voffA[0][i] = (unsigned)(R * lda + C) * 2u; voffA[1][i] = (unsigned)((R + HALF) * lda + C) * 2u; voffN[0][i] = voffA[0][i]; voffN[1][i] = voffA[1][i]; }
;     const size_t kstep = (size_t)(BK * 2);
;     const size_t kstepB = kstepB_arg ? kstepB_arg : kstep;
;     const size_t hstepB = nB64 ? (size_t)HALF * 64 : (size_t)HALF * ldb * 2;
;     const unsigned ldsw = (unsigned)wid * 1024u;
;     const int aoff = lds_byte(wr * 64 + fr, fq * 8), boff = lds_byte(wc * 32 + fr, fq * 8);
;     ...
;     PG8_STAGE_B(PG8_SB(0, 0), cB); PG8_STAGE_B(PG8_SB(0, 1), cB + hstepB); PG8_STAGE_A(PG8_SA(0, 0), cA, voffA, 0); PG8_STAGE_A(PG8_SA(0, 1), cA, voffA, 1);
;     if (wr == 1) PG8_BAR;
.LBB0_610:
	s_and_b64 vcc, exec, s[38:39]
	s_cbranch_vccnz .LBB0_684
	v_readlane_b32 s0, v249, 40
	s_mov_b32 s1, 0x3ffffe0
	v_mov_b32_e32 v14, 0x40000
	v_lshl_or_b32 v0, v12, 4, s0
	v_ashrrev_i32_e32 v1, 31, v0
	v_lshrrev_b32_e32 v1, 22, v1
	v_add_u32_e32 v1, v0, v1
	v_ashrrev_i32_e32 v4, 10, v1
	v_mul_i32_i24_e32 v1, 0x400, v4
	v_sub_u32_e32 v1, v0, v1
	v_lshrrev_b32_e32 v2, 4, v1
	v_bitop3_b32 v1, v2, v1, 32 bitop3:0x6c
	v_ashrrev_i32_e32 v3, 31, v1
	v_lshrrev_b32_e32 v3, 26, v3
	v_lshlrev_b32_e32 v2, 3, v4
	v_add_u32_e32 v3, v1, v3
	v_and_b32_e32 v2, -16, v2
	v_ashrrev_i32_e32 v5, 6, v3
	v_and_b32_e32 v3, 0xc0, v3
	v_add_u32_e32 v2, v5, v2
	v_lshlrev_b32_e32 v6, 5, v4
	v_sub_u32_e32 v1, v1, v3
	v_and_b32_e32 v6, 32, v6
	v_ashrrev_i16_sdwa v7, v222, sext(v1) dst_sel:DWORD dst_unused:UNUSED_PAD src0_sel:DWORD src1_sel:BYTE_0
	v_lshlrev_b32_e32 v3, 1, v2
	v_lshrrev_b32_e32 v8, 2, v2
	v_and_b32_e32 v9, 3, v5
	v_add_u32_sdwa v1, v6, sext(v7) dst_sel:DWORD dst_unused:UNUSED_PAD src0_sel:DWORD src1_sel:WORD_0
	v_and_b32_e32 v3, 24, v3
	v_and_b32_e32 v8, 4, v8
	v_and_or_b32 v9, v2, s1, v9
	v_or3_b32 v3, v9, v8, v3
	v_lshlrev_b32_e32 v8, 1, v1
	v_lshrrev_b32_e32 v9, 5, v1
	v_lshl_add_u32 v1, v2, 10, v1
	v_add_u32_e32 v0, 0x2000, v0
	v_lshl_add_u32 v196, v1, 1, v14
	v_ashrrev_i32_e32 v1, 31, v0
	v_lshrrev_b32_e32 v1, 22, v1
	v_mul_i32_i24_e32 v9, 0xc0000, v9
	v_add_u32_e32 v1, v0, v1
	v_and_or_b32 v9, v8, 62, v9
	v_lshl_add_u32 v64, v2, 11, v8
	v_ashrrev_i32_e32 v8, 10, v1
	v_mul_i32_i24_e32 v1, 0x400, v8
	v_sub_u32_e32 v0, v0, v1
	v_lshrrev_b32_e32 v1, 4, v0
	v_bitop3_b32 v0, v1, v0, 32 bitop3:0x6c
	v_ashrrev_i32_e32 v2, 31, v0
	v_lshrrev_b32_e32 v2, 26, v2
	v_add_u32_e32 v2, v0, v2
	v_lshl_add_u32 v194, v3, 6, v9
	v_ashrrev_i32_e32 v9, 6, v2
	v_and_b32_e32 v2, 0xffc0, v2
	v_sub_u32_e32 v0, v0, v2
	v_lshlrev_b32_e32 v1, 3, v8
	v_lshrrev_b16_e32 v2, 7, v0
	v_and_b32_e32 v1, -16, v1
	v_and_b32_e32 v2, 1, v2
	v_add_u32_e32 v1, v9, v1
	v_lshlrev_b32_e32 v3, 5, v8
	v_add_u16_e32 v0, v0, v2
	v_and_b32_e32 v10, 32, v3
	v_ashrrev_i16_sdwa v11, v222, sext(v0) dst_sel:DWORD dst_unused:UNUSED_PAD src0_sel:DWORD src1_sel:BYTE_0
	v_lshlrev_b32_e32 v2, 1, v1
	v_lshrrev_b32_e32 v3, 2, v1
	v_and_b32_e32 v13, 3, v9
	v_add_u32_sdwa v0, v10, sext(v11) dst_sel:DWORD dst_unused:UNUSED_PAD src0_sel:DWORD src1_sel:WORD_0
	v_and_b32_e32 v2, 24, v2
	v_and_b32_e32 v3, 4, v3
	v_and_or_b32 v13, v1, s1, v13
	v_or3_b32 v2, v13, v3, v2
	v_lshrrev_b32_e32 v13, 5, v0
	s_add_i32 s24, s0, 0
	v_lshlrev_b32_e32 v3, 1, v0
	v_mul_i32_i24_e32 v13, 0xc0000, v13
	s_add_i32 s25, s24, 0x10000
	s_add_i32 s26, s24, 0x12000
	v_and_or_b32 v13, v3, 62, v13
	s_mov_b32 m0, s25
	s_add_u32 s0, s2, 0x2000
	v_lshl_add_u32 v198, v2, 6, v13
	global_load_lds_dwordx4 v194, s[2:3]
	s_mov_b32 m0, s26
	s_addc_u32 s1, s3, 0
	s_add_i32 s27, s24, 0x14000
	global_load_lds_dwordx4 v198, s[2:3]
	s_mov_b32 m0, s27
	s_add_i32 s28, s24, 0x16000
	global_load_lds_dwordx4 v194, s[0:1]
	s_mov_b32 m0, s28
	s_add_i32 s29, s24, 0x2000
	global_load_lds_dwordx4 v198, s[0:1]
	s_mov_b32 m0, s24
	v_lshl_add_u32 v200, v1, 11, v3
	global_load_lds_dwordx4 v64, s[4:5]
	s_mov_b32 m0, s29
	s_add_i32 s31, s24, 0x4000
	v_lshl_add_u32 v0, v1, 10, v0
	global_load_lds_dwordx4 v200, s[4:5]
	s_mov_b32 m0, s31
	s_add_i32 s34, s24, 0x6000
	v_lshl_add_u32 v202, v0, 1, v14
	global_load_lds_dwordx4 v196, s[4:5]
	s_mov_b32 m0, s34
	v_readlane_b32 s6, v249, 47
	global_load_lds_dwordx4 v202, s[4:5]
	v_readlane_b32 s7, v249, 48
	v_mov_b32_e32 v201, v65
	v_lshl_add_u64 v[0:1], s[4:5], 0, v[64:65]
	v_cndmask_b32_e64 v13, 0, 1, s[6:7]
	v_lshl_add_u64 v[2:3], s[4:5], 0, v[200:201]
	v_cmp_ne_u32_e64 s[0:1], 1, v13
	s_andn2_b64 vcc, exec, s[6:7]
	s_cbranch_vccnz .LBB0_613
	s_barrier
	s_setprio 1

; #define PG8_STAGE_B(bufoff, gbase) do { _Pragma("unroll") for (int _i = 0; _i < 2; ++_i) \
;         __builtin_amdgcn_global_load_lds((const unsigned*)((const char*)(gbase) + voffB[_i]), (LAS unsigned*)(lds + (bufoff) + ldsw + _i * 8192), 16, 0, 0); } while (0)
; #define PG8_STAGE_A(bufoff, gbase, VO, h) do { _Pragma("unroll") for (int _i = 0; _i < 2; ++_i) \
;         __builtin_amdgcn_global_load_lds((const unsigned*)((const char*)(gbase) + (VO)[h][_i]), (LAS unsigned*)(lds + (bufoff) + ldsw + _i * 8192), 16, 0, 0); } while (0)
; #define PG8_WAIT_V(n) asm volatile("s_waitcnt vmcnt(" #n ")" ::: "memory")
; #define PG8_WAIT_L(n) asm volatile("s_waitcnt lgkmcnt(" #n ")" ::: "memory")
; #define PG8_WAIT_VX(rx) do { if (rx) asm volatile("s_waitcnt vmcnt(%0)" :: "n"(8 + Epi::NVM) : "memory"); else asm volatile("s_waitcnt vmcnt(8)" ::: "memory"); } while (0)
; #define PG8_BAR __builtin_amdgcn_s_barrier()
; #define PG8_SCHED __builtin_amdgcn_sched_barrier(0)
;     ...
;             PG8_WAIT_VX(rx); PG8_WAIT_L(0); PG8_BAR; PG8_MMA(0, 0, At, B0); PG8_MMA(0, 1, At, B1); PG8_BAR; PG8_SCHED;
;             PG8_LDA(At, 1, 1); PG8_STAGE_B(PG8_SB(1, 0), b3); PG8_STAGE_B(PG8_SB(1, 1), b3 + hstepB); PG8_STAGE_A(PG8_SA(1, 0), a3, vo2, 0);
;             PG8_WAIT_V(8); PG8_WAIT_L(0); PG8_BAR; PG8_MMA(1, 0, At, B0); PG8_MMA(1, 1, At, B1); PG8_BAR; PG8_SCHED;
.LBB0_623:
	s_waitcnt lgkmcnt(0)
	s_add_u32 s2, s18, 0x180000
	s_addc_u32 s3, s19, 0
	s_barrier
	s_waitcnt lgkmcnt(0)
	v_mfma_scale_f32_16x16x128_f8f6f4 v[190:193], v[24:31], v[56:63], v[190:193], v226, v225 op_sel_hi:[0,0,0]
	v_mfma_scale_f32_16x16x128_f8f6f4 v[186:189], v[16:23], v[56:63], v[186:189], v226, v225 op_sel_hi:[0,0,0]
	v_mfma_scale_f32_16x16x128_f8f6f4 v[174:177], v[24:31], v[48:55], v[174:177], v226, v225 op_sel_hi:[0,0,0]
	v_mfma_scale_f32_16x16x128_f8f6f4 v[170:173], v[16:23], v[48:55], v[170:173], v226, v225 op_sel_hi:[0,0,0]
	v_mfma_scale_f32_16x16x128_f8f6f4 v[158:161], v[24:31], v[40:47], v[158:161], v226, v225 op_sel_hi:[0,0,0]
	v_mfma_scale_f32_16x16x128_f8f6f4 v[154:157], v[16:23], v[40:47], v[154:157], v226, v225 op_sel_hi:[0,0,0]
	v_mfma_scale_f32_16x16x128_f8f6f4 v[142:145], v[24:31], v[32:39], v[142:145], v226, v225 op_sel_hi:[0,0,0]
	v_mfma_scale_f32_16x16x128_f8f6f4 v[138:141], v[16:23], v[32:39], v[138:141], v226, v225 op_sel_hi:[0,0,0]
	v_mfma_scale_f32_16x16x128_f8f6f4 v[182:185], v[8:15], v[56:63], v[182:185], v226, v225 op_sel_hi:[0,0,0]
	v_mfma_scale_f32_16x16x128_f8f6f4 v[178:181], v[0:7], v[56:63], v[178:181], v226, v225 op_sel_hi:[0,0,0]
	v_mfma_scale_f32_16x16x128_f8f6f4 v[166:169], v[8:15], v[48:55], v[166:169], v226, v225 op_sel_hi:[0,0,0]
	v_mfma_scale_f32_16x16x128_f8f6f4 v[162:165], v[0:7], v[48:55], v[162:165], v226, v225 op_sel_hi:[0,0,0]
	v_mfma_scale_f32_16x16x128_f8f6f4 v[150:153], v[8:15], v[40:47], v[150:153], v226, v225 op_sel_hi:[0,0,0]
	v_mfma_scale_f32_16x16x128_f8f6f4 v[146:149], v[0:7], v[40:47], v[146:149], v226, v225 op_sel_hi:[0,0,0]
	v_mfma_scale_f32_16x16x128_f8f6f4 v[134:137], v[8:15], v[32:39], v[134:137], v226, v225 op_sel_hi:[0,0,0]
	v_mfma_scale_f32_16x16x128_f8f6f4 v[130:133], v[0:7], v[32:39], v[130:133], v226, v225 op_sel_hi:[0,0,0]
	s_barrier
	s_mov_b32 m0, s35
	v_lshl_add_u64 v[220:221], s[2:3], 0, v[194:195]
	ds_read_b128 v[32:35], v219 offset:49152
	ds_read_b128 v[36:39], v219 offset:50176
	ds_read_b128 v[40:43], v219 offset:51200
	ds_read_b128 v[44:47], v219 offset:52224
	ds_read_b128 v[48:51], v219 offset:53248
	ds_read_b128 v[52:55], v219 offset:54272
	ds_read_b128 v[56:59], v219 offset:55296
	ds_read_b128 v[60:63], v219 offset:56320
	global_load_lds_dwordx4 v[220:221], off
	v_lshl_add_u64 v[220:221], s[2:3], 0, v[198:199]
	s_add_u32 s2, s18, 0x182000
	s_mov_b32 m0, s36
	s_addc_u32 s3, s19, 0
	global_load_lds_dwordx4 v[220:221], off
	v_lshl_add_u64 v[220:221], s[2:3], 0, v[194:195]
	s_mov_b32 m0, s41
	v_lshl_add_u64 v[212:213], v[212:213], 0, s[94:95]
	global_load_lds_dwordx4 v[220:221], off
	v_lshl_add_u64 v[220:221], s[2:3], 0, v[198:199]
	s_mov_b32 m0, s42
	s_nop 0
	global_load_lds_dwordx4 v[220:221], off
	s_mov_b32 m0, s37
	s_nop 0
	global_load_lds_dwordx4 v[212:213], off
	v_lshl_add_u64 v[212:213], v[214:215], 0, s[94:95]
	s_mov_b32 m0, s40
	s_nop 0
	global_load_lds_dwordx4 v[212:213], off
	s_waitcnt vmcnt(8)
	s_waitcnt lgkmcnt(0)
	s_barrier
	s_waitcnt lgkmcnt(0)
	v_mfma_scale_f32_16x16x128_f8f6f4 v[126:129], v[24:31], v[32:39], v[126:129], v226, v225 op_sel_hi:[0,0,0]
	v_mfma_scale_f32_16x16x128_f8f6f4 v[122:125], v[16:23], v[32:39], v[122:125], v226, v225 op_sel_hi:[0,0,0]
	v_mfma_scale_f32_16x16x128_f8f6f4 v[110:113], v[24:31], v[40:47], v[110:113], v226, v225 op_sel_hi:[0,0,0]
	v_mfma_scale_f32_16x16x128_f8f6f4 v[106:109], v[16:23], v[40:47], v[106:109], v226, v225 op_sel_hi:[0,0,0]
	v_mfma_scale_f32_16x16x128_f8f6f4 v[94:97], v[24:31], v[48:55], v[94:97], v226, v225 op_sel_hi:[0,0,0]
	v_mfma_scale_f32_16x16x128_f8f6f4 v[86:89], v[16:23], v[48:55], v[86:89], v226, v225 op_sel_hi:[0,0,0]
	v_mfma_scale_f32_16x16x128_f8f6f4 v[78:81], v[24:31], v[56:63], v[78:81], v226, v225 op_sel_hi:[0,0,0]
	v_mfma_scale_f32_16x16x128_f8f6f4 v[66:69], v[16:23], v[56:63], v[66:69], v226, v225 op_sel_hi:[0,0,0]
	v_mfma_scale_f32_16x16x128_f8f6f4 v[118:121], v[8:15], v[32:39], v[118:121], v226, v225 op_sel_hi:[0,0,0]
	v_mfma_scale_f32_16x16x128_f8f6f4 v[114:117], v[0:7], v[32:39], v[114:117], v226, v225 op_sel_hi:[0,0,0]
	v_mfma_scale_f32_16x16x128_f8f6f4 v[102:105], v[8:15], v[40:47], v[102:105], v226, v225 op_sel_hi:[0,0,0]
	v_mfma_scale_f32_16x16x128_f8f6f4 v[98:101], v[0:7], v[40:47], v[98:101], v226, v225 op_sel_hi:[0,0,0]
	v_mfma_scale_f32_16x16x128_f8f6f4 v[90:93], v[8:15], v[48:55], v[90:93], v226, v225 op_sel_hi:[0,0,0]
	v_mfma_scale_f32_16x16x128_f8f6f4 v[82:85], v[0:7], v[48:55], v[82:85], v226, v225 op_sel_hi:[0,0,0]
	v_mfma_scale_f32_16x16x128_f8f6f4 v[74:77], v[8:15], v[56:63], v[74:77], v226, v225 op_sel_hi:[0,0,0]
	v_mfma_scale_f32_16x16x128_f8f6f4 v[70:73], v[0:7], v[56:63], v[70:73], v226, v225 op_sel_hi:[0,0,0]
	s_barrier
	s_add_i32 s50, s50, 2
	s_add_u32 s48, s48, 0x300000
	s_addc_u32 s49, s49, 0
	s_add_u32 s16, s16, 0x100
	s_addc_u32 s17, s17, 0
	s_cmp_gt_u32 s50, 13
	s_cbranch_scc1 .LBB0_636

; #define PG8_STAGE_B(bufoff, gbase) do { _Pragma("unroll") for (int _i = 0; _i < 2; ++_i) \
;         __builtin_amdgcn_global_load_lds((const unsigned*)((const char*)(gbase) + voffB[_i]), (LAS unsigned*)(lds + (bufoff) + ldsw + _i * 8192), 16, 0, 0); } while (0)
; #define PG8_STAGE_A(bufoff, gbase, VO, h) do { _Pragma("unroll") for (int _i = 0; _i < 2; ++_i) \
;         __builtin_amdgcn_global_load_lds((const unsigned*)((const char*)(gbase) + (VO)[h][_i]), (LAS unsigned*)(lds + (bufoff) + ldsw + _i * 8192), 16, 0, 0); } while (0)
; #define PG8_WAIT_L(n) asm volatile("s_waitcnt lgkmcnt(" #n ")" ::: "memory")
; #define PG8_WAIT_VX(rx) do { if (rx) asm volatile("s_waitcnt vmcnt(%0)" :: "n"(8 + Epi::NVM) : "memory"); else asm volatile("s_waitcnt vmcnt(8)" ::: "memory"); } while (0)
; #define PG8_BAR __builtin_amdgcn_s_barrier()
; #define PG8_SCHED __builtin_amdgcn_sched_barrier(0)
;     ...
;             const bool last = (t == nt - 2); int rxi = (relax && t == 0) ? 1 : 0; asm volatile("" : "+v"(rxi)); const bool rx = __builtin_amdgcn_readfirstlane(rxi) != 0;
;             if constexpr (Epi::HAS_MID) { constexpr int SEGT = (F8 != 0) ? 8 : 16; if (t == SEGT || t == 2 * SEGT) { PG8_SCHED; E.mid(acc, cur, t / SEGT, wr, wc, fr, fq); PG8_SCHED; } }
;             const char* a1 = cA + (size_t)(t + 1) * kstep;
;             const char* a2 = last ? nA : cA + (size_t)(t + 2) * kstep; const char* b2 = last ? nB : cB + (size_t)(t + 2) * kstepB;
;             const char* a3 = a2 + kstep; const char* b3 = b2 + kstepB;
;             unsigned vo2[2][2];
; #pragma unroll
;             for (int h = 0; h < 2; ++h)
; #pragma unroll
;                 for (int i = 0; i < 2; ++i) vo2[h][i] = (GATHER && last) ? voffN[h][i] : voffA[h][i];
;             PG8_LDB(B0, 0, 0); PG8_LDB(B1, 0, 1); PG8_SCHED; PG8_LDA(At, 0, 0); if (!rx) PG8_STAGE_A(PG8_SA(1, 1), a1, voffA, 1);
;             PG8_WAIT_VX(rx); PG8_WAIT_L(0); PG8_BAR; PG8_MMA(0, 0, At, B0); PG8_MMA(0, 1, At, B1); PG8_BAR; PG8_SCHED;
;             PG8_LDA(At, 0, 1); PG8_STAGE_B(PG8_SB(0, 0), b2); PG8_STAGE_B(PG8_SB(0, 1), b2 + hstepB); PG8_STAGE_A(PG8_SA(0, 0), a2, vo2, 0);
.LBB0_627:
	s_add_u32 s2, s4, s16
	s_addc_u32 s3, s5, s17
	s_add_u32 s2, s2, 0x100
	s_addc_u32 s3, s3, 0
	s_waitcnt lgkmcnt(0)
	s_cmpk_eq_i32 s16, 0x700
	s_cselect_b32 s21, s9, s3
	s_cselect_b32 s20, s8, s2
	s_cselect_b32 s19, s11, s49
	s_cselect_b32 s18, s10, s48
	s_barrier
	s_waitcnt lgkmcnt(0)
	v_mfma_scale_f32_16x16x128_f8f6f4 v[190:193], v[24:31], v[56:63], v[190:193], v226, v225 op_sel_hi:[0,0,0]
	v_mfma_scale_f32_16x16x128_f8f6f4 v[186:189], v[16:23], v[56:63], v[186:189], v226, v225 op_sel_hi:[0,0,0]
	v_mfma_scale_f32_16x16x128_f8f6f4 v[174:177], v[24:31], v[48:55], v[174:177], v226, v225 op_sel_hi:[0,0,0]
	v_mfma_scale_f32_16x16x128_f8f6f4 v[170:173], v[16:23], v[48:55], v[170:173], v226, v225 op_sel_hi:[0,0,0]
	v_mfma_scale_f32_16x16x128_f8f6f4 v[158:161], v[24:31], v[40:47], v[158:161], v226, v225 op_sel_hi:[0,0,0]
	v_mfma_scale_f32_16x16x128_f8f6f4 v[154:157], v[16:23], v[40:47], v[154:157], v226, v225 op_sel_hi:[0,0,0]
	v_mfma_scale_f32_16x16x128_f8f6f4 v[142:145], v[24:31], v[32:39], v[142:145], v226, v225 op_sel_hi:[0,0,0]
	v_mfma_scale_f32_16x16x128_f8f6f4 v[138:141], v[16:23], v[32:39], v[138:141], v226, v225 op_sel_hi:[0,0,0]
	v_mfma_scale_f32_16x16x128_f8f6f4 v[182:185], v[8:15], v[56:63], v[182:185], v226, v225 op_sel_hi:[0,0,0]
	v_mfma_scale_f32_16x16x128_f8f6f4 v[178:181], v[0:7], v[56:63], v[178:181], v226, v225 op_sel_hi:[0,0,0]
	v_mfma_scale_f32_16x16x128_f8f6f4 v[166:169], v[8:15], v[48:55], v[166:169], v226, v225 op_sel_hi:[0,0,0]
	v_mfma_scale_f32_16x16x128_f8f6f4 v[162:165], v[0:7], v[48:55], v[162:165], v226, v225 op_sel_hi:[0,0,0]
	v_mfma_scale_f32_16x16x128_f8f6f4 v[150:153], v[8:15], v[40:47], v[150:153], v226, v225 op_sel_hi:[0,0,0]
	v_mfma_scale_f32_16x16x128_f8f6f4 v[146:149], v[0:7], v[40:47], v[146:149], v226, v225 op_sel_hi:[0,0,0]
	v_mfma_scale_f32_16x16x128_f8f6f4 v[134:137], v[8:15], v[32:39], v[134:137], v226, v225 op_sel_hi:[0,0,0]
	v_mfma_scale_f32_16x16x128_f8f6f4 v[130:133], v[0:7], v[32:39], v[130:133], v226, v225 op_sel_hi:[0,0,0]
	s_barrier
	s_mov_b32 m0, s25
	v_lshl_add_u64 v[212:213], s[18:19], 0, v[194:195]
	s_add_u32 s2, s18, 0x2000
	ds_read_b128 v[56:59], v219 offset:16384
	ds_read_b128 v[60:63], v219 offset:17408
	ds_read_b128 v[48:51], v219 offset:18432
	ds_read_b128 v[52:55], v219 offset:19456
	ds_read_b128 v[40:43], v219 offset:20480
	ds_read_b128 v[44:47], v219 offset:21504
	ds_read_b128 v[32:35], v219 offset:22528
	ds_read_b128 v[36:39], v219 offset:23552
	global_load_lds_dwordx4 v[212:213], off
	v_lshl_add_u64 v[212:213], s[18:19], 0, v[198:199]
	s_mov_b32 m0, s26
	s_addc_u32 s3, s19, 0
	global_load_lds_dwordx4 v[212:213], off
	v_lshl_add_u64 v[212:213], s[2:3], 0, v[194:195]
	s_mov_b32 m0, s27
	v_lshl_add_u64 v[214:215], s[20:21], 0, v[200:201]
	global_load_lds_dwordx4 v[212:213], off
	v_lshl_add_u64 v[212:213], s[2:3], 0, v[198:199]
	s_mov_b32 m0, s28
	v_cndmask_b32_e64 v220, 0, 1, s[22:23]
	global_load_lds_dwordx4 v[212:213], off
	v_lshl_add_u64 v[212:213], s[20:21], 0, v[64:65]
	s_mov_b32 m0, s24
	v_cmp_ne_u32_e64 s[2:3], 1, v220
	global_load_lds_dwordx4 v[212:213], off
	s_mov_b32 m0, s29
	s_andn2_b64 vcc, exec, s[22:23]
	global_load_lds_dwordx4 v[214:215], off
	s_cbranch_vccnz .LBB0_633
	s_waitcnt vmcnt(24)
	s_cbranch_execnz .LBB0_630

; #define PG8_STAGE_A(bufoff, gbase, VO, h) do { _Pragma("unroll") for (int _i = 0; _i < 2; ++_i) \
;         __builtin_amdgcn_global_load_lds((const unsigned*)((const char*)(gbase) + (VO)[h][_i]), (LAS unsigned*)(lds + (bufoff) + ldsw + _i * 8192), 16, 0, 0); } while (0)
; #define PG8_WAIT_L(n) asm volatile("s_waitcnt lgkmcnt(" #n ")" ::: "memory")
; #define PG8_WAIT_VX(rx) do { if (rx) asm volatile("s_waitcnt vmcnt(%0)" :: "n"(8 + Epi::NVM) : "memory"); else asm volatile("s_waitcnt vmcnt(8)" ::: "memory"); } while (0)
; #define PG8_BAR __builtin_amdgcn_s_barrier()
; #define PG8_SCHED __builtin_amdgcn_sched_barrier(0)
;     ...
;             PG8_WAIT_VX(rx); PG8_WAIT_L(0); PG8_BAR; PG8_MMA(1, 0, At, B0); PG8_MMA(1, 1, At, B1); PG8_BAR; PG8_SCHED;
;             PG8_LDB(B0, 1, 0); PG8_LDB(B1, 1, 1); PG8_SCHED; PG8_LDA(At, 1, 0); PG8_STAGE_A(PG8_SA(0, 1), a2, vo2, 1);
.LBB0_630:
	s_waitcnt lgkmcnt(0)
	s_barrier
	s_waitcnt lgkmcnt(0)
	v_mfma_scale_f32_16x16x128_f8f6f4 v[126:129], v[24:31], v[56:63], v[126:129], v226, v225 op_sel_hi:[0,0,0]
	v_mfma_scale_f32_16x16x128_f8f6f4 v[122:125], v[16:23], v[56:63], v[122:125], v226, v225 op_sel_hi:[0,0,0]
	v_mfma_scale_f32_16x16x128_f8f6f4 v[110:113], v[24:31], v[48:55], v[110:113], v226, v225 op_sel_hi:[0,0,0]
	v_mfma_scale_f32_16x16x128_f8f6f4 v[106:109], v[16:23], v[48:55], v[106:109], v226, v225 op_sel_hi:[0,0,0]
	v_mfma_scale_f32_16x16x128_f8f6f4 v[94:97], v[24:31], v[40:47], v[94:97], v226, v225 op_sel_hi:[0,0,0]
	v_mfma_scale_f32_16x16x128_f8f6f4 v[86:89], v[16:23], v[40:47], v[86:89], v226, v225 op_sel_hi:[0,0,0]
	v_mfma_scale_f32_16x16x128_f8f6f4 v[78:81], v[24:31], v[32:39], v[78:81], v226, v225 op_sel_hi:[0,0,0]
	v_mfma_scale_f32_16x16x128_f8f6f4 v[66:69], v[16:23], v[32:39], v[66:69], v226, v225 op_sel_hi:[0,0,0]
	v_mfma_scale_f32_16x16x128_f8f6f4 v[118:121], v[8:15], v[56:63], v[118:121], v226, v225 op_sel_hi:[0,0,0]
	v_mfma_scale_f32_16x16x128_f8f6f4 v[114:117], v[0:7], v[56:63], v[114:117], v226, v225 op_sel_hi:[0,0,0]
	v_mfma_scale_f32_16x16x128_f8f6f4 v[102:105], v[8:15], v[48:55], v[102:105], v226, v225 op_sel_hi:[0,0,0]
	v_mfma_scale_f32_16x16x128_f8f6f4 v[98:101], v[0:7], v[48:55], v[98:101], v226, v225 op_sel_hi:[0,0,0]
	v_mfma_scale_f32_16x16x128_f8f6f4 v[90:93], v[8:15], v[40:47], v[90:93], v226, v225 op_sel_hi:[0,0,0]
	v_mfma_scale_f32_16x16x128_f8f6f4 v[82:85], v[0:7], v[40:47], v[82:85], v226, v225 op_sel_hi:[0,0,0]
	v_mfma_scale_f32_16x16x128_f8f6f4 v[74:77], v[8:15], v[32:39], v[74:77], v226, v225 op_sel_hi:[0,0,0]
	v_mfma_scale_f32_16x16x128_f8f6f4 v[70:73], v[0:7], v[32:39], v[70:73], v226, v225 op_sel_hi:[0,0,0]
	s_barrier
	v_add_u32_e32 v0, 0x18000, v218
	v_add_u32_e32 v4, 0x1c000, v218
	ds_read_b128 v[24:27], v0
	ds_read_b128 v[28:31], v0 offset:1024
	ds_read_b128 v[16:19], v0 offset:2048
	ds_read_b128 v[20:23], v0 offset:3072
	ds_read_b128 v[8:11], v4
	ds_read_b128 v[12:15], v4 offset:1024
	ds_read_b128 v[0:3], v4 offset:2048
	ds_read_b128 v[4:7], v4 offset:3072
	s_mov_b32 m0, s31
	v_lshl_add_u64 v[220:221], s[20:21], 0, v[196:197]
	ds_read_b128 v[56:59], v219 offset:32768
	ds_read_b128 v[60:63], v219 offset:33792
	ds_read_b128 v[48:51], v219 offset:34816
	ds_read_b128 v[52:55], v219 offset:35840
	ds_read_b128 v[40:43], v219 offset:36864
	ds_read_b128 v[44:47], v219 offset:37888
	ds_read_b128 v[32:35], v219 offset:38912
	ds_read_b128 v[36:39], v219 offset:39936
	global_load_lds_dwordx4 v[220:221], off
	v_lshl_add_u64 v[220:221], s[20:21], 0, v[202:203]
	s_mov_b32 m0, s34
	s_and_b64 vcc, exec, s[2:3]
	global_load_lds_dwordx4 v[220:221], off
	s_cbranch_vccnz .LBB0_634
	s_waitcnt vmcnt(24)
	s_cbranch_execnz .LBB0_623
	s_branch .LBB0_635

; __device__ __forceinline__ int ltid(int wave0) { int t; asm volatile("v_mbcnt_lo_u32_b32 %0, -1, 0\n\tv_mbcnt_hi_u32_b32 %0, -1, %0" : "=v"(t)); return (wave0 << 6) | t; }
; #define PG8_STAGE_B(bufoff, gbase) do { _Pragma("unroll") for (int _i = 0; _i < 2; ++_i) \
;         __builtin_amdgcn_global_load_lds((const unsigned*)((const char*)(gbase) + voffB[_i]), (LAS unsigned*)(lds + (bufoff) + ldsw + _i * 8192), 16, 0, 0); } while (0)
; #define PG8_STAGE_A(bufoff, gbase, VO, h) do { _Pragma("unroll") for (int _i = 0; _i < 2; ++_i) \
;         __builtin_amdgcn_global_load_lds((const unsigned*)((const char*)(gbase) + (VO)[h][_i]), (LAS unsigned*)(lds + (bufoff) + ldsw + _i * 8192), 16, 0, 0); } while (0)
; #define PG8_BAR __builtin_amdgcn_s_barrier()
;     ...
;     const int tid = ltid(wave0), wid = wave0, lane = tid & 63, wr = wid >> 2, wc = wid & 3, fr = lane & 15, fq = lane >> 4;
;     const int nt = K / BK;
;     unsigned voffB[2], voffA[2][2], voffN[2][2]; int Rr[2], Cc[2];
; #pragma unroll
;     for (int i = 0; i < 2; ++i) { int R, C; stage_rc(tid * 16 + i * 8192, R, C); const int Rb = (R & ~31) + perm32(R & 31);
;         Rr[i] = R; Cc[i] = C; voffB[i] = nB64 ? (unsigned)(Rb * 64 + ((C * 2) & 63) + ((C * 2) >> 6) * nB64 * 64) : (unsigned)(Rb * ldb + C) * 2u;
;         voffA[0][i] = (unsigned)(R * lda + C) * 2u; voffA[1][i] = (unsigned)((R + HALF) * lda + C) * 2u; voffN[0][i] = voffA[0][i]; voffN[1][i] = voffA[1][i]; }
;     ...
;     const char* cA = cur.A; const char* cB = cur.B;
;     PG8_STAGE_B(PG8_SB(0, 0), cB); PG8_STAGE_B(PG8_SB(0, 1), cB + hstepB); PG8_STAGE_A(PG8_SA(0, 0), cA, voffA, 0); PG8_STAGE_A(PG8_SA(0, 1), cA, voffA, 1);
;     if (wr == 1) PG8_BAR;
.LBB0_686:
	s_and_b64 vcc, exec, s[38:39]
	s_cbranch_vccnz .LBB0_726
	v_readlane_b32 s2, v249, 40
	s_mov_b32 s3, 0x3ffffe0
	s_movk_i32 s4, 0x600
	v_lshl_or_b32 v4, v8, 4, s2
	v_ashrrev_i32_e32 v0, 31, v4
	v_lshrrev_b32_e32 v0, 22, v0
	v_add_u32_e32 v0, v4, v0
	v_ashrrev_i32_e32 v0, 10, v0
	v_mul_i32_i24_e32 v1, 0x400, v0
	v_sub_u32_e32 v1, v4, v1
	v_lshrrev_b32_e32 v2, 4, v1
	v_bitop3_b32 v3, v2, v1, 32 bitop3:0x6c
	v_ashrrev_i32_e32 v2, 31, v3
	v_lshrrev_b32_e32 v2, 26, v2
	v_lshlrev_b32_e32 v1, 3, v0
	v_add_u32_e32 v5, v3, v2
	v_and_b32_e32 v1, -16, v1
	v_ashrrev_i32_e32 v2, 6, v5
	v_and_b32_e32 v5, 0xc0, v5
	v_add_u32_e32 v6, v2, v1
	v_lshlrev_b32_e32 v1, 5, v0
	v_sub_u32_e32 v3, v3, v5
	v_and_b32_e32 v1, 32, v1
	v_ashrrev_i16_sdwa v3, v222, sext(v3) dst_sel:DWORD dst_unused:UNUSED_PAD src0_sel:DWORD src1_sel:BYTE_0
	v_lshlrev_b32_e32 v7, 1, v6
	v_lshrrev_b32_e32 v9, 2, v6
	v_and_b32_e32 v10, 3, v2
	v_add_u32_sdwa v5, v1, sext(v3) dst_sel:DWORD dst_unused:UNUSED_PAD src0_sel:DWORD src1_sel:WORD_0
	v_and_b32_e32 v7, 24, v7
	v_and_b32_e32 v9, 4, v9
	v_and_or_b32 v10, v6, s3, v10
	v_mul_lo_u32 v6, v6, s4
	v_or3_b32 v7, v10, v9, v7
	v_lshlrev_b32_e32 v9, 1, v5
	v_lshlrev_b32_e32 v10, 12, v5
	v_add_lshl_u32 v196, v5, v6, 1
	v_add_u32_e32 v5, 0x2000, v4
	v_ashrrev_i32_e32 v4, 31, v5
	v_lshrrev_b32_e32 v4, 22, v4
	v_add_u32_e32 v4, v5, v4
	v_ashrrev_i32_e32 v4, 10, v4
	v_mul_i32_i24_e32 v6, 0x400, v4
	v_and_b32_e32 v9, 62, v9
	s_mov_b32 s5, 0xfffe0000
	v_sub_u32_e32 v5, v5, v6
	v_and_or_b32 v9, v10, s5, v9
	v_lshrrev_b32_e32 v6, 4, v5
	v_lshl_add_u32 v194, v7, 6, v9
	v_bitop3_b32 v7, v6, v5, 32 bitop3:0x6c
	v_ashrrev_i32_e32 v6, 31, v7
	v_lshrrev_b32_e32 v6, 26, v6
	v_add_u32_e32 v9, v7, v6
	v_ashrrev_i32_e32 v6, 6, v9
	v_and_b32_e32 v9, 0xffc0, v9
	v_sub_u32_e32 v7, v7, v9
	v_lshlrev_b32_e32 v5, 3, v4
	v_lshrrev_b16_e32 v9, 7, v7
	v_and_b32_e32 v5, -16, v5
	v_and_b32_e32 v9, 1, v9
	v_add_u32_e32 v10, v6, v5
	v_lshlrev_b32_e32 v5, 5, v4
	v_add_u16_e32 v7, v7, v9
	v_and_b32_e32 v5, 32, v5
	v_ashrrev_i16_sdwa v7, v222, sext(v7) dst_sel:DWORD dst_unused:UNUSED_PAD src0_sel:DWORD src1_sel:BYTE_0
	v_lshlrev_b32_e32 v11, 1, v10
	v_lshrrev_b32_e32 v12, 2, v10
	v_and_b32_e32 v13, 3, v6
	v_add_u32_sdwa v9, v5, sext(v7) dst_sel:DWORD dst_unused:UNUSED_PAD src0_sel:DWORD src1_sel:WORD_0
	v_and_b32_e32 v11, 24, v11
	v_and_b32_e32 v12, 4, v12
	v_and_or_b32 v13, v10, s3, v13
	v_or3_b32 v11, v13, v12, v11
	v_lshlrev_b32_e32 v12, 1, v9
	s_add_i32 s24, s2, 0
	v_and_b32_e32 v12, 62, v12
	v_lshlrev_b32_e32 v13, 12, v9
	s_add_i32 s25, s24, 0x10000
	s_add_i32 s26, s24, 0x12000
	v_and_or_b32 v12, v13, s5, v12
	s_mov_b32 m0, s25
	s_add_u32 s2, s0, 0x2000
	v_lshl_add_u32 v200, v11, 6, v12
	global_load_lds_dwordx4 v194, s[0:1]
	s_mov_b32 m0, s26
	s_addc_u32 s3, s1, 0
	s_add_i32 s27, s24, 0x14000
	global_load_lds_dwordx4 v200, s[0:1]
	s_mov_b32 m0, s27
	s_add_i32 s28, s24, 0x16000
	global_load_lds_dwordx4 v194, s[2:3]
	s_mov_b32 m0, s28
	v_mul_lo_u32 v10, v10, s4
	global_load_lds_dwordx4 v200, s[2:3]
	s_mov_b32 m0, s24
	s_add_i32 s29, s24, 0x2000
	v_add_lshl_u32 v202, v9, v10, 1
	global_load_lds_dwordx4 v196, s[6:7]
	s_mov_b32 m0, s29
	s_add_i32 s34, s24, 0x4000
	v_add_u32_e32 v198, 0x60000, v196
	global_load_lds_dwordx4 v202, s[6:7]
	s_mov_b32 m0, s34
	s_add_i32 s35, s24, 0x6000
	v_add_u32_e32 v204, 0x60000, v202
	global_load_lds_dwordx4 v198, s[6:7]
	s_mov_b32 m0, s35
	v_readlane_b32 s2, v249, 47
	global_load_lds_dwordx4 v204, s[6:7]
	v_readlane_b32 s3, v249, 48
	s_andn2_b64 vcc, exec, s[2:3]
	s_nop 0
	v_cndmask_b32_e64 v9, 0, 1, s[2:3]
	v_cmp_ne_u32_e64 s[40:41], 1, v9
	s_cbranch_vccnz .LBB0_689
	s_barrier
	s_setprio 1

; #define PG8_STAGE_B(bufoff, gbase) do { _Pragma("unroll") for (int _i = 0; _i < 2; ++_i) \
;         __builtin_amdgcn_global_load_lds((const unsigned*)((const char*)(gbase) + voffB[_i]), (LAS unsigned*)(lds + (bufoff) + ldsw + _i * 8192), 16, 0, 0); } while (0)
; #define PG8_STAGE_A(bufoff, gbase, VO, h) do { _Pragma("unroll") for (int _i = 0; _i < 2; ++_i) \
;         __builtin_amdgcn_global_load_lds((const unsigned*)((const char*)(gbase) + (VO)[h][_i]), (LAS unsigned*)(lds + (bufoff) + ldsw + _i * 8192), 16, 0, 0); } while (0)
; #define PG8_WAIT_V(n) asm volatile("s_waitcnt vmcnt(" #n ")" ::: "memory")
; #define PG8_WAIT_L(n) asm volatile("s_waitcnt lgkmcnt(" #n ")" ::: "memory")
; #define PG8_WAIT_VX(rx) do { if (rx) asm volatile("s_waitcnt vmcnt(%0)" :: "n"(8 + Epi::NVM) : "memory"); else asm volatile("s_waitcnt vmcnt(8)" ::: "memory"); } while (0)
; #define PG8_BAR __builtin_amdgcn_s_barrier()
; #define PG8_SCHED __builtin_amdgcn_sched_barrier(0)
;     ...
;             PG8_WAIT_VX(rx); PG8_WAIT_L(0); PG8_BAR; PG8_MMA(0, 0, At, B0); PG8_MMA(0, 1, At, B1); PG8_BAR; PG8_SCHED;
;             PG8_LDA(At, 1, 1); PG8_STAGE_B(PG8_SB(1, 0), b3); PG8_STAGE_B(PG8_SB(1, 1), b3 + hstepB); PG8_STAGE_A(PG8_SA(1, 0), a3, vo2, 0);
;             PG8_WAIT_V(8); PG8_WAIT_L(0); PG8_BAR; PG8_MMA(1, 0, At, B0); PG8_MMA(1, 1, At, B1); PG8_BAR; PG8_SCHED;
.LBB0_699:
	s_waitcnt lgkmcnt(0)
	s_add_u32 s0, s16, 0x40000
	s_addc_u32 s1, s17, 0
	s_barrier
	s_waitcnt lgkmcnt(0)
	v_mfma_scale_f32_16x16x128_f8f6f4 v[190:193], v[24:31], v[56:63], v[190:193], v226, v227 op_sel_hi:[0,0,0]
	v_mfma_scale_f32_16x16x128_f8f6f4 v[186:189], v[16:23], v[56:63], v[186:189], v226, v227 op_sel_hi:[0,0,0]
	v_mfma_scale_f32_16x16x128_f8f6f4 v[174:177], v[24:31], v[48:55], v[174:177], v226, v227 op_sel_hi:[0,0,0]
	v_mfma_scale_f32_16x16x128_f8f6f4 v[170:173], v[16:23], v[48:55], v[170:173], v226, v227 op_sel_hi:[0,0,0]
	v_mfma_scale_f32_16x16x128_f8f6f4 v[158:161], v[24:31], v[40:47], v[158:161], v226, v227 op_sel_hi:[0,0,0]
	v_mfma_scale_f32_16x16x128_f8f6f4 v[154:157], v[16:23], v[40:47], v[154:157], v226, v227 op_sel_hi:[0,0,0]
	v_mfma_scale_f32_16x16x128_f8f6f4 v[142:145], v[24:31], v[32:39], v[142:145], v226, v227 op_sel_hi:[0,0,0]
	v_mfma_scale_f32_16x16x128_f8f6f4 v[138:141], v[16:23], v[32:39], v[138:141], v226, v227 op_sel_hi:[0,0,0]
	v_mfma_scale_f32_16x16x128_f8f6f4 v[182:185], v[8:15], v[56:63], v[182:185], v226, v227 op_sel_hi:[0,0,0]
	v_mfma_scale_f32_16x16x128_f8f6f4 v[178:181], v[0:7], v[56:63], v[178:181], v226, v227 op_sel_hi:[0,0,0]
	v_mfma_scale_f32_16x16x128_f8f6f4 v[166:169], v[8:15], v[48:55], v[166:169], v226, v227 op_sel_hi:[0,0,0]
	v_mfma_scale_f32_16x16x128_f8f6f4 v[162:165], v[0:7], v[48:55], v[162:165], v226, v227 op_sel_hi:[0,0,0]
	v_mfma_scale_f32_16x16x128_f8f6f4 v[150:153], v[8:15], v[40:47], v[150:153], v226, v227 op_sel_hi:[0,0,0]
	v_mfma_scale_f32_16x16x128_f8f6f4 v[146:149], v[0:7], v[40:47], v[146:149], v226, v227 op_sel_hi:[0,0,0]
	v_mfma_scale_f32_16x16x128_f8f6f4 v[134:137], v[8:15], v[32:39], v[134:137], v226, v227 op_sel_hi:[0,0,0]
	v_mfma_scale_f32_16x16x128_f8f6f4 v[130:133], v[0:7], v[32:39], v[130:133], v226, v227 op_sel_hi:[0,0,0]
	s_barrier
	s_mov_b32 m0, s36
	v_lshl_add_u64 v[240:241], s[0:1], 0, v[194:195]
	ds_read_b128 v[32:35], v238 offset:49152
	ds_read_b128 v[36:39], v238 offset:50176
	ds_read_b128 v[40:43], v238 offset:51200
	ds_read_b128 v[44:47], v238 offset:52224
	ds_read_b128 v[48:51], v238 offset:53248
	ds_read_b128 v[52:55], v238 offset:54272
	ds_read_b128 v[56:59], v238 offset:55296
	ds_read_b128 v[60:63], v238 offset:56320
	global_load_lds_dwordx4 v[240:241], off
	v_lshl_add_u64 v[240:241], s[0:1], 0, v[200:201]
	s_add_u32 s0, s16, 0x42000
	s_mov_b32 m0, s37
	s_addc_u32 s1, s17, 0
	global_load_lds_dwordx4 v[240:241], off
	v_lshl_add_u64 v[240:241], s[0:1], 0, v[194:195]
	s_mov_b32 m0, s44
	v_lshl_add_u64 v[218:219], v[218:219], 0, s[94:95]
	global_load_lds_dwordx4 v[240:241], off
	v_lshl_add_u64 v[240:241], s[0:1], 0, v[200:201]
	s_mov_b32 m0, s45
	s_nop 0
	global_load_lds_dwordx4 v[240:241], off
	s_mov_b32 m0, s42
	s_nop 0
	global_load_lds_dwordx4 v[218:219], off
	v_lshl_add_u64 v[218:219], v[220:221], 0, s[94:95]
	s_mov_b32 m0, s43
	s_nop 0
	global_load_lds_dwordx4 v[218:219], off
	s_waitcnt vmcnt(8)
	s_waitcnt lgkmcnt(0)
	s_barrier
	s_waitcnt lgkmcnt(0)
	v_mfma_scale_f32_16x16x128_f8f6f4 v[126:129], v[24:31], v[32:39], v[126:129], v226, v227 op_sel_hi:[0,0,0]
	v_mfma_scale_f32_16x16x128_f8f6f4 v[122:125], v[16:23], v[32:39], v[122:125], v226, v227 op_sel_hi:[0,0,0]
	v_mfma_scale_f32_16x16x128_f8f6f4 v[110:113], v[24:31], v[40:47], v[110:113], v226, v227 op_sel_hi:[0,0,0]
	v_mfma_scale_f32_16x16x128_f8f6f4 v[106:109], v[16:23], v[40:47], v[106:109], v226, v227 op_sel_hi:[0,0,0]
	v_mfma_scale_f32_16x16x128_f8f6f4 v[94:97], v[24:31], v[48:55], v[94:97], v226, v227 op_sel_hi:[0,0,0]
	v_mfma_scale_f32_16x16x128_f8f6f4 v[90:93], v[16:23], v[48:55], v[90:93], v226, v227 op_sel_hi:[0,0,0]
	v_mfma_scale_f32_16x16x128_f8f6f4 v[78:81], v[24:31], v[56:63], v[78:81], v226, v227 op_sel_hi:[0,0,0]
	v_mfma_scale_f32_16x16x128_f8f6f4 v[74:77], v[16:23], v[56:63], v[74:77], v226, v227 op_sel_hi:[0,0,0]
	v_mfma_scale_f32_16x16x128_f8f6f4 v[118:121], v[8:15], v[32:39], v[118:121], v226, v227 op_sel_hi:[0,0,0]
	v_mfma_scale_f32_16x16x128_f8f6f4 v[114:117], v[0:7], v[32:39], v[114:117], v226, v227 op_sel_hi:[0,0,0]
	v_mfma_scale_f32_16x16x128_f8f6f4 v[102:105], v[8:15], v[40:47], v[102:105], v226, v227 op_sel_hi:[0,0,0]
	v_mfma_scale_f32_16x16x128_f8f6f4 v[98:101], v[0:7], v[40:47], v[98:101], v226, v227 op_sel_hi:[0,0,0]
	v_mfma_scale_f32_16x16x128_f8f6f4 v[86:89], v[8:15], v[48:55], v[86:89], v226, v227 op_sel_hi:[0,0,0]
	v_mfma_scale_f32_16x16x128_f8f6f4 v[82:85], v[0:7], v[48:55], v[82:85], v226, v227 op_sel_hi:[0,0,0]
	v_mfma_scale_f32_16x16x128_f8f6f4 v[70:73], v[8:15], v[56:63], v[70:73], v226, v227 op_sel_hi:[0,0,0]
	v_mfma_scale_f32_16x16x128_f8f6f4 v[66:69], v[0:7], v[56:63], v[66:69], v226, v227 op_sel_hi:[0,0,0]
	s_barrier
	s_add_i32 s0, s50, 2
	s_add_u32 s31, s31, 0x80000
	s_addc_u32 s49, s49, 0
	s_add_u32 s14, s14, 0x100
	s_addc_u32 s15, s15, 0
	s_cmp_gt_u32 s50, 21
	s_mov_b32 s50, s0
	s_cbranch_scc1 .LBB0_718

; #define PG8_STAGE_B(bufoff, gbase) do { _Pragma("unroll") for (int _i = 0; _i < 2; ++_i) \
;         __builtin_amdgcn_global_load_lds((const unsigned*)((const char*)(gbase) + voffB[_i]), (LAS unsigned*)(lds + (bufoff) + ldsw + _i * 8192), 16, 0, 0); } while (0)
; #define PG8_STAGE_A(bufoff, gbase, VO, h) do { _Pragma("unroll") for (int _i = 0; _i < 2; ++_i) \
;         __builtin_amdgcn_global_load_lds((const unsigned*)((const char*)(gbase) + (VO)[h][_i]), (LAS unsigned*)(lds + (bufoff) + ldsw + _i * 8192), 16, 0, 0); } while (0)
; #define PG8_WAIT_L(n) asm volatile("s_waitcnt lgkmcnt(" #n ")" ::: "memory")
; #define PG8_WAIT_VX(rx) do { if (rx) asm volatile("s_waitcnt vmcnt(%0)" :: "n"(8 + Epi::NVM) : "memory"); else asm volatile("s_waitcnt vmcnt(8)" ::: "memory"); } while (0)
; #define PG8_BAR __builtin_amdgcn_s_barrier()
; #define PG8_SCHED __builtin_amdgcn_sched_barrier(0)
;     ...
;             const bool last = (t == nt - 2); int rxi = (relax && t == 0) ? 1 : 0; asm volatile("" : "+v"(rxi)); const bool rx = __builtin_amdgcn_readfirstlane(rxi) != 0;
;             if constexpr (Epi::HAS_MID) { constexpr int SEGT = (F8 != 0) ? 8 : 16; if (t == SEGT || t == 2 * SEGT) { PG8_SCHED; E.mid(acc, cur, t / SEGT, wr, wc, fr, fq); PG8_SCHED; } }
;             const char* a1 = cA + (size_t)(t + 1) * kstep;
;             const char* a2 = last ? nA : cA + (size_t)(t + 2) * kstep; const char* b2 = last ? nB : cB + (size_t)(t + 2) * kstepB;
;             const char* a3 = a2 + kstep; const char* b3 = b2 + kstepB;
;             unsigned vo2[2][2];
; #pragma unroll
;             for (int h = 0; h < 2; ++h)
; #pragma unroll
;                 for (int i = 0; i < 2; ++i) vo2[h][i] = (GATHER && last) ? voffN[h][i] : voffA[h][i];
;             PG8_LDB(B0, 0, 0); PG8_LDB(B1, 0, 1); PG8_SCHED; PG8_LDA(At, 0, 0); if (!rx) PG8_STAGE_A(PG8_SA(1, 1), a1, voffA, 1);
;             PG8_WAIT_VX(rx); PG8_WAIT_L(0); PG8_BAR; PG8_MMA(0, 0, At, B0); PG8_MMA(0, 1, At, B1); PG8_BAR; PG8_SCHED;
;             PG8_LDA(At, 0, 1); PG8_STAGE_B(PG8_SB(0, 0), b2); PG8_STAGE_B(PG8_SB(0, 1), b2 + hstepB); PG8_STAGE_A(PG8_SA(0, 0), a2, vo2, 0);
.LBB0_709:
	s_add_u32 s0, s6, s14
	s_addc_u32 s1, s7, s15
	s_add_u32 s0, s0, 0x100
	s_addc_u32 s1, s1, 0
	s_waitcnt lgkmcnt(0)
	s_cmpk_eq_i32 s14, 0xb00
	s_cselect_b32 s19, s3, s1
	s_cselect_b32 s18, s2, s0
	s_cselect_b32 s17, s5, s49
	s_cselect_b32 s16, s4, s31
	s_barrier
	s_waitcnt lgkmcnt(0)
	v_mfma_scale_f32_16x16x128_f8f6f4 v[190:193], v[24:31], v[56:63], v[190:193], v226, v227 op_sel_hi:[0,0,0]
	v_mfma_scale_f32_16x16x128_f8f6f4 v[186:189], v[16:23], v[56:63], v[186:189], v226, v227 op_sel_hi:[0,0,0]
	v_mfma_scale_f32_16x16x128_f8f6f4 v[174:177], v[24:31], v[48:55], v[174:177], v226, v227 op_sel_hi:[0,0,0]
	v_mfma_scale_f32_16x16x128_f8f6f4 v[170:173], v[16:23], v[48:55], v[170:173], v226, v227 op_sel_hi:[0,0,0]
	v_mfma_scale_f32_16x16x128_f8f6f4 v[158:161], v[24:31], v[40:47], v[158:161], v226, v227 op_sel_hi:[0,0,0]
	v_mfma_scale_f32_16x16x128_f8f6f4 v[154:157], v[16:23], v[40:47], v[154:157], v226, v227 op_sel_hi:[0,0,0]
	v_mfma_scale_f32_16x16x128_f8f6f4 v[142:145], v[24:31], v[32:39], v[142:145], v226, v227 op_sel_hi:[0,0,0]
	v_mfma_scale_f32_16x16x128_f8f6f4 v[138:141], v[16:23], v[32:39], v[138:141], v226, v227 op_sel_hi:[0,0,0]
	v_mfma_scale_f32_16x16x128_f8f6f4 v[182:185], v[8:15], v[56:63], v[182:185], v226, v227 op_sel_hi:[0,0,0]
	v_mfma_scale_f32_16x16x128_f8f6f4 v[178:181], v[0:7], v[56:63], v[178:181], v226, v227 op_sel_hi:[0,0,0]
	v_mfma_scale_f32_16x16x128_f8f6f4 v[166:169], v[8:15], v[48:55], v[166:169], v226, v227 op_sel_hi:[0,0,0]
	v_mfma_scale_f32_16x16x128_f8f6f4 v[162:165], v[0:7], v[48:55], v[162:165], v226, v227 op_sel_hi:[0,0,0]
	v_mfma_scale_f32_16x16x128_f8f6f4 v[150:153], v[8:15], v[40:47], v[150:153], v226, v227 op_sel_hi:[0,0,0]
	v_mfma_scale_f32_16x16x128_f8f6f4 v[146:149], v[0:7], v[40:47], v[146:149], v226, v227 op_sel_hi:[0,0,0]
	v_mfma_scale_f32_16x16x128_f8f6f4 v[134:137], v[8:15], v[32:39], v[134:137], v226, v227 op_sel_hi:[0,0,0]
	v_mfma_scale_f32_16x16x128_f8f6f4 v[130:133], v[0:7], v[32:39], v[130:133], v226, v227 op_sel_hi:[0,0,0]
	s_barrier
	s_mov_b32 m0, s25
	v_lshl_add_u64 v[218:219], s[16:17], 0, v[194:195]
	s_add_u32 s0, s16, 0x2000
	ds_read_b128 v[56:59], v238 offset:16384
	ds_read_b128 v[60:63], v238 offset:17408
	ds_read_b128 v[48:51], v238 offset:18432
	ds_read_b128 v[52:55], v238 offset:19456
	ds_read_b128 v[40:43], v238 offset:20480
	ds_read_b128 v[44:47], v238 offset:21504
	ds_read_b128 v[32:35], v238 offset:22528
	ds_read_b128 v[36:39], v238 offset:23552
	global_load_lds_dwordx4 v[218:219], off
	v_lshl_add_u64 v[218:219], s[16:17], 0, v[200:201]
	s_mov_b32 m0, s26
	s_addc_u32 s1, s17, 0
	global_load_lds_dwordx4 v[218:219], off
	v_lshl_add_u64 v[218:219], s[0:1], 0, v[194:195]
	s_mov_b32 m0, s27
	v_lshl_add_u64 v[220:221], s[18:19], 0, v[202:203]
	global_load_lds_dwordx4 v[218:219], off
	v_lshl_add_u64 v[218:219], s[0:1], 0, v[200:201]
	s_mov_b32 m0, s28
	v_cndmask_b32_e64 v64, 0, 1, s[20:21]
	global_load_lds_dwordx4 v[218:219], off
	v_lshl_add_u64 v[218:219], s[18:19], 0, v[196:197]
	s_mov_b32 m0, s24
	v_cmp_ne_u32_e64 s[0:1], 1, v64
	global_load_lds_dwordx4 v[218:219], off
	s_mov_b32 m0, s29
	s_andn2_b64 vcc, exec, s[20:21]
	global_load_lds_dwordx4 v[220:221], off
	s_cbranch_vccnz .LBB0_715
	s_waitcnt vmcnt(24)
	s_cbranch_execnz .LBB0_712

; #define PG8_STAGE_A(bufoff, gbase, VO, h) do { _Pragma("unroll") for (int _i = 0; _i < 2; ++_i) \
;         __builtin_amdgcn_global_load_lds((const unsigned*)((const char*)(gbase) + (VO)[h][_i]), (LAS unsigned*)(lds + (bufoff) + ldsw + _i * 8192), 16, 0, 0); } while (0)
; #define PG8_WAIT_L(n) asm volatile("s_waitcnt lgkmcnt(" #n ")" ::: "memory")
; #define PG8_WAIT_VX(rx) do { if (rx) asm volatile("s_waitcnt vmcnt(%0)" :: "n"(8 + Epi::NVM) : "memory"); else asm volatile("s_waitcnt vmcnt(8)" ::: "memory"); } while (0)
; #define PG8_BAR __builtin_amdgcn_s_barrier()
; #define PG8_SCHED __builtin_amdgcn_sched_barrier(0)
;     ...
;             PG8_WAIT_VX(rx); PG8_WAIT_L(0); PG8_BAR; PG8_MMA(1, 0, At, B0); PG8_MMA(1, 1, At, B1); PG8_BAR; PG8_SCHED;
;             PG8_LDB(B0, 1, 0); PG8_LDB(B1, 1, 1); PG8_SCHED; PG8_LDA(At, 1, 0); PG8_STAGE_A(PG8_SA(0, 1), a2, vo2, 1);
.LBB0_712:
	s_waitcnt lgkmcnt(0)
	s_barrier
	s_waitcnt lgkmcnt(0)
	v_mfma_scale_f32_16x16x128_f8f6f4 v[126:129], v[24:31], v[56:63], v[126:129], v226, v227 op_sel_hi:[0,0,0]
	v_mfma_scale_f32_16x16x128_f8f6f4 v[122:125], v[16:23], v[56:63], v[122:125], v226, v227 op_sel_hi:[0,0,0]
	v_mfma_scale_f32_16x16x128_f8f6f4 v[110:113], v[24:31], v[48:55], v[110:113], v226, v227 op_sel_hi:[0,0,0]
	v_mfma_scale_f32_16x16x128_f8f6f4 v[106:109], v[16:23], v[48:55], v[106:109], v226, v227 op_sel_hi:[0,0,0]
	v_mfma_scale_f32_16x16x128_f8f6f4 v[94:97], v[24:31], v[40:47], v[94:97], v226, v227 op_sel_hi:[0,0,0]
	v_mfma_scale_f32_16x16x128_f8f6f4 v[90:93], v[16:23], v[40:47], v[90:93], v226, v227 op_sel_hi:[0,0,0]
	v_mfma_scale_f32_16x16x128_f8f6f4 v[78:81], v[24:31], v[32:39], v[78:81], v226, v227 op_sel_hi:[0,0,0]
	v_mfma_scale_f32_16x16x128_f8f6f4 v[74:77], v[16:23], v[32:39], v[74:77], v226, v227 op_sel_hi:[0,0,0]
	v_mfma_scale_f32_16x16x128_f8f6f4 v[118:121], v[8:15], v[56:63], v[118:121], v226, v227 op_sel_hi:[0,0,0]
	v_mfma_scale_f32_16x16x128_f8f6f4 v[114:117], v[0:7], v[56:63], v[114:117], v226, v227 op_sel_hi:[0,0,0]
	v_mfma_scale_f32_16x16x128_f8f6f4 v[102:105], v[8:15], v[48:55], v[102:105], v226, v227 op_sel_hi:[0,0,0]
	v_mfma_scale_f32_16x16x128_f8f6f4 v[98:101], v[0:7], v[48:55], v[98:101], v226, v227 op_sel_hi:[0,0,0]
	v_mfma_scale_f32_16x16x128_f8f6f4 v[86:89], v[8:15], v[40:47], v[86:89], v226, v227 op_sel_hi:[0,0,0]
	v_mfma_scale_f32_16x16x128_f8f6f4 v[82:85], v[0:7], v[40:47], v[82:85], v226, v227 op_sel_hi:[0,0,0]
	v_mfma_scale_f32_16x16x128_f8f6f4 v[70:73], v[8:15], v[32:39], v[70:73], v226, v227 op_sel_hi:[0,0,0]
	v_mfma_scale_f32_16x16x128_f8f6f4 v[66:69], v[0:7], v[32:39], v[66:69], v226, v227 op_sel_hi:[0,0,0]
	s_barrier
	v_add_u32_e32 v0, 0x18000, v237
	v_add_u32_e32 v4, 0x1c000, v237
	ds_read_b128 v[24:27], v0
	ds_read_b128 v[28:31], v0 offset:1024
	ds_read_b128 v[16:19], v0 offset:2048
	ds_read_b128 v[20:23], v0 offset:3072
	ds_read_b128 v[8:11], v4
	ds_read_b128 v[12:15], v4 offset:1024
	ds_read_b128 v[0:3], v4 offset:2048
	ds_read_b128 v[4:7], v4 offset:3072
	s_mov_b32 m0, s34
	v_lshl_add_u64 v[240:241], s[18:19], 0, v[198:199]
	ds_read_b128 v[56:59], v238 offset:32768
	ds_read_b128 v[60:63], v238 offset:33792
	ds_read_b128 v[48:51], v238 offset:34816
	ds_read_b128 v[52:55], v238 offset:35840
	ds_read_b128 v[40:43], v238 offset:36864
	ds_read_b128 v[44:47], v238 offset:37888
	ds_read_b128 v[32:35], v238 offset:38912
	ds_read_b128 v[36:39], v238 offset:39936
	global_load_lds_dwordx4 v[240:241], off
	v_lshl_add_u64 v[240:241], s[18:19], 0, v[204:205]
	s_mov_b32 m0, s35
	s_and_b64 vcc, exec, s[0:1]
	global_load_lds_dwordx4 v[240:241], off
	s_cbranch_vccnz .LBB0_716
	s_waitcnt vmcnt(24)
	s_cbranch_execnz .LBB0_699
	s_branch .LBB0_717

; #define PG8_STAGE_A(bufoff, gbase, VO, h) do { _Pragma("unroll") for (int _i = 0; _i < 2; ++_i) \
;         __builtin_amdgcn_global_load_lds((const unsigned*)((const char*)(gbase) + (VO)[h][_i]), (LAS unsigned*)(lds + (bufoff) + ldsw + _i * 8192), 16, 0, 0); } while (0)
; #define PG8_BAR __builtin_amdgcn_s_barrier()
;     ...
;         if (ALIGN_EPI) { if (wr == 0) PG8_BAR; }
;         if (ALIGN_EPI && has_next) { if constexpr (GATHER) PG8_STAGE_A(PG8_SA(1, 1), nA + kstep, voffN, 1); else PG8_STAGE_A(PG8_SA(1, 1), nA + kstep, voffA, 1); }
.LBB0_718:
	s_setprio 0
	v_readlane_b32 s0, v249, 49
	v_readlane_b32 s1, v249, 50
	s_and_b64 vcc, exec, s[0:1]
	s_cbranch_vccz .LBB0_720
	s_barrier

; __device__ __forceinline__ int ltid(int wave0) { int t; asm volatile("v_mbcnt_lo_u32_b32 %0, -1, 0\n\tv_mbcnt_hi_u32_b32 %0, -1, %0" : "=v"(t)); return (wave0 << 6) | t; }
; #define PG8_STAGE_B(bufoff, gbase) do { _Pragma("unroll") for (int _i = 0; _i < 2; ++_i) \
;         __builtin_amdgcn_global_load_lds((const unsigned*)((const char*)(gbase) + voffB[_i]), (LAS unsigned*)(lds + (bufoff) + ldsw + _i * 8192), 16, 0, 0); } while (0)
; #define PG8_STAGE_A(bufoff, gbase, VO, h) do { _Pragma("unroll") for (int _i = 0; _i < 2; ++_i) \
;         __builtin_amdgcn_global_load_lds((const unsigned*)((const char*)(gbase) + (VO)[h][_i]), (LAS unsigned*)(lds + (bufoff) + ldsw + _i * 8192), 16, 0, 0); } while (0)
; #define PG8_BAR __builtin_amdgcn_s_barrier()
;     ...
;     const int tid = ltid(wave0), wid = wave0, lane = tid & 63, wr = wid >> 2, wc = wid & 3, fr = lane & 15, fq = lane >> 4;
;     const int nt = K / BK;
;     unsigned voffB[2], voffA[2][2], voffN[2][2]; int Rr[2], Cc[2];
; #pragma unroll
;     for (int i = 0; i < 2; ++i) { int R, C; stage_rc(tid * 16 + i * 8192, R, C); const int Rb = (R & ~31) + perm32(R & 31);
;         Rr[i] = R; Cc[i] = C; voffB[i] = nB64 ? (unsigned)(Rb * 64 + ((C * 2) & 63) + ((C * 2) >> 6) * nB64 * 64) : (unsigned)(Rb * ldb + C) * 2u;
;         voffA[0][i] = (unsigned)(R * lda + C) * 2u; voffA[1][i] = (unsigned)((R + HALF) * lda + C) * 2u; voffN[0][i] = voffA[0][i]; voffN[1][i] = voffA[1][i]; }
;     ...
;     const char* cA = cur.A; const char* cB = cur.B;
;     PG8_STAGE_B(PG8_SB(0, 0), cB); PG8_STAGE_B(PG8_SB(0, 1), cB + hstepB); PG8_STAGE_A(PG8_SA(0, 0), cA, voffA, 0); PG8_STAGE_A(PG8_SA(0, 1), cA, voffA, 1);
;     if (wr == 1) PG8_BAR;
.LBB0_781:
	s_and_b64 vcc, exec, s[38:39]
	s_cbranch_vccnz .LBB0_815
	v_readlane_b32 s0, v249, 40
	s_mov_b32 s1, 0x3ffffe0
	v_mov_b32_e32 v15, 0x40000
	v_lshl_or_b32 v4, v8, 4, s0
	v_ashrrev_i32_e32 v0, 31, v4
	v_lshrrev_b32_e32 v0, 22, v0
	v_add_u32_e32 v0, v4, v0
	v_ashrrev_i32_e32 v0, 10, v0
	v_mul_i32_i24_e32 v1, 0x400, v0
	v_sub_u32_e32 v1, v4, v1
	v_lshrrev_b32_e32 v2, 4, v1
	v_bitop3_b32 v3, v2, v1, 32 bitop3:0x6c
	v_lshlrev_b32_e32 v1, 3, v0
	v_and_b32_e32 v2, -16, v1
	v_ashrrev_i32_e32 v1, 31, v3
	v_lshrrev_b32_e32 v1, 26, v1
	v_add_u32_e32 v5, v3, v1
	v_ashrrev_i32_e32 v1, 6, v5
	v_and_b32_e32 v5, 0xc0, v5
	v_add_u32_e32 v6, v1, v2
	v_lshlrev_b32_e32 v2, 5, v0
	v_sub_u32_e32 v3, v3, v5
	v_and_b32_e32 v2, 32, v2
	v_ashrrev_i16_sdwa v3, v222, sext(v3) dst_sel:DWORD dst_unused:UNUSED_PAD src0_sel:DWORD src1_sel:BYTE_0
	v_lshlrev_b32_e32 v7, 1, v6
	s_waitcnt lgkmcnt(0)
	v_lshrrev_b32_e32 v9, 2, v6
	v_and_b32_e32 v10, 3, v1
	v_add_u32_sdwa v5, v2, sext(v3) dst_sel:DWORD dst_unused:UNUSED_PAD src0_sel:DWORD src1_sel:WORD_0
	v_and_b32_e32 v7, 24, v7
	v_and_b32_e32 v9, 4, v9
	v_and_or_b32 v10, v6, s1, v10
	v_or3_b32 v7, v10, v9, v7
	v_lshlrev_b32_e32 v9, 1, v5
	v_lshlrev_b32_e32 v11, 12, v5
	v_lshl_add_u32 v5, v6, 10, v5
	v_lshl_add_u32 v198, v5, 1, v15
	v_add_u32_e32 v5, 0x2000, v4
	v_ashrrev_i32_e32 v4, 31, v5
	v_lshrrev_b32_e32 v4, 22, v4
	v_add_u32_e32 v4, v5, v4
	v_ashrrev_i32_e32 v4, 10, v4
	v_lshl_add_u32 v196, v6, 11, v9
	v_mul_i32_i24_e32 v6, 0x400, v4
	v_and_b32_e32 v10, 62, v9
	s_mov_b32 s6, 0xfffe0000
	v_sub_u32_e32 v5, v5, v6
	v_and_or_b32 v10, v11, s6, v10
	v_lshrrev_b32_e32 v6, 4, v5
	v_lshl_add_u32 v194, v7, 6, v10
	v_bitop3_b32 v7, v6, v5, 32 bitop3:0x6c
	v_lshlrev_b32_e32 v5, 3, v4
	v_and_b32_e32 v6, -16, v5
	v_ashrrev_i32_e32 v5, 31, v7
	v_lshrrev_b32_e32 v5, 26, v5
	v_add_u32_e32 v9, v7, v5
	v_ashrrev_i32_e32 v5, 6, v9
	v_and_b32_e32 v9, 0xffc0, v9
	v_sub_u32_e32 v7, v7, v9
	v_lshrrev_b16_e32 v9, 7, v7
	v_and_b32_e32 v9, 1, v9
	v_add_u32_e32 v10, v5, v6
	v_lshlrev_b32_e32 v6, 5, v4
	v_add_u16_e32 v7, v7, v9
	v_and_b32_e32 v6, 32, v6
	v_ashrrev_i16_sdwa v7, v222, sext(v7) dst_sel:DWORD dst_unused:UNUSED_PAD src0_sel:DWORD src1_sel:BYTE_0
	v_lshlrev_b32_e32 v11, 1, v10
	v_lshrrev_b32_e32 v12, 2, v10
	v_and_b32_e32 v13, 3, v5
	v_add_u32_sdwa v9, v6, sext(v7) dst_sel:DWORD dst_unused:UNUSED_PAD src0_sel:DWORD src1_sel:WORD_0
	v_and_b32_e32 v11, 24, v11
	v_and_b32_e32 v12, 4, v12
	v_and_or_b32 v13, v10, s1, v13
	v_or3_b32 v11, v13, v12, v11
	v_lshlrev_b32_e32 v12, 1, v9
	s_add_i32 s24, s0, 0
	v_and_b32_e32 v13, 62, v12
	v_lshlrev_b32_e32 v14, 12, v9
	s_add_i32 s25, s24, 0x10000
	s_add_i32 s26, s24, 0x12000
	v_and_or_b32 v13, v14, s6, v13
	s_mov_b32 m0, s25
	s_add_u32 s0, s2, 0x2000
	v_lshl_add_u32 v200, v11, 6, v13
	global_load_lds_dwordx4 v194, s[2:3]
	s_mov_b32 m0, s26
	s_addc_u32 s1, s3, 0
	s_add_i32 s27, s24, 0x14000
	global_load_lds_dwordx4 v200, s[2:3]
	s_mov_b32 m0, s27
	s_add_i32 s28, s24, 0x16000
	global_load_lds_dwordx4 v194, s[0:1]
	s_mov_b32 m0, s28
	s_add_i32 s29, s24, 0x2000
	global_load_lds_dwordx4 v200, s[0:1]
	s_mov_b32 m0, s24
	v_lshl_add_u32 v202, v10, 11, v12
	global_load_lds_dwordx4 v196, s[4:5]
	s_mov_b32 m0, s29
	s_add_i32 s31, s24, 0x4000
	v_lshl_add_u32 v9, v10, 10, v9
	global_load_lds_dwordx4 v202, s[4:5]
	s_mov_b32 m0, s31
	s_add_i32 s34, s24, 0x6000
	v_lshl_add_u32 v204, v9, 1, v15
	global_load_lds_dwordx4 v198, s[4:5]
	s_mov_b32 m0, s34
	v_readlane_b32 s6, v249, 47
	global_load_lds_dwordx4 v204, s[4:5]
	v_readlane_b32 s7, v249, 48
	s_andn2_b64 vcc, exec, s[6:7]
	s_nop 0
	v_cndmask_b32_e64 v9, 0, 1, s[6:7]
	v_cmp_ne_u32_e64 s[0:1], 1, v9
	s_cbranch_vccnz .LBB0_784
	s_barrier
	s_setprio 1

; #define PG8_STAGE_B(bufoff, gbase) do { _Pragma("unroll") for (int _i = 0; _i < 2; ++_i) \
;         __builtin_amdgcn_global_load_lds((const unsigned*)((const char*)(gbase) + voffB[_i]), (LAS unsigned*)(lds + (bufoff) + ldsw + _i * 8192), 16, 0, 0); } while (0)
; #define PG8_STAGE_A(bufoff, gbase, VO, h) do { _Pragma("unroll") for (int _i = 0; _i < 2; ++_i) \
;         __builtin_amdgcn_global_load_lds((const unsigned*)((const char*)(gbase) + (VO)[h][_i]), (LAS unsigned*)(lds + (bufoff) + ldsw + _i * 8192), 16, 0, 0); } while (0)
; #define PG8_WAIT_V(n) asm volatile("s_waitcnt vmcnt(" #n ")" ::: "memory")
; #define PG8_WAIT_L(n) asm volatile("s_waitcnt lgkmcnt(" #n ")" ::: "memory")
; #define PG8_WAIT_VX(rx) do { if (rx) asm volatile("s_waitcnt vmcnt(%0)" :: "n"(8 + Epi::NVM) : "memory"); else asm volatile("s_waitcnt vmcnt(8)" ::: "memory"); } while (0)
; #define PG8_BAR __builtin_amdgcn_s_barrier()
; #define PG8_SCHED __builtin_amdgcn_sched_barrier(0)
;     ...
;             PG8_WAIT_VX(rx); PG8_WAIT_L(0); PG8_BAR; PG8_MMA(0, 0, At, B0); PG8_MMA(0, 1, At, B1); PG8_BAR; PG8_SCHED;
;             PG8_LDA(At, 1, 1); PG8_STAGE_B(PG8_SB(1, 0), b3); PG8_STAGE_B(PG8_SB(1, 1), b3 + hstepB); PG8_STAGE_A(PG8_SA(1, 0), a3, vo2, 0);
;             PG8_WAIT_V(8); PG8_WAIT_L(0); PG8_BAR; PG8_MMA(1, 0, At, B0); PG8_MMA(1, 1, At, B1); PG8_BAR; PG8_SCHED;
.LBB0_794:
	s_waitcnt lgkmcnt(0)
	s_add_u32 s2, s16, 0x40000
	s_addc_u32 s3, s17, 0
	s_barrier
	s_waitcnt lgkmcnt(0)
	v_mfma_scale_f32_16x16x128_f8f6f4 v[190:193], v[24:31], v[56:63], v[190:193], v226, v227 op_sel_hi:[0,0,0]
	v_mfma_scale_f32_16x16x128_f8f6f4 v[186:189], v[16:23], v[56:63], v[186:189], v226, v227 op_sel_hi:[0,0,0]
	v_mfma_scale_f32_16x16x128_f8f6f4 v[182:185], v[24:31], v[48:55], v[182:185], v226, v227 op_sel_hi:[0,0,0]
	v_mfma_scale_f32_16x16x128_f8f6f4 v[174:177], v[16:23], v[48:55], v[174:177], v226, v227 op_sel_hi:[0,0,0]
	v_mfma_scale_f32_16x16x128_f8f6f4 v[166:169], v[24:31], v[40:47], v[166:169], v226, v227 op_sel_hi:[0,0,0]
	v_mfma_scale_f32_16x16x128_f8f6f4 v[158:161], v[16:23], v[40:47], v[158:161], v226, v227 op_sel_hi:[0,0,0]
	v_mfma_scale_f32_16x16x128_f8f6f4 v[150:153], v[24:31], v[32:39], v[150:153], v226, v227 op_sel_hi:[0,0,0]
	v_mfma_scale_f32_16x16x128_f8f6f4 v[142:145], v[16:23], v[32:39], v[142:145], v226, v227 op_sel_hi:[0,0,0]
	v_mfma_scale_f32_16x16x128_f8f6f4 v[178:181], v[8:15], v[56:63], v[178:181], v226, v227 op_sel_hi:[0,0,0]
	v_mfma_scale_f32_16x16x128_f8f6f4 v[170:173], v[0:7], v[56:63], v[170:173], v226, v227 op_sel_hi:[0,0,0]
	v_mfma_scale_f32_16x16x128_f8f6f4 v[162:165], v[8:15], v[48:55], v[162:165], v226, v227 op_sel_hi:[0,0,0]
	v_mfma_scale_f32_16x16x128_f8f6f4 v[154:157], v[0:7], v[48:55], v[154:157], v226, v227 op_sel_hi:[0,0,0]
	v_mfma_scale_f32_16x16x128_f8f6f4 v[146:149], v[8:15], v[40:47], v[146:149], v226, v227 op_sel_hi:[0,0,0]
	v_mfma_scale_f32_16x16x128_f8f6f4 v[138:141], v[0:7], v[40:47], v[138:141], v226, v227 op_sel_hi:[0,0,0]
	v_mfma_scale_f32_16x16x128_f8f6f4 v[134:137], v[8:15], v[32:39], v[134:137], v226, v227 op_sel_hi:[0,0,0]
	v_mfma_scale_f32_16x16x128_f8f6f4 v[130:133], v[0:7], v[32:39], v[130:133], v226, v227 op_sel_hi:[0,0,0]
	s_barrier
	s_mov_b32 m0, s35
	v_lshl_add_u64 v[238:239], s[2:3], 0, v[194:195]
	ds_read_b128 v[32:35], v220 offset:49152
	ds_read_b128 v[36:39], v220 offset:50176
	ds_read_b128 v[40:43], v220 offset:51200
	ds_read_b128 v[44:47], v220 offset:52224
	ds_read_b128 v[48:51], v220 offset:53248
	ds_read_b128 v[52:55], v220 offset:54272
	ds_read_b128 v[56:59], v220 offset:55296
	ds_read_b128 v[60:63], v220 offset:56320
	global_load_lds_dwordx4 v[238:239], off
	v_lshl_add_u64 v[238:239], s[2:3], 0, v[200:201]
	s_add_u32 s2, s16, 0x42000
	s_mov_b32 m0, s36
	s_addc_u32 s3, s17, 0
	global_load_lds_dwordx4 v[238:239], off
	v_lshl_add_u64 v[238:239], s[2:3], 0, v[194:195]
	s_mov_b32 m0, s41
	v_lshl_add_u64 v[214:215], v[214:215], 0, s[94:95]
	global_load_lds_dwordx4 v[238:239], off
	v_lshl_add_u64 v[238:239], s[2:3], 0, v[200:201]
	s_mov_b32 m0, s42
	s_nop 0
	global_load_lds_dwordx4 v[238:239], off
	s_mov_b32 m0, s37
	s_nop 0
	global_load_lds_dwordx4 v[214:215], off
	v_lshl_add_u64 v[214:215], v[216:217], 0, s[94:95]
	s_mov_b32 m0, s40
	s_nop 0
	global_load_lds_dwordx4 v[214:215], off
	s_waitcnt vmcnt(8)
	s_waitcnt lgkmcnt(0)
	s_barrier
	s_waitcnt lgkmcnt(0)
	v_mfma_scale_f32_16x16x128_f8f6f4 v[126:129], v[24:31], v[32:39], v[126:129], v226, v227 op_sel_hi:[0,0,0]
	v_mfma_scale_f32_16x16x128_f8f6f4 v[122:125], v[16:23], v[32:39], v[122:125], v226, v227 op_sel_hi:[0,0,0]
	v_mfma_scale_f32_16x16x128_f8f6f4 v[110:113], v[24:31], v[40:47], v[110:113], v226, v227 op_sel_hi:[0,0,0]
	v_mfma_scale_f32_16x16x128_f8f6f4 v[102:105], v[16:23], v[40:47], v[102:105], v226, v227 op_sel_hi:[0,0,0]
	v_mfma_scale_f32_16x16x128_f8f6f4 v[86:89], v[24:31], v[48:55], v[86:89], v226, v227 op_sel_hi:[0,0,0]
	v_mfma_scale_f32_16x16x128_f8f6f4 v[78:81], v[16:23], v[48:55], v[78:81], v226, v227 op_sel_hi:[0,0,0]
	v_mfma_scale_f32_16x16x128_f8f6f4 v[70:73], v[24:31], v[56:63], v[70:73], v226, v227 op_sel_hi:[0,0,0]
	v_mfma_scale_f32_16x16x128_f8f6f4 v[66:69], v[16:23], v[56:63], v[66:69], v226, v227 op_sel_hi:[0,0,0]
	v_mfma_scale_f32_16x16x128_f8f6f4 v[106:109], v[8:15], v[32:39], v[106:109], v226, v227 op_sel_hi:[0,0,0]
	v_mfma_scale_f32_16x16x128_f8f6f4 v[98:101], v[0:7], v[32:39], v[98:101], v226, v227 op_sel_hi:[0,0,0]
	v_mfma_scale_f32_16x16x128_f8f6f4 v[82:85], v[8:15], v[40:47], v[82:85], v226, v227 op_sel_hi:[0,0,0]
	v_mfma_scale_f32_16x16x128_f8f6f4 v[74:77], v[0:7], v[40:47], v[74:77], v226, v227 op_sel_hi:[0,0,0]
	v_mfma_scale_f32_16x16x128_f8f6f4 v[118:121], v[8:15], v[48:55], v[118:121], v226, v227 op_sel_hi:[0,0,0]
	v_mfma_scale_f32_16x16x128_f8f6f4 v[114:117], v[0:7], v[48:55], v[114:117], v226, v227 op_sel_hi:[0,0,0]
	v_mfma_scale_f32_16x16x128_f8f6f4 v[94:97], v[8:15], v[56:63], v[94:97], v226, v227 op_sel_hi:[0,0,0]
	v_mfma_scale_f32_16x16x128_f8f6f4 v[90:93], v[0:7], v[56:63], v[90:93], v226, v227 op_sel_hi:[0,0,0]
	s_barrier
	s_add_i32 s50, s50, 2
	s_add_u32 s48, s48, 0x80000
	s_addc_u32 s49, s49, 0
	s_add_u32 s14, s14, 0x100
	s_addc_u32 s15, s15, 0
	s_cmp_gt_u32 s50, 13
	s_cbranch_scc1 .LBB0_807

; #define PG8_STAGE_B(bufoff, gbase) do { _Pragma("unroll") for (int _i = 0; _i < 2; ++_i) \
;         __builtin_amdgcn_global_load_lds((const unsigned*)((const char*)(gbase) + voffB[_i]), (LAS unsigned*)(lds + (bufoff) + ldsw + _i * 8192), 16, 0, 0); } while (0)
; #define PG8_STAGE_A(bufoff, gbase, VO, h) do { _Pragma("unroll") for (int _i = 0; _i < 2; ++_i) \
;         __builtin_amdgcn_global_load_lds((const unsigned*)((const char*)(gbase) + (VO)[h][_i]), (LAS unsigned*)(lds + (bufoff) + ldsw + _i * 8192), 16, 0, 0); } while (0)
; #define PG8_WAIT_L(n) asm volatile("s_waitcnt lgkmcnt(" #n ")" ::: "memory")
; #define PG8_WAIT_VX(rx) do { if (rx) asm volatile("s_waitcnt vmcnt(%0)" :: "n"(8 + Epi::NVM) : "memory"); else asm volatile("s_waitcnt vmcnt(8)" ::: "memory"); } while (0)
; #define PG8_BAR __builtin_amdgcn_s_barrier()
; #define PG8_SCHED __builtin_amdgcn_sched_barrier(0)
;     ...
;             const bool last = (t == nt - 2); int rxi = (relax && t == 0) ? 1 : 0; asm volatile("" : "+v"(rxi)); const bool rx = __builtin_amdgcn_readfirstlane(rxi) != 0;
;             if constexpr (Epi::HAS_MID) { constexpr int SEGT = (F8 != 0) ? 8 : 16; if (t == SEGT || t == 2 * SEGT) { PG8_SCHED; E.mid(acc, cur, t / SEGT, wr, wc, fr, fq); PG8_SCHED; } }
;             const char* a1 = cA + (size_t)(t + 1) * kstep;
;             const char* a2 = last ? nA : cA + (size_t)(t + 2) * kstep; const char* b2 = last ? nB : cB + (size_t)(t + 2) * kstepB;
;             const char* a3 = a2 + kstep; const char* b3 = b2 + kstepB;
;             unsigned vo2[2][2];
; #pragma unroll
;             for (int h = 0; h < 2; ++h)
; #pragma unroll
;                 for (int i = 0; i < 2; ++i) vo2[h][i] = (GATHER && last) ? voffN[h][i] : voffA[h][i];
;             PG8_LDB(B0, 0, 0); PG8_LDB(B1, 0, 1); PG8_SCHED; PG8_LDA(At, 0, 0); if (!rx) PG8_STAGE_A(PG8_SA(1, 1), a1, voffA, 1);
;             PG8_WAIT_VX(rx); PG8_WAIT_L(0); PG8_BAR; PG8_MMA(0, 0, At, B0); PG8_MMA(0, 1, At, B1); PG8_BAR; PG8_SCHED;
;             PG8_LDA(At, 0, 1); PG8_STAGE_B(PG8_SB(0, 0), b2); PG8_STAGE_B(PG8_SB(0, 1), b2 + hstepB); PG8_STAGE_A(PG8_SA(0, 0), a2, vo2, 0);
.LBB0_798:
	s_add_u32 s2, s4, s14
	s_addc_u32 s3, s5, s15
	s_add_u32 s2, s2, 0x100
	s_addc_u32 s3, s3, 0
	s_waitcnt lgkmcnt(0)
	s_cmpk_eq_i32 s14, 0x700
	s_cselect_b32 s19, s7, s3
	s_cselect_b32 s18, s6, s2
	s_cselect_b32 s17, s9, s49
	s_cselect_b32 s16, s8, s48
	s_barrier
	s_waitcnt lgkmcnt(0)
	v_mfma_scale_f32_16x16x128_f8f6f4 v[190:193], v[24:31], v[56:63], v[190:193], v226, v227 op_sel_hi:[0,0,0]
	v_mfma_scale_f32_16x16x128_f8f6f4 v[186:189], v[16:23], v[56:63], v[186:189], v226, v227 op_sel_hi:[0,0,0]
	v_mfma_scale_f32_16x16x128_f8f6f4 v[182:185], v[24:31], v[48:55], v[182:185], v226, v227 op_sel_hi:[0,0,0]
	v_mfma_scale_f32_16x16x128_f8f6f4 v[174:177], v[16:23], v[48:55], v[174:177], v226, v227 op_sel_hi:[0,0,0]
	v_mfma_scale_f32_16x16x128_f8f6f4 v[166:169], v[24:31], v[40:47], v[166:169], v226, v227 op_sel_hi:[0,0,0]
	v_mfma_scale_f32_16x16x128_f8f6f4 v[158:161], v[16:23], v[40:47], v[158:161], v226, v227 op_sel_hi:[0,0,0]
	v_mfma_scale_f32_16x16x128_f8f6f4 v[150:153], v[24:31], v[32:39], v[150:153], v226, v227 op_sel_hi:[0,0,0]
	v_mfma_scale_f32_16x16x128_f8f6f4 v[142:145], v[16:23], v[32:39], v[142:145], v226, v227 op_sel_hi:[0,0,0]
	v_mfma_scale_f32_16x16x128_f8f6f4 v[178:181], v[8:15], v[56:63], v[178:181], v226, v227 op_sel_hi:[0,0,0]
	v_mfma_scale_f32_16x16x128_f8f6f4 v[170:173], v[0:7], v[56:63], v[170:173], v226, v227 op_sel_hi:[0,0,0]
	v_mfma_scale_f32_16x16x128_f8f6f4 v[162:165], v[8:15], v[48:55], v[162:165], v226, v227 op_sel_hi:[0,0,0]
	v_mfma_scale_f32_16x16x128_f8f6f4 v[154:157], v[0:7], v[48:55], v[154:157], v226, v227 op_sel_hi:[0,0,0]
	v_mfma_scale_f32_16x16x128_f8f6f4 v[146:149], v[8:15], v[40:47], v[146:149], v226, v227 op_sel_hi:[0,0,0]
	v_mfma_scale_f32_16x16x128_f8f6f4 v[138:141], v[0:7], v[40:47], v[138:141], v226, v227 op_sel_hi:[0,0,0]
	v_mfma_scale_f32_16x16x128_f8f6f4 v[134:137], v[8:15], v[32:39], v[134:137], v226, v227 op_sel_hi:[0,0,0]
	v_mfma_scale_f32_16x16x128_f8f6f4 v[130:133], v[0:7], v[32:39], v[130:133], v226, v227 op_sel_hi:[0,0,0]
	s_barrier
	s_mov_b32 m0, s25
	v_lshl_add_u64 v[214:215], s[16:17], 0, v[194:195]
	s_add_u32 s2, s16, 0x2000
	ds_read_b128 v[56:59], v220 offset:16384
	ds_read_b128 v[60:63], v220 offset:17408
	ds_read_b128 v[48:51], v220 offset:18432
	ds_read_b128 v[52:55], v220 offset:19456
	ds_read_b128 v[40:43], v220 offset:20480
	ds_read_b128 v[44:47], v220 offset:21504
	ds_read_b128 v[32:35], v220 offset:22528
	ds_read_b128 v[36:39], v220 offset:23552
	global_load_lds_dwordx4 v[214:215], off
	v_lshl_add_u64 v[214:215], s[16:17], 0, v[200:201]
	s_mov_b32 m0, s26
	s_addc_u32 s3, s17, 0
	global_load_lds_dwordx4 v[214:215], off
	v_lshl_add_u64 v[214:215], s[2:3], 0, v[194:195]
	s_mov_b32 m0, s27
	v_lshl_add_u64 v[216:217], s[18:19], 0, v[202:203]
	global_load_lds_dwordx4 v[214:215], off
	v_lshl_add_u64 v[214:215], s[2:3], 0, v[200:201]
	s_mov_b32 m0, s28
	v_cndmask_b32_e64 v221, 0, 1, s[20:21]
	global_load_lds_dwordx4 v[214:215], off
	v_lshl_add_u64 v[214:215], s[18:19], 0, v[196:197]
	s_mov_b32 m0, s24
	v_cmp_ne_u32_e64 s[2:3], 1, v221
	global_load_lds_dwordx4 v[214:215], off
	s_mov_b32 m0, s29
	s_andn2_b64 vcc, exec, s[20:21]
	global_load_lds_dwordx4 v[216:217], off
	s_cbranch_vccnz .LBB0_804
	s_waitcnt vmcnt(24)
	s_cbranch_execnz .LBB0_801

; #define PG8_STAGE_A(bufoff, gbase, VO, h) do { _Pragma("unroll") for (int _i = 0; _i < 2; ++_i) \
;         __builtin_amdgcn_global_load_lds((const unsigned*)((const char*)(gbase) + (VO)[h][_i]), (LAS unsigned*)(lds + (bufoff) + ldsw + _i * 8192), 16, 0, 0); } while (0)
; #define PG8_WAIT_L(n) asm volatile("s_waitcnt lgkmcnt(" #n ")" ::: "memory")
; #define PG8_WAIT_VX(rx) do { if (rx) asm volatile("s_waitcnt vmcnt(%0)" :: "n"(8 + Epi::NVM) : "memory"); else asm volatile("s_waitcnt vmcnt(8)" ::: "memory"); } while (0)
; #define PG8_BAR __builtin_amdgcn_s_barrier()
; #define PG8_SCHED __builtin_amdgcn_sched_barrier(0)
;     ...
;             PG8_WAIT_VX(rx); PG8_WAIT_L(0); PG8_BAR; PG8_MMA(1, 0, At, B0); PG8_MMA(1, 1, At, B1); PG8_BAR; PG8_SCHED;
;             PG8_LDB(B0, 1, 0); PG8_LDB(B1, 1, 1); PG8_SCHED; PG8_LDA(At, 1, 0); PG8_STAGE_A(PG8_SA(0, 1), a2, vo2, 1);
.LBB0_801:
	s_waitcnt lgkmcnt(0)
	s_barrier
	s_waitcnt lgkmcnt(0)
	v_mfma_scale_f32_16x16x128_f8f6f4 v[126:129], v[24:31], v[56:63], v[126:129], v226, v227 op_sel_hi:[0,0,0]
	v_mfma_scale_f32_16x16x128_f8f6f4 v[122:125], v[16:23], v[56:63], v[122:125], v226, v227 op_sel_hi:[0,0,0]
	v_mfma_scale_f32_16x16x128_f8f6f4 v[110:113], v[24:31], v[48:55], v[110:113], v226, v227 op_sel_hi:[0,0,0]
	v_mfma_scale_f32_16x16x128_f8f6f4 v[102:105], v[16:23], v[48:55], v[102:105], v226, v227 op_sel_hi:[0,0,0]
	v_mfma_scale_f32_16x16x128_f8f6f4 v[86:89], v[24:31], v[40:47], v[86:89], v226, v227 op_sel_hi:[0,0,0]
	v_mfma_scale_f32_16x16x128_f8f6f4 v[78:81], v[16:23], v[40:47], v[78:81], v226, v227 op_sel_hi:[0,0,0]
	v_mfma_scale_f32_16x16x128_f8f6f4 v[70:73], v[24:31], v[32:39], v[70:73], v226, v227 op_sel_hi:[0,0,0]
	v_mfma_scale_f32_16x16x128_f8f6f4 v[66:69], v[16:23], v[32:39], v[66:69], v226, v227 op_sel_hi:[0,0,0]
	v_mfma_scale_f32_16x16x128_f8f6f4 v[106:109], v[8:15], v[56:63], v[106:109], v226, v227 op_sel_hi:[0,0,0]
	v_mfma_scale_f32_16x16x128_f8f6f4 v[98:101], v[0:7], v[56:63], v[98:101], v226, v227 op_sel_hi:[0,0,0]
	v_mfma_scale_f32_16x16x128_f8f6f4 v[82:85], v[8:15], v[48:55], v[82:85], v226, v227 op_sel_hi:[0,0,0]
	v_mfma_scale_f32_16x16x128_f8f6f4 v[74:77], v[0:7], v[48:55], v[74:77], v226, v227 op_sel_hi:[0,0,0]
	v_mfma_scale_f32_16x16x128_f8f6f4 v[118:121], v[8:15], v[40:47], v[118:121], v226, v227 op_sel_hi:[0,0,0]
	v_mfma_scale_f32_16x16x128_f8f6f4 v[114:117], v[0:7], v[40:47], v[114:117], v226, v227 op_sel_hi:[0,0,0]
	v_mfma_scale_f32_16x16x128_f8f6f4 v[94:97], v[8:15], v[32:39], v[94:97], v226, v227 op_sel_hi:[0,0,0]
	v_mfma_scale_f32_16x16x128_f8f6f4 v[90:93], v[0:7], v[32:39], v[90:93], v226, v227 op_sel_hi:[0,0,0]
	s_barrier
	v_add_u32_e32 v0, 0x18000, v219
	v_add_u32_e32 v4, 0x1c000, v219
	ds_read_b128 v[24:27], v0
	ds_read_b128 v[28:31], v0 offset:1024
	ds_read_b128 v[16:19], v0 offset:2048
	ds_read_b128 v[20:23], v0 offset:3072
	ds_read_b128 v[8:11], v4
	ds_read_b128 v[12:15], v4 offset:1024
	ds_read_b128 v[0:3], v4 offset:2048
	ds_read_b128 v[4:7], v4 offset:3072
	s_mov_b32 m0, s31
	v_lshl_add_u64 v[238:239], s[18:19], 0, v[198:199]
	ds_read_b128 v[56:59], v220 offset:32768
	ds_read_b128 v[60:63], v220 offset:33792
	ds_read_b128 v[48:51], v220 offset:34816
	ds_read_b128 v[52:55], v220 offset:35840
	ds_read_b128 v[40:43], v220 offset:36864
	ds_read_b128 v[44:47], v220 offset:37888
	ds_read_b128 v[32:35], v220 offset:38912
	ds_read_b128 v[36:39], v220 offset:39936
	global_load_lds_dwordx4 v[238:239], off
	v_lshl_add_u64 v[238:239], s[18:19], 0, v[204:205]
	s_mov_b32 m0, s34
	s_and_b64 vcc, exec, s[2:3]
	global_load_lds_dwordx4 v[238:239], off
	s_cbranch_vccnz .LBB0_805
	s_waitcnt vmcnt(24)
	s_cbranch_execnz .LBB0_794
	s_branch .LBB0_806

; __device__ __forceinline__ int ltid(int wave0) { int t; asm volatile("v_mbcnt_lo_u32_b32 %0, -1, 0\n\tv_mbcnt_hi_u32_b32 %0, -1, %0" : "=v"(t)); return (wave0 << 6) | t; }
; #define PG8_STAGE_B(bufoff, gbase) do { _Pragma("unroll") for (int _i = 0; _i < 2; ++_i) \
;         __builtin_amdgcn_global_load_lds((const unsigned*)((const char*)(gbase) + voffB[_i]), (LAS unsigned*)(lds + (bufoff) + ldsw + _i * 8192), 16, 0, 0); } while (0)
; #define PG8_STAGE_A(bufoff, gbase, VO, h) do { _Pragma("unroll") for (int _i = 0; _i < 2; ++_i) \
;         __builtin_amdgcn_global_load_lds((const unsigned*)((const char*)(gbase) + (VO)[h][_i]), (LAS unsigned*)(lds + (bufoff) + ldsw + _i * 8192), 16, 0, 0); } while (0)
; #define PG8_BAR __builtin_amdgcn_s_barrier()
;     ...
;     const int tid = ltid(wave0), wid = wave0, lane = tid & 63, wr = wid >> 2, wc = wid & 3, fr = lane & 15, fq = lane >> 4;
;     const int nt = K / BK;
;     unsigned voffB[2], voffA[2][2], voffN[2][2]; int Rr[2], Cc[2];
; #pragma unroll
;     for (int i = 0; i < 2; ++i) { int R, C; stage_rc(tid * 16 + i * 8192, R, C); const int Rb = (R & ~31) + perm32(R & 31);
;         Rr[i] = R; Cc[i] = C; voffB[i] = nB64 ? (unsigned)(Rb * 64 + ((C * 2) & 63) + ((C * 2) >> 6) * nB64 * 64) : (unsigned)(Rb * ldb + C) * 2u;
;         voffA[0][i] = (unsigned)(R * lda + C) * 2u; voffA[1][i] = (unsigned)((R + HALF) * lda + C) * 2u; voffN[0][i] = voffA[0][i]; voffN[1][i] = voffA[1][i]; }
;     ...
;     if constexpr (GATHER) {
; #pragma unroll
;         for (int h = 0; h < 2; ++h)
; #pragma unroll
;             for (int i = 0; i < 2; ++i) voffA[h][i] = (unsigned)(S.row(cur, Rr[i] + h * HALF) * lda + Cc[i]) * 2u;
;     }
;     f32x4 acc[2][2][4][2];
; #pragma unroll
;     for (int a = 0; a < 2; ++a)
; #pragma unroll
;         for (int b = 0; b < 2; ++b)
; #pragma unroll
;             for (int m = 0; m < 4; ++m)
; #pragma unroll
;                 for (int n = 0; n < 2; ++n) acc[a][b][m][n] = (f32x4){0.f, 0.f, 0.f, 0.f};
;     bf16x8 At[4][2], B0[2][2], B1[2][2]; i32x8 At_8[4], B0_8[2], B1_8[2];
;     constexpr int SCW = 0x79797979, SCX = (F8 == 4) ? (int)0x80808080 : (F8 == 2) ? 0x7d7d7d7d : 0x7f7f7f7f;
;     const char* cA = cur.A; const char* cB = cur.B;
;     PG8_STAGE_B(PG8_SB(0, 0), cB); PG8_STAGE_B(PG8_SB(0, 1), cB + hstepB); PG8_STAGE_A(PG8_SA(0, 0), cA, voffA, 0); PG8_STAGE_A(PG8_SA(0, 1), cA, voffA, 1);
;     if (wr == 1) PG8_BAR;
.LBB0_1287:
	s_andn2_b64 vcc, exec, s[0:1]
	s_cbranch_vccnz .LBB0_1326
	v_readlane_b32 s0, v249, 40
	s_mov_b32 s1, 0x3ffffe0
	s_mov_b32 s2, 0xffff0000
	v_lshl_or_b32 v1, v0, 4, s0
	v_ashrrev_i32_e32 v2, 31, v1
	v_lshrrev_b32_e32 v2, 22, v2
	v_add_u32_e32 v2, v1, v2
	v_ashrrev_i32_e32 v2, 10, v2
	v_mul_i32_i24_e32 v3, 0x400, v2
	v_sub_u32_e32 v3, v1, v3
	v_lshrrev_b32_e32 v4, 4, v3
	v_bitop3_b32 v3, v4, v3, 32 bitop3:0x6c
	v_ashrrev_i32_e32 v5, 31, v3
	v_lshrrev_b32_e32 v5, 26, v5
	v_lshlrev_b32_e32 v4, 3, v2
	v_add_u32_e32 v5, v3, v5
	v_and_b32_e32 v4, -16, v4
	v_ashrrev_i32_e32 v6, 6, v5
	v_add_u32_e32 v218, v6, v4
	v_and_b32_e32 v4, 0xc0, v5
	v_lshlrev_b32_e32 v2, 5, v2
	v_sub_u32_e32 v3, v3, v4
	v_and_b32_e32 v2, 32, v2
	v_ashrrev_i16_sdwa v3, v222, sext(v3) dst_sel:DWORD dst_unused:UNUSED_PAD src0_sel:DWORD src1_sel:BYTE_0
	v_add_u32_sdwa v2, v2, sext(v3) dst_sel:DWORD dst_unused:UNUSED_PAD src0_sel:DWORD src1_sel:WORD_0
	v_lshlrev_b32_e32 v3, 1, v218
	v_lshrrev_b32_e32 v4, 2, v218
	v_and_b32_e32 v5, 3, v6
	v_and_b32_e32 v3, 24, v3
	v_and_b32_e32 v4, 4, v4
	v_and_or_b32 v5, v218, s1, v5
	v_lshlrev_b32_e32 v219, 1, v2
	v_or3_b32 v3, v5, v4, v3
	v_and_b32_e32 v4, 62, v219
	v_lshlrev_b32_e32 v2, 11, v2
	v_and_or_b32 v2, v2, s2, v4
	v_add_u32_e32 v1, 0x2000, v1
	v_lshl_add_u32 v194, v3, 6, v2
	v_ashrrev_i32_e32 v2, 31, v1
	v_lshrrev_b32_e32 v2, 22, v2
	v_add_u32_e32 v2, v1, v2
	v_ashrrev_i32_e32 v2, 10, v2
	v_mul_i32_i24_e32 v3, 0x400, v2
	v_sub_u32_e32 v1, v1, v3
	v_lshrrev_b32_e32 v3, 4, v1
	v_bitop3_b32 v1, v3, v1, 32 bitop3:0x6c
	v_ashrrev_i32_e32 v4, 31, v1
	v_lshrrev_b32_e32 v4, 26, v4
	v_lshlrev_b32_e32 v3, 3, v2
	v_add_u32_e32 v4, v1, v4
	v_and_b32_e32 v3, -16, v3
	v_ashrrev_i32_e32 v5, 6, v4
	v_add_u32_e32 v220, v5, v3
	v_and_b32_e32 v3, 0xffc0, v4
	v_sub_u32_e32 v1, v1, v3
	v_lshrrev_b16_e32 v3, 7, v1
	v_and_b32_e32 v3, 1, v3
	v_lshlrev_b32_e32 v2, 5, v2
	v_add_u16_e32 v1, v1, v3
	v_and_b32_e32 v2, 32, v2
	v_ashrrev_i16_sdwa v1, v222, sext(v1) dst_sel:DWORD dst_unused:UNUSED_PAD src0_sel:DWORD src1_sel:BYTE_0
	v_add_u32_sdwa v1, v2, sext(v1) dst_sel:DWORD dst_unused:UNUSED_PAD src0_sel:DWORD src1_sel:WORD_0
	v_lshlrev_b32_e32 v2, 1, v220
	v_lshrrev_b32_e32 v3, 2, v220
	v_and_b32_e32 v4, 3, v5
	v_and_b32_e32 v2, 24, v2
	v_and_b32_e32 v3, 4, v3
	v_and_or_b32 v4, v220, s1, v4
	v_lshlrev_b32_e32 v221, 1, v1
	v_or3_b32 v2, v4, v3, v2
	v_and_b32_e32 v3, 62, v221
	v_lshlrev_b32_e32 v1, 11, v1
	v_and_or_b32 v1, v1, s2, v3
	v_lshl_add_u32 v196, v2, 6, v1
	v_lshlrev_b32_e32 v1, 2, v218
	v_add_u32_e32 v2, s18, v1
	ds_read_b32 v2, v2
	v_readlane_b32 s1, v254, 13
	s_add_i32 s31, s0, 0
	s_add_i32 s34, s31, 0x10000
	v_add_u32_e32 v1, s1, v1
	ds_read_b32 v1, v1
	s_waitcnt lgkmcnt(1)
	v_lshl_add_u32 v204, v2, 11, v219
	v_lshlrev_b32_e32 v2, 2, v220
	v_add_u32_e32 v3, s18, v2
	s_add_i32 s35, s31, 0x12000
	ds_read_b32 v3, v3
	s_waitcnt lgkmcnt(1)
	v_lshl_add_u32 v208, v1, 11, v219
	v_add_u32_e32 v1, s1, v2
	s_mov_b32 m0, s34
	s_add_u32 s0, s4, 0x2000
	ds_read_b32 v1, v1
	global_load_lds_dwordx4 v194, s[4:5]
	s_mov_b32 m0, s35
	s_addc_u32 s1, s5, 0
	s_add_i32 s36, s31, 0x14000
	global_load_lds_dwordx4 v196, s[4:5]
	s_mov_b32 m0, s36
	s_add_i32 s37, s31, 0x16000
	global_load_lds_dwordx4 v194, s[0:1]
	s_mov_b32 m0, s37
	s_add_i32 s38, s31, 0x2000
	global_load_lds_dwordx4 v196, s[0:1]
	s_mov_b32 m0, s31
	s_waitcnt lgkmcnt(0)
	v_lshl_add_u32 v206, v3, 11, v221
	global_load_lds_dwordx4 v204, s[16:17]
	s_mov_b32 m0, s38
	s_add_i32 s39, s31, 0x4000
	global_load_lds_dwordx4 v206, s[16:17]
	s_mov_b32 m0, s39
	s_add_i32 s40, s31, 0x6000
	v_lshl_add_u32 v210, v1, 11, v221
	global_load_lds_dwordx4 v208, s[16:17]
	s_mov_b32 m0, s40
	v_readlane_b32 s2, v249, 47
	global_load_lds_dwordx4 v210, s[16:17]
	v_readlane_b32 s3, v249, 48
	s_andn2_b64 vcc, exec, s[2:3]
	s_nop 0
	v_cndmask_b32_e64 v1, 0, 1, s[2:3]
	v_cmp_ne_u32_e64 s[0:1], 1, v1
	s_cbranch_vccnz .LBB0_1290
	s_barrier
	s_setprio 1

; #define PG8_STAGE_B(bufoff, gbase) do { _Pragma("unroll") for (int _i = 0; _i < 2; ++_i) \
;         __builtin_amdgcn_global_load_lds((const unsigned*)((const char*)(gbase) + voffB[_i]), (LAS unsigned*)(lds + (bufoff) + ldsw + _i * 8192), 16, 0, 0); } while (0)
; #define PG8_STAGE_A(bufoff, gbase, VO, h) do { _Pragma("unroll") for (int _i = 0; _i < 2; ++_i) \
;         __builtin_amdgcn_global_load_lds((const unsigned*)((const char*)(gbase) + (VO)[h][_i]), (LAS unsigned*)(lds + (bufoff) + ldsw + _i * 8192), 16, 0, 0); } while (0)
; #define PG8_WAIT_V(n) asm volatile("s_waitcnt vmcnt(" #n ")" ::: "memory")
; #define PG8_WAIT_L(n) asm volatile("s_waitcnt lgkmcnt(" #n ")" ::: "memory")
; #define PG8_WAIT_VX(rx) do { if (rx) asm volatile("s_waitcnt vmcnt(%0)" :: "n"(8 + Epi::NVM) : "memory"); else asm volatile("s_waitcnt vmcnt(8)" ::: "memory"); } while (0)
; #define PG8_BAR __builtin_amdgcn_s_barrier()
; #define PG8_SCHED __builtin_amdgcn_sched_barrier(0)
;     ...
;             PG8_WAIT_VX(rx); PG8_WAIT_L(0); PG8_BAR; PG8_MMA(0, 0, At, B0); PG8_MMA(0, 1, At, B1); PG8_BAR; PG8_SCHED;
;             PG8_LDA(At, 1, 1); PG8_STAGE_B(PG8_SB(1, 0), b3); PG8_STAGE_B(PG8_SB(1, 1), b3 + hstepB); PG8_STAGE_A(PG8_SA(1, 0), a3, vo2, 0);
;             PG8_WAIT_V(8); PG8_WAIT_L(0); PG8_BAR; PG8_MMA(1, 0, At, B0); PG8_MMA(1, 1, At, B1); PG8_BAR; PG8_SCHED;
.LBB0_1298:
	s_waitcnt lgkmcnt(0)
	v_mov_b32_e32 v217, v65
	s_add_u32 s4, s22, 0x20000
	v_lshl_add_u64 v[242:243], s[24:25], 0, v[64:65]
	v_lshl_add_u64 v[216:217], s[24:25], 0, v[216:217]
	s_addc_u32 s5, s23, 0
	s_barrier
	s_waitcnt lgkmcnt(0)
	v_mfma_scale_f32_16x16x128_f8f6f4 v[190:193], v[24:31], v[56:63], v[190:193], v226, v225 op_sel_hi:[0,0,0]
	v_mfma_scale_f32_16x16x128_f8f6f4 v[182:185], v[16:23], v[56:63], v[182:185], v226, v225 op_sel_hi:[0,0,0]
	v_mfma_scale_f32_16x16x128_f8f6f4 v[174:177], v[24:31], v[48:55], v[174:177], v226, v225 op_sel_hi:[0,0,0]
	v_mfma_scale_f32_16x16x128_f8f6f4 v[166:169], v[16:23], v[48:55], v[166:169], v226, v225 op_sel_hi:[0,0,0]
	v_mfma_scale_f32_16x16x128_f8f6f4 v[158:161], v[24:31], v[40:47], v[158:161], v226, v225 op_sel_hi:[0,0,0]
	v_mfma_scale_f32_16x16x128_f8f6f4 v[150:153], v[16:23], v[40:47], v[150:153], v226, v225 op_sel_hi:[0,0,0]
	v_mfma_scale_f32_16x16x128_f8f6f4 v[142:145], v[24:31], v[32:39], v[142:145], v226, v225 op_sel_hi:[0,0,0]
	v_mfma_scale_f32_16x16x128_f8f6f4 v[134:137], v[16:23], v[32:39], v[134:137], v226, v225 op_sel_hi:[0,0,0]
	v_mfma_scale_f32_16x16x128_f8f6f4 v[186:189], v[8:15], v[56:63], v[186:189], v226, v225 op_sel_hi:[0,0,0]
	v_mfma_scale_f32_16x16x128_f8f6f4 v[178:181], v[0:7], v[56:63], v[178:181], v226, v225 op_sel_hi:[0,0,0]
	v_mfma_scale_f32_16x16x128_f8f6f4 v[170:173], v[8:15], v[48:55], v[170:173], v226, v225 op_sel_hi:[0,0,0]
	v_mfma_scale_f32_16x16x128_f8f6f4 v[162:165], v[0:7], v[48:55], v[162:165], v226, v225 op_sel_hi:[0,0,0]
	v_mfma_scale_f32_16x16x128_f8f6f4 v[154:157], v[8:15], v[40:47], v[154:157], v226, v225 op_sel_hi:[0,0,0]
	v_mfma_scale_f32_16x16x128_f8f6f4 v[146:149], v[0:7], v[40:47], v[146:149], v226, v225 op_sel_hi:[0,0,0]
	v_mfma_scale_f32_16x16x128_f8f6f4 v[138:141], v[8:15], v[32:39], v[138:141], v226, v225 op_sel_hi:[0,0,0]
	v_mfma_scale_f32_16x16x128_f8f6f4 v[130:133], v[0:7], v[32:39], v[130:133], v226, v225 op_sel_hi:[0,0,0]
	s_barrier
	s_mov_b32 m0, s41
	v_lshl_add_u64 v[244:245], s[4:5], 0, v[194:195]
	ds_read_b128 v[32:35], v237 offset:49152
	ds_read_b128 v[36:39], v237 offset:50176
	ds_read_b128 v[40:43], v237 offset:51200
	ds_read_b128 v[44:47], v237 offset:52224
	ds_read_b128 v[48:51], v237 offset:53248
	ds_read_b128 v[52:55], v237 offset:54272
	ds_read_b128 v[56:59], v237 offset:55296
	ds_read_b128 v[60:63], v237 offset:56320
	global_load_lds_dwordx4 v[244:245], off
	v_lshl_add_u64 v[244:245], s[4:5], 0, v[196:197]
	s_add_u32 s4, s22, 0x22000
	s_mov_b32 m0, s42
	s_addc_u32 s5, s23, 0
	global_load_lds_dwordx4 v[244:245], off
	v_lshl_add_u64 v[244:245], s[4:5], 0, v[194:195]
	s_mov_b32 m0, s45
	v_lshl_add_u64 v[242:243], v[242:243], 0, s[94:95]
	global_load_lds_dwordx4 v[244:245], off
	v_lshl_add_u64 v[244:245], s[4:5], 0, v[196:197]
	s_mov_b32 m0, s46
	v_lshl_add_u64 v[216:217], v[216:217], 0, s[94:95]
	global_load_lds_dwordx4 v[244:245], off
	s_mov_b32 m0, s43
	s_nop 0
	global_load_lds_dwordx4 v[242:243], off
	s_mov_b32 m0, s44
	s_nop 0
	global_load_lds_dwordx4 v[216:217], off
	s_waitcnt vmcnt(8)
	s_waitcnt lgkmcnt(0)
	s_barrier
	s_waitcnt lgkmcnt(0)
	v_mfma_scale_f32_16x16x128_f8f6f4 v[126:129], v[24:31], v[32:39], v[126:129], v226, v225 op_sel_hi:[0,0,0]
	v_mfma_scale_f32_16x16x128_f8f6f4 v[118:121], v[16:23], v[32:39], v[118:121], v226, v225 op_sel_hi:[0,0,0]
	v_mfma_scale_f32_16x16x128_f8f6f4 v[110:113], v[24:31], v[40:47], v[110:113], v226, v225 op_sel_hi:[0,0,0]
	v_mfma_scale_f32_16x16x128_f8f6f4 v[102:105], v[16:23], v[40:47], v[102:105], v226, v225 op_sel_hi:[0,0,0]
	v_mfma_scale_f32_16x16x128_f8f6f4 v[94:97], v[24:31], v[48:55], v[94:97], v226, v225 op_sel_hi:[0,0,0]
	v_mfma_scale_f32_16x16x128_f8f6f4 v[86:89], v[16:23], v[48:55], v[86:89], v226, v225 op_sel_hi:[0,0,0]
	v_mfma_scale_f32_16x16x128_f8f6f4 v[78:81], v[24:31], v[56:63], v[78:81], v226, v225 op_sel_hi:[0,0,0]
	v_mfma_scale_f32_16x16x128_f8f6f4 v[70:73], v[16:23], v[56:63], v[70:73], v226, v225 op_sel_hi:[0,0,0]
	v_mfma_scale_f32_16x16x128_f8f6f4 v[122:125], v[8:15], v[32:39], v[122:125], v226, v225 op_sel_hi:[0,0,0]
	v_mfma_scale_f32_16x16x128_f8f6f4 v[114:117], v[0:7], v[32:39], v[114:117], v226, v225 op_sel_hi:[0,0,0]
	v_mfma_scale_f32_16x16x128_f8f6f4 v[106:109], v[8:15], v[40:47], v[106:109], v226, v225 op_sel_hi:[0,0,0]
	v_mfma_scale_f32_16x16x128_f8f6f4 v[98:101], v[0:7], v[40:47], v[98:101], v226, v225 op_sel_hi:[0,0,0]
	v_mfma_scale_f32_16x16x128_f8f6f4 v[90:93], v[8:15], v[48:55], v[90:93], v226, v225 op_sel_hi:[0,0,0]
	v_mfma_scale_f32_16x16x128_f8f6f4 v[82:85], v[0:7], v[48:55], v[82:85], v226, v225 op_sel_hi:[0,0,0]
	v_mfma_scale_f32_16x16x128_f8f6f4 v[74:77], v[8:15], v[56:63], v[74:77], v226, v225 op_sel_hi:[0,0,0]
	v_mfma_scale_f32_16x16x128_f8f6f4 v[66:69], v[0:7], v[56:63], v[66:69], v226, v225 op_sel_hi:[0,0,0]
	s_barrier
	s_add_i32 s51, s51, 2
	s_add_u32 s49, s49, 0x40000
	s_addc_u32 s50, s50, 0
	s_add_u32 s20, s20, 0x100
	s_addc_u32 s21, s21, 0
	s_cmp_gt_u32 s51, 13
	s_cbranch_scc1 .LBB0_1311

; #define PG8_STAGE_B(bufoff, gbase) do { _Pragma("unroll") for (int _i = 0; _i < 2; ++_i) \
;         __builtin_amdgcn_global_load_lds((const unsigned*)((const char*)(gbase) + voffB[_i]), (LAS unsigned*)(lds + (bufoff) + ldsw + _i * 8192), 16, 0, 0); } while (0)
; #define PG8_STAGE_A(bufoff, gbase, VO, h) do { _Pragma("unroll") for (int _i = 0; _i < 2; ++_i) \
;         __builtin_amdgcn_global_load_lds((const unsigned*)((const char*)(gbase) + (VO)[h][_i]), (LAS unsigned*)(lds + (bufoff) + ldsw + _i * 8192), 16, 0, 0); } while (0)
; #define PG8_WAIT_L(n) asm volatile("s_waitcnt lgkmcnt(" #n ")" ::: "memory")
; #define PG8_WAIT_VX(rx) do { if (rx) asm volatile("s_waitcnt vmcnt(%0)" :: "n"(8 + Epi::NVM) : "memory"); else asm volatile("s_waitcnt vmcnt(8)" ::: "memory"); } while (0)
; #define PG8_BAR __builtin_amdgcn_s_barrier()
; #define PG8_SCHED __builtin_amdgcn_sched_barrier(0)
;     ...
;             const bool last = (t == nt - 2); int rxi = (relax && t == 0) ? 1 : 0; asm volatile("" : "+v"(rxi)); const bool rx = __builtin_amdgcn_readfirstlane(rxi) != 0;
;             if constexpr (Epi::HAS_MID) { constexpr int SEGT = (F8 != 0) ? 8 : 16; if (t == SEGT || t == 2 * SEGT) { PG8_SCHED; E.mid(acc, cur, t / SEGT, wr, wc, fr, fq); PG8_SCHED; } }
;             const char* a1 = cA + (size_t)(t + 1) * kstep;
;             const char* a2 = last ? nA : cA + (size_t)(t + 2) * kstep; const char* b2 = last ? nB : cB + (size_t)(t + 2) * kstepB;
;             const char* a3 = a2 + kstep; const char* b3 = b2 + kstepB;
;             unsigned vo2[2][2];
; #pragma unroll
;             for (int h = 0; h < 2; ++h)
; #pragma unroll
;                 for (int i = 0; i < 2; ++i) vo2[h][i] = (GATHER && last) ? voffN[h][i] : voffA[h][i];
;             PG8_LDB(B0, 0, 0); PG8_LDB(B1, 0, 1); PG8_SCHED; PG8_LDA(At, 0, 0); if (!rx) PG8_STAGE_A(PG8_SA(1, 1), a1, voffA, 1);
;             PG8_WAIT_VX(rx); PG8_WAIT_L(0); PG8_BAR; PG8_MMA(0, 0, At, B0); PG8_MMA(0, 1, At, B1); PG8_BAR; PG8_SCHED;
;             PG8_LDA(At, 0, 1); PG8_STAGE_B(PG8_SB(0, 0), b2); PG8_STAGE_B(PG8_SB(0, 1), b2 + hstepB); PG8_STAGE_A(PG8_SA(0, 0), a2, vo2, 0);
.LBB0_1302:
	s_add_u32 s4, s16, s20
	s_addc_u32 s5, s17, s21
	s_add_u32 s22, s4, 0x100
	s_addc_u32 s23, s5, 0
	s_cmpk_eq_i32 s20, 0x700
	s_cselect_b64 s[4:5], -1, 0
	s_waitcnt lgkmcnt(0)
	s_and_b64 s[6:7], s[4:5], exec
	v_cndmask_b32_e64 v64, v204, v240, s[4:5]
	s_cselect_b32 s25, s15, s23
	s_cselect_b32 s24, s14, s22
	v_cndmask_b32_e64 v216, v206, v239, s[4:5]
	s_cselect_b32 s23, s13, s50
	s_cselect_b32 s22, s12, s49
	s_barrier
	s_waitcnt lgkmcnt(0)
	v_mfma_scale_f32_16x16x128_f8f6f4 v[190:193], v[24:31], v[56:63], v[190:193], v226, v225 op_sel_hi:[0,0,0]
	v_mfma_scale_f32_16x16x128_f8f6f4 v[182:185], v[16:23], v[56:63], v[182:185], v226, v225 op_sel_hi:[0,0,0]
	v_mfma_scale_f32_16x16x128_f8f6f4 v[174:177], v[24:31], v[48:55], v[174:177], v226, v225 op_sel_hi:[0,0,0]
	v_mfma_scale_f32_16x16x128_f8f6f4 v[166:169], v[16:23], v[48:55], v[166:169], v226, v225 op_sel_hi:[0,0,0]
	v_mfma_scale_f32_16x16x128_f8f6f4 v[158:161], v[24:31], v[40:47], v[158:161], v226, v225 op_sel_hi:[0,0,0]
	v_mfma_scale_f32_16x16x128_f8f6f4 v[150:153], v[16:23], v[40:47], v[150:153], v226, v225 op_sel_hi:[0,0,0]
	v_mfma_scale_f32_16x16x128_f8f6f4 v[142:145], v[24:31], v[32:39], v[142:145], v226, v225 op_sel_hi:[0,0,0]
	v_mfma_scale_f32_16x16x128_f8f6f4 v[134:137], v[16:23], v[32:39], v[134:137], v226, v225 op_sel_hi:[0,0,0]
	v_mfma_scale_f32_16x16x128_f8f6f4 v[186:189], v[8:15], v[56:63], v[186:189], v226, v225 op_sel_hi:[0,0,0]
	v_mfma_scale_f32_16x16x128_f8f6f4 v[178:181], v[0:7], v[56:63], v[178:181], v226, v225 op_sel_hi:[0,0,0]
	v_mfma_scale_f32_16x16x128_f8f6f4 v[170:173], v[8:15], v[48:55], v[170:173], v226, v225 op_sel_hi:[0,0,0]
	v_mfma_scale_f32_16x16x128_f8f6f4 v[162:165], v[0:7], v[48:55], v[162:165], v226, v225 op_sel_hi:[0,0,0]
	v_mfma_scale_f32_16x16x128_f8f6f4 v[154:157], v[8:15], v[40:47], v[154:157], v226, v225 op_sel_hi:[0,0,0]
	v_mfma_scale_f32_16x16x128_f8f6f4 v[146:149], v[0:7], v[40:47], v[146:149], v226, v225 op_sel_hi:[0,0,0]
	v_mfma_scale_f32_16x16x128_f8f6f4 v[138:141], v[8:15], v[32:39], v[138:141], v226, v225 op_sel_hi:[0,0,0]
	v_mfma_scale_f32_16x16x128_f8f6f4 v[130:133], v[0:7], v[32:39], v[130:133], v226, v225 op_sel_hi:[0,0,0]
	s_barrier
	s_mov_b32 m0, s34
	v_lshl_add_u64 v[242:243], s[22:23], 0, v[194:195]
	s_add_u32 s6, s22, 0x2000
	ds_read_b128 v[56:59], v237 offset:16384
	ds_read_b128 v[60:63], v237 offset:17408
	ds_read_b128 v[48:51], v237 offset:18432
	ds_read_b128 v[52:55], v237 offset:19456
	ds_read_b128 v[40:43], v237 offset:20480
	ds_read_b128 v[44:47], v237 offset:21504
	ds_read_b128 v[32:35], v237 offset:22528
	ds_read_b128 v[36:39], v237 offset:23552
	global_load_lds_dwordx4 v[242:243], off
	v_lshl_add_u64 v[242:243], s[22:23], 0, v[196:197]
	s_mov_b32 m0, s35
	s_addc_u32 s7, s23, 0
	global_load_lds_dwordx4 v[242:243], off
	v_lshl_add_u64 v[242:243], s[6:7], 0, v[194:195]
	s_mov_b32 m0, s36
	v_cndmask_b32_e64 v201, 0, 1, s[26:27]
	global_load_lds_dwordx4 v[242:243], off
	v_lshl_add_u64 v[242:243], s[6:7], 0, v[196:197]
	s_mov_b32 m0, s37
	v_cmp_ne_u32_e64 s[6:7], 1, v201
	global_load_lds_dwordx4 v[242:243], off
	s_mov_b32 m0, s31
	s_andn2_b64 vcc, exec, s[26:27]
	global_load_lds_dwordx4 v64, s[24:25]
	s_mov_b32 m0, s38
	s_nop 0
	global_load_lds_dwordx4 v216, s[24:25]
	s_cbranch_vccnz .LBB0_1308
	s_waitcnt vmcnt(16)
	s_cbranch_execnz .LBB0_1305

; #define PG8_STAGE_B(bufoff, gbase) do { _Pragma("unroll") for (int _i = 0; _i < 2; ++_i) \
;         __builtin_amdgcn_global_load_lds((const unsigned*)((const char*)(gbase) + voffB[_i]), (LAS unsigned*)(lds + (bufoff) + ldsw + _i * 8192), 16, 0, 0); } while (0)
; #define PG8_STAGE_A(bufoff, gbase, VO, h) do { _Pragma("unroll") for (int _i = 0; _i < 2; ++_i) \
;         __builtin_amdgcn_global_load_lds((const unsigned*)((const char*)(gbase) + (VO)[h][_i]), (LAS unsigned*)(lds + (bufoff) + ldsw + _i * 8192), 16, 0, 0); } while (0)
; #define PG8_WAIT_L(n) asm volatile("s_waitcnt lgkmcnt(" #n ")" ::: "memory")
; #define PG8_WAIT_VX(rx) do { if (rx) asm volatile("s_waitcnt vmcnt(%0)" :: "n"(8 + Epi::NVM) : "memory"); else asm volatile("s_waitcnt vmcnt(8)" ::: "memory"); } while (0)
; #define PG8_BAR __builtin_amdgcn_s_barrier()
; #define PG8_SCHED __builtin_amdgcn_sched_barrier(0)
;     ...
;                 for (int i = 0; i < 2; ++i) vo2[h][i] = (GATHER && last) ? voffN[h][i] : voffA[h][i];
;             PG8_LDB(B0, 0, 0); PG8_LDB(B1, 0, 1); PG8_SCHED; PG8_LDA(At, 0, 0); if (!rx) PG8_STAGE_A(PG8_SA(1, 1), a1, voffA, 1);
;             PG8_WAIT_VX(rx); PG8_WAIT_L(0); PG8_BAR; PG8_MMA(0, 0, At, B0); PG8_MMA(0, 1, At, B1); PG8_BAR; PG8_SCHED;
;             PG8_LDA(At, 0, 1); PG8_STAGE_B(PG8_SB(0, 0), b2); PG8_STAGE_B(PG8_SB(0, 1), b2 + hstepB); PG8_STAGE_A(PG8_SA(0, 0), a2, vo2, 0);
;             PG8_WAIT_VX(rx); PG8_WAIT_L(0); PG8_BAR; PG8_MMA(1, 0, At, B0); PG8_MMA(1, 1, At, B1); PG8_BAR; PG8_SCHED;
;             PG8_LDB(B0, 1, 0); PG8_LDB(B1, 1, 1); PG8_SCHED; PG8_LDA(At, 1, 0); PG8_STAGE_A(PG8_SA(0, 1), a2, vo2, 1);
.LBB0_1305:
	s_waitcnt lgkmcnt(0)
	v_cndmask_b32_e64 v201, v208, v202, s[4:5]
	v_cndmask_b32_e64 v203, v210, v200, s[4:5]
	s_barrier
	s_waitcnt lgkmcnt(0)
	v_mfma_scale_f32_16x16x128_f8f6f4 v[126:129], v[24:31], v[56:63], v[126:129], v226, v225 op_sel_hi:[0,0,0]
	v_mfma_scale_f32_16x16x128_f8f6f4 v[118:121], v[16:23], v[56:63], v[118:121], v226, v225 op_sel_hi:[0,0,0]
	v_mfma_scale_f32_16x16x128_f8f6f4 v[110:113], v[24:31], v[48:55], v[110:113], v226, v225 op_sel_hi:[0,0,0]
	v_mfma_scale_f32_16x16x128_f8f6f4 v[102:105], v[16:23], v[48:55], v[102:105], v226, v225 op_sel_hi:[0,0,0]
	v_mfma_scale_f32_16x16x128_f8f6f4 v[94:97], v[24:31], v[40:47], v[94:97], v226, v225 op_sel_hi:[0,0,0]
	v_mfma_scale_f32_16x16x128_f8f6f4 v[86:89], v[16:23], v[40:47], v[86:89], v226, v225 op_sel_hi:[0,0,0]
	v_mfma_scale_f32_16x16x128_f8f6f4 v[78:81], v[24:31], v[32:39], v[78:81], v226, v225 op_sel_hi:[0,0,0]
	v_mfma_scale_f32_16x16x128_f8f6f4 v[70:73], v[16:23], v[32:39], v[70:73], v226, v225 op_sel_hi:[0,0,0]
	v_mfma_scale_f32_16x16x128_f8f6f4 v[122:125], v[8:15], v[56:63], v[122:125], v226, v225 op_sel_hi:[0,0,0]
	v_mfma_scale_f32_16x16x128_f8f6f4 v[114:117], v[0:7], v[56:63], v[114:117], v226, v225 op_sel_hi:[0,0,0]
	v_mfma_scale_f32_16x16x128_f8f6f4 v[106:109], v[8:15], v[48:55], v[106:109], v226, v225 op_sel_hi:[0,0,0]
	v_mfma_scale_f32_16x16x128_f8f6f4 v[98:101], v[0:7], v[48:55], v[98:101], v226, v225 op_sel_hi:[0,0,0]
	v_mfma_scale_f32_16x16x128_f8f6f4 v[90:93], v[8:15], v[40:47], v[90:93], v226, v225 op_sel_hi:[0,0,0]
	v_mfma_scale_f32_16x16x128_f8f6f4 v[82:85], v[0:7], v[40:47], v[82:85], v226, v225 op_sel_hi:[0,0,0]
	v_mfma_scale_f32_16x16x128_f8f6f4 v[74:77], v[8:15], v[32:39], v[74:77], v226, v225 op_sel_hi:[0,0,0]
	v_mfma_scale_f32_16x16x128_f8f6f4 v[66:69], v[0:7], v[32:39], v[66:69], v226, v225 op_sel_hi:[0,0,0]
	s_barrier
	v_add_u32_e32 v0, 0x18000, v207
	v_add_u32_e32 v4, 0x1c000, v207
	ds_read_b128 v[24:27], v0
	ds_read_b128 v[28:31], v0 offset:1024
	ds_read_b128 v[16:19], v0 offset:2048
	ds_read_b128 v[20:23], v0 offset:3072
	ds_read_b128 v[8:11], v4
	ds_read_b128 v[12:15], v4 offset:1024
	ds_read_b128 v[0:3], v4 offset:2048
	ds_read_b128 v[4:7], v4 offset:3072
	s_mov_b32 m0, s39
	ds_read_b128 v[56:59], v237 offset:32768
	ds_read_b128 v[60:63], v237 offset:33792
	ds_read_b128 v[48:51], v237 offset:34816
	ds_read_b128 v[52:55], v237 offset:35840
	ds_read_b128 v[40:43], v237 offset:36864
	ds_read_b128 v[44:47], v237 offset:37888
	ds_read_b128 v[32:35], v237 offset:38912
	ds_read_b128 v[36:39], v237 offset:39936
	global_load_lds_dwordx4 v201, s[24:25]
	s_mov_b32 m0, s40
	s_and_b64 vcc, exec, s[6:7]
	global_load_lds_dwordx4 v203, s[24:25]
	s_cbranch_vccnz .LBB0_1309
	s_waitcnt vmcnt(16)
	s_cbranch_execnz .LBB0_1298
	s_branch .LBB0_1310

; #define PG8_STAGE_A(bufoff, gbase, VO, h) do { _Pragma("unroll") for (int _i = 0; _i < 2; ++_i) \
;         __builtin_amdgcn_global_load_lds((const unsigned*)((const char*)(gbase) + (VO)[h][_i]), (LAS unsigned*)(lds + (bufoff) + ldsw + _i * 8192), 16, 0, 0); } while (0)
; #define PG8_BAR __builtin_amdgcn_s_barrier()
;     ...
;         if (ALIGN_EPI) { if (wr == 0) PG8_BAR; }
;         if (ALIGN_EPI && has_next) { if constexpr (GATHER) PG8_STAGE_A(PG8_SA(1, 1), nA + kstep, voffN, 1); else PG8_STAGE_A(PG8_SA(1, 1), nA + kstep, voffA, 1); }
.LBB0_1311:
	s_setprio 0
	v_readlane_b32 s4, v249, 49
	v_readlane_b32 s5, v249, 50
	s_and_b64 vcc, exec, s[4:5]
	s_cbranch_vccz .LBB0_1313
	s_barrier

; __device__ __forceinline__ int ltid(int wave0) { int t; asm volatile("v_mbcnt_lo_u32_b32 %0, -1, 0\n\tv_mbcnt_hi_u32_b32 %0, -1, %0" : "=v"(t)); return (wave0 << 6) | t; }
;     __device__ __forceinline__ bool next(int i, Unit& u) const {
;         const int L = i * G + vcu; if (L >= tb->tq[65] * NT) return false;
;         const int mt = L / NT, pn = L % NT; const int e = tb->tile_e[mt];
;         const int m0 = (mt - tb->tq[e]) * BM;
;         u.e = e; u.m0 = m0; u.orow = tb->rb[e] + m0; u.pn = pn; u.seg = i;
;         u.B = B + (size_t)e * bexp + (size_t)pn * btile;
;         u.A = GATH ? A : A + (size_t)u.orow * arow; return true; }
;     ...
;     const int tid = ltid(wave0), wid = wave0, lane = tid & 63, wr = wid >> 2, wc = wid & 3, fr = lane & 15, fq = lane >> 4;
;     const int nt = K / BK;
;     unsigned voffB[2], voffA[2][2], voffN[2][2]; int Rr[2], Cc[2];
; #pragma unroll
;     for (int i = 0; i < 2; ++i) { int R, C; stage_rc(tid * 16 + i * 8192, R, C); const int Rb = (R & ~31) + perm32(R & 31);
;         Rr[i] = R; Cc[i] = C; voffB[i] = nB64 ? (unsigned)(Rb * 64 + ((C * 2) & 63) + ((C * 2) >> 6) * nB64 * 64) : (unsigned)(Rb * ldb + C) * 2u;
;         voffA[0][i] = (unsigned)(R * lda + C) * 2u; voffA[1][i] = (unsigned)((R + HALF) * lda + C) * 2u; voffN[0][i] = voffA[0][i]; voffN[1][i] = voffA[1][i]; }
.LBB0_1401:
	v_readlane_b32 s0, v254, 12
	v_mbcnt_lo_u32_b32 v0, -1, 0
	v_mbcnt_hi_u32_b32 v0, -1, v0
	s_nop 1
	v_mov_b32_e32 v1, s0
	ds_read_b32 v1, v1
	v_readlane_b32 s0, v249, 2
	s_waitcnt lgkmcnt(0)
	v_lshlrev_b32_e32 v1, 3, v1
	v_cmp_ge_i32_e32 vcc, s0, v1
	s_cbranch_vccnz .LBB0_1431
	v_readlane_b32 s4, v249, 40
	v_mov_b32_e32 v7, 0x10000
	s_mov_b32 s3, 0xfffe0000
	v_lshl_or_b32 v1, v0, 4, s4
	v_add_u32_e32 v2, 0x2000, v1
	v_ashrrev_i32_e32 v3, 31, v2
	v_lshrrev_b32_e32 v3, 22, v3
	v_add_u32_e32 v3, v2, v3
	v_ashrrev_i32_e32 v3, 10, v3
	v_mul_i32_i24_e32 v4, 0x400, v3
	v_sub_u32_e32 v2, v2, v4
	v_lshrrev_b32_e32 v4, 4, v2
	v_bitop3_b32 v2, v4, v2, 32 bitop3:0x6c
	v_ashrrev_i32_e32 v4, 31, v2
	v_lshrrev_b32_e32 v4, 26, v4
	v_add_u32_e32 v4, v2, v4
	v_ashrrev_i32_e32 v5, 6, v4
	v_and_b32_e32 v4, 0xffc0, v4
	v_sub_u32_e32 v2, v2, v4
	v_lshrrev_b16_e32 v4, 7, v2
	v_and_b32_e32 v4, 1, v4
	v_lshlrev_b32_e32 v6, 3, v3
	v_lshlrev_b32_e32 v3, 5, v3
	v_add_u16_e32 v2, v2, v4
	v_and_b32_e32 v6, -16, v6
	v_and_b32_e32 v3, 32, v3
	v_ashrrev_i16_sdwa v2, v222, sext(v2) dst_sel:DWORD dst_unused:UNUSED_PAD src0_sel:DWORD src1_sel:BYTE_0
	v_add_u32_e32 v6, v5, v6
	v_add_u32_sdwa v2, v3, sext(v2) dst_sel:DWORD dst_unused:UNUSED_PAD src0_sel:DWORD src1_sel:WORD_0
	v_lshl_add_u32 v3, v6, 8, v2
	v_lshl_add_u32 v194, v3, 1, v7
	v_lshlrev_b32_e32 v3, 1, v2
	v_lshl_add_u32 v196, v6, 9, v3
	v_lshlrev_b32_e32 v2, 12, v2
	v_and_b32_e32 v3, 62, v3
	v_and_or_b32 v2, v2, s3, v3
	v_and_b32_e32 v3, 3, v5
	s_mov_b32 s2, 0x3ffffe0
	v_lshrrev_b32_e32 v4, 2, v6
	v_lshlrev_b32_e32 v5, 1, v6
	v_and_or_b32 v3, v6, s2, v3
	v_and_b32_e32 v4, 4, v4
	v_and_b32_e32 v5, 24, v5
	v_or3_b32 v3, v3, v4, v5
	v_lshl_add_u32 v198, v3, 6, v2
	v_and_b32_e32 v9, -32, v6
	v_lshl_add_u32 v198, v9, 6, v198
	v_and_b32_e32 v9, 12, v6
	v_lshl_add_u32 v198, v9, 7, v198
	v_ashrrev_i32_e32 v2, 31, v1
	v_lshrrev_b32_e32 v2, 22, v2
	v_add_u32_e32 v2, v1, v2
	v_ashrrev_i32_e32 v2, 10, v2
	v_mul_i32_i24_e32 v3, 0x400, v2
	v_sub_u32_e32 v1, v1, v3
	v_lshrrev_b32_e32 v3, 4, v1
	v_bitop3_b32 v1, v3, v1, 32 bitop3:0x6c
	v_ashrrev_i32_e32 v3, 31, v1
	v_lshrrev_b32_e32 v3, 26, v3
	v_add_u32_e32 v3, v1, v3
	v_ashrrev_i32_e32 v4, 6, v3
	v_and_b32_e32 v3, 0xc0, v3
	v_lshlrev_b32_e32 v5, 3, v2
	v_lshlrev_b32_e32 v2, 5, v2
	v_sub_u32_e32 v1, v1, v3
	v_and_b32_e32 v5, -16, v5
	v_and_b32_e32 v2, 32, v2
	v_ashrrev_i16_sdwa v1, v222, sext(v1) dst_sel:DWORD dst_unused:UNUSED_PAD src0_sel:DWORD src1_sel:BYTE_0
	v_add_u32_e32 v5, v4, v5
	v_add_u32_sdwa v1, v2, sext(v1) dst_sel:DWORD dst_unused:UNUSED_PAD src0_sel:DWORD src1_sel:WORD_0
	v_readlane_b32 s0, v254, 22
	v_lshl_add_u32 v2, v5, 8, v1
	s_add_u32 s31, s0, 0x14800000
	v_readlane_b32 s0, v254, 23
	v_lshl_add_u32 v200, v2, 1, v7
	v_lshlrev_b32_e32 v2, 1, v1
	s_addc_u32 s34, s0, 0
	v_readlane_b32 s0, v251, 43
	v_lshl_add_u32 v202, v5, 9, v2
	v_lshlrev_b32_e32 v1, 12, v1
	v_and_b32_e32 v2, 62, v2
	v_readlane_b32 s1, v251, 44
	s_add_u32 s0, s31, s0
	v_and_or_b32 v1, v1, s3, v2
	v_and_b32_e32 v2, 3, v4
	v_lshrrev_b32_e32 v3, 2, v5
	v_lshlrev_b32_e32 v4, 1, v5
	v_readlane_b32 s3, v251, 40
	s_addc_u32 s1, s34, s1
	v_and_or_b32 v2, v5, s2, v2
	v_and_b32_e32 v3, 4, v3
	v_and_b32_e32 v4, 24, v4
	s_add_i32 s2, s3, 0
	v_or3_b32 v2, v2, v3, v4
	s_add_i32 s2, s2, 0x23320
	v_lshl_add_u32 v64, v2, 6, v1
	v_and_b32_e32 v9, -32, v5
	v_lshl_add_u32 v64, v9, 6, v64
	v_and_b32_e32 v9, 12, v5
	v_lshl_add_u32 v64, v9, 7, v64
	v_mov_b32_e32 v1, s2
	ds_read_u8 v1, v1
	s_waitcnt lgkmcnt(0)
	v_lshlrev_b32_e32 v2, 2, v1
	v_add_u32_e32 v2, 0, v2
	v_add_u32_e32 v3, 0x2320c, v2
	ds_read_b32 v3, v3
	v_add_u32_e32 v2, 0x23104, v2
	ds_read_b32 v2, v2
	s_waitcnt lgkmcnt(0)
	v_readfirstlane_b32 s2, v3
	s_sub_i32 s2, s3, s2
	s_lshl_b32 s2, s2, 8
	v_readfirstlane_b32 s3, v2
	s_add_i32 s12, s2, s3
	v_readfirstlane_b32 s2, v1
	s_lshl_b32 s2, s2, 20
	s_add_u32 s14, s0, s2
	s_addc_u32 s15, s1, 0
	s_ashr_i32 s13, s12, 31
	s_lshl_b64 s[0:1], s[12:13], 9
	v_readlane_b32 s2, v251, 32
	v_readlane_b32 s3, v251, 33
	s_add_u32 s16, s2, s0
	s_addc_u32 s17, s3, s1
	s_add_i32 s13, s4, 0
	s_add_i32 s35, s13, 0x10000
	s_add_i32 s36, s13, 0x12000
	s_mov_b32 m0, s35
	s_add_u32 s0, s14, 0x200
	global_load_lds_dwordx4 v64, s[14:15]
	s_mov_b32 m0, s36
	s_addc_u32 s1, s15, 0
	s_add_i32 s37, s13, 0x14000
	global_load_lds_dwordx4 v198, s[14:15]
	s_mov_b32 m0, s37
	s_add_i32 s38, s13, 0x16000
	global_load_lds_dwordx4 v64, s[0:1]
	s_mov_b32 m0, s38
	s_add_i32 s39, s13, 0x2000
	global_load_lds_dwordx4 v198, s[0:1]
	s_mov_b32 m0, s13
	s_add_i32 s40, s13, 0x4000
	global_load_lds_dwordx4 v202, s[16:17]
	s_mov_b32 m0, s39
	s_add_i32 s41, s13, 0x6000
	global_load_lds_dwordx4 v196, s[16:17]
	s_mov_b32 m0, s40
	v_readlane_b32 s2, v249, 47
	global_load_lds_dwordx4 v200, s[16:17]
	s_mov_b32 m0, s41
	v_readlane_b32 s3, v249, 48
	global_load_lds_dwordx4 v194, s[16:17]
	s_nop 0
	v_cndmask_b32_e64 v1, 0, 1, s[2:3]
	v_cmp_ne_u32_e64 s[0:1], 1, v1
	s_andn2_b64 vcc, exec, s[2:3]
	s_cbranch_vccnz .LBB0_1404
	s_barrier
	s_setprio 1

; #define PG8_STAGE_B(bufoff, gbase) do { _Pragma("unroll") for (int _i = 0; _i < 2; ++_i) \
;         __builtin_amdgcn_global_load_lds((const unsigned*)((const char*)(gbase) + voffB[_i]), (LAS unsigned*)(lds + (bufoff) + ldsw + _i * 8192), 16, 0, 0); } while (0)
; #define PG8_STAGE_A(bufoff, gbase, VO, h) do { _Pragma("unroll") for (int _i = 0; _i < 2; ++_i) \
;         __builtin_amdgcn_global_load_lds((const unsigned*)((const char*)(gbase) + (VO)[h][_i]), (LAS unsigned*)(lds + (bufoff) + ldsw + _i * 8192), 16, 0, 0); } while (0)
; #define PG8_WAIT_V(n) asm volatile("s_waitcnt vmcnt(" #n ")" ::: "memory")
; #define PG8_WAIT_L(n) asm volatile("s_waitcnt lgkmcnt(" #n ")" ::: "memory")
; #define PG8_WAIT_VX(rx) do { if (rx) asm volatile("s_waitcnt vmcnt(%0)" :: "n"(8 + Epi::NVM) : "memory"); else asm volatile("s_waitcnt vmcnt(8)" ::: "memory"); } while (0)
; #define PG8_BAR __builtin_amdgcn_s_barrier()
; #define PG8_SCHED __builtin_amdgcn_sched_barrier(0)
;     ...
;             PG8_WAIT_VX(rx); PG8_WAIT_L(0); PG8_BAR; PG8_MMA(0, 0, At, B0); PG8_MMA(0, 1, At, B1); PG8_BAR; PG8_SCHED;
;             PG8_LDA(At, 1, 1); PG8_STAGE_B(PG8_SB(1, 0), b3); PG8_STAGE_B(PG8_SB(1, 1), b3 + hstepB); PG8_STAGE_A(PG8_SA(1, 0), a3, vo2, 0);
;             PG8_WAIT_V(8); PG8_WAIT_L(0); PG8_BAR; PG8_MMA(1, 0, At, B0); PG8_MMA(1, 1, At, B1); PG8_BAR; PG8_SCHED;
.LBB0_1410:
	s_xor_b64 s[26:27], s[22:23], -1
	s_waitcnt lgkmcnt(0)
	s_add_u32 s2, s24, 0x40000
	s_addc_u32 s3, s25, 0
	s_barrier
	s_waitcnt lgkmcnt(0)
	v_mfma_scale_f32_16x16x128_f8f6f4 v[190:193], v[24:31], v[56:63], v[190:193], v226, v228 op_sel_hi:[0,0,0]
	v_mfma_scale_f32_16x16x128_f8f6f4 v[186:189], v[16:23], v[56:63], v[186:189], v226, v228 op_sel_hi:[0,0,0]
	v_mfma_scale_f32_16x16x128_f8f6f4 v[178:181], v[24:31], v[48:55], v[178:181], v226, v228 op_sel_hi:[0,0,0]
	v_mfma_scale_f32_16x16x128_f8f6f4 v[170:173], v[16:23], v[48:55], v[170:173], v226, v228 op_sel_hi:[0,0,0]
	v_mfma_scale_f32_16x16x128_f8f6f4 v[162:165], v[24:31], v[40:47], v[162:165], v226, v228 op_sel_hi:[0,0,0]
	v_mfma_scale_f32_16x16x128_f8f6f4 v[154:157], v[16:23], v[40:47], v[154:157], v226, v228 op_sel_hi:[0,0,0]
	v_mfma_scale_f32_16x16x128_f8f6f4 v[146:149], v[24:31], v[32:39], v[146:149], v226, v228 op_sel_hi:[0,0,0]
	v_mfma_scale_f32_16x16x128_f8f6f4 v[138:141], v[16:23], v[32:39], v[138:141], v226, v228 op_sel_hi:[0,0,0]
	v_mfma_scale_f32_16x16x128_f8f6f4 v[182:185], v[8:15], v[56:63], v[182:185], v226, v228 op_sel_hi:[0,0,0]
	v_mfma_scale_f32_16x16x128_f8f6f4 v[174:177], v[0:7], v[56:63], v[174:177], v226, v228 op_sel_hi:[0,0,0]
	v_mfma_scale_f32_16x16x128_f8f6f4 v[166:169], v[8:15], v[48:55], v[166:169], v226, v228 op_sel_hi:[0,0,0]
	v_mfma_scale_f32_16x16x128_f8f6f4 v[158:161], v[0:7], v[48:55], v[158:161], v226, v228 op_sel_hi:[0,0,0]
	v_mfma_scale_f32_16x16x128_f8f6f4 v[150:153], v[8:15], v[40:47], v[150:153], v226, v228 op_sel_hi:[0,0,0]
	v_mfma_scale_f32_16x16x128_f8f6f4 v[142:145], v[0:7], v[40:47], v[142:145], v226, v228 op_sel_hi:[0,0,0]
	v_mfma_scale_f32_16x16x128_f8f6f4 v[134:137], v[8:15], v[32:39], v[134:137], v226, v228 op_sel_hi:[0,0,0]
	v_mfma_scale_f32_16x16x128_f8f6f4 v[130:133], v[0:7], v[32:39], v[130:133], v226, v228 op_sel_hi:[0,0,0]
	s_barrier
	s_mov_b32 m0, s42
	v_lshl_add_u64 v[214:215], s[2:3], 0, v[64:65]
	ds_read_b128 v[32:35], v212 offset:49152
	ds_read_b128 v[36:39], v212 offset:50176
	ds_read_b128 v[40:43], v212 offset:51200
	ds_read_b128 v[44:47], v212 offset:52224
	ds_read_b128 v[48:51], v212 offset:53248
	ds_read_b128 v[52:55], v212 offset:54272
	ds_read_b128 v[56:59], v212 offset:55296
	ds_read_b128 v[60:63], v212 offset:56320
	global_load_lds_dwordx4 v[214:215], off
	v_lshl_add_u64 v[214:215], s[2:3], 0, v[198:199]
	s_add_u32 s2, s24, 0x40200
	s_mov_b32 m0, s43
	s_addc_u32 s3, s25, 0
	global_load_lds_dwordx4 v[214:215], off
	v_lshl_add_u64 v[214:215], s[2:3], 0, v[64:65]
	s_mov_b32 m0, s46
	v_lshl_add_u64 v[206:207], v[206:207], 0, s[94:95]
	global_load_lds_dwordx4 v[214:215], off
	v_lshl_add_u64 v[214:215], s[2:3], 0, v[198:199]
	s_mov_b32 m0, s47
	s_nop 0
	global_load_lds_dwordx4 v[214:215], off
	s_mov_b32 m0, s44
	s_nop 0
	global_load_lds_dwordx4 v[206:207], off
	v_lshl_add_u64 v[206:207], v[208:209], 0, s[94:95]
	s_mov_b32 m0, s45
	s_nop 0
	global_load_lds_dwordx4 v[206:207], off
	s_waitcnt vmcnt(8)
	s_waitcnt lgkmcnt(0)
	s_barrier
	s_waitcnt lgkmcnt(0)
	v_mfma_scale_f32_16x16x128_f8f6f4 v[126:129], v[24:31], v[32:39], v[126:129], v226, v228 op_sel_hi:[0,0,0]
	v_mfma_scale_f32_16x16x128_f8f6f4 v[122:125], v[16:23], v[32:39], v[122:125], v226, v228 op_sel_hi:[0,0,0]
	v_mfma_scale_f32_16x16x128_f8f6f4 v[114:117], v[24:31], v[40:47], v[114:117], v226, v228 op_sel_hi:[0,0,0]
	v_mfma_scale_f32_16x16x128_f8f6f4 v[106:109], v[16:23], v[40:47], v[106:109], v226, v228 op_sel_hi:[0,0,0]
	v_mfma_scale_f32_16x16x128_f8f6f4 v[90:93], v[24:31], v[48:55], v[90:93], v226, v228 op_sel_hi:[0,0,0]
	v_mfma_scale_f32_16x16x128_f8f6f4 v[82:85], v[16:23], v[48:55], v[82:85], v226, v228 op_sel_hi:[0,0,0]
	v_mfma_scale_f32_16x16x128_f8f6f4 v[70:73], v[24:31], v[56:63], v[70:73], v226, v228 op_sel_hi:[0,0,0]
	v_mfma_scale_f32_16x16x128_f8f6f4 v[66:69], v[16:23], v[56:63], v[66:69], v226, v228 op_sel_hi:[0,0,0]
	v_mfma_scale_f32_16x16x128_f8f6f4 v[118:121], v[8:15], v[32:39], v[118:121], v226, v228 op_sel_hi:[0,0,0]
	v_mfma_scale_f32_16x16x128_f8f6f4 v[110:113], v[0:7], v[32:39], v[110:113], v226, v228 op_sel_hi:[0,0,0]
	v_mfma_scale_f32_16x16x128_f8f6f4 v[94:97], v[8:15], v[40:47], v[94:97], v226, v228 op_sel_hi:[0,0,0]
	v_mfma_scale_f32_16x16x128_f8f6f4 v[86:89], v[0:7], v[40:47], v[86:89], v226, v228 op_sel_hi:[0,0,0]
	v_mfma_scale_f32_16x16x128_f8f6f4 v[102:105], v[8:15], v[48:55], v[102:105], v226, v228 op_sel_hi:[0,0,0]
	v_mfma_scale_f32_16x16x128_f8f6f4 v[98:101], v[0:7], v[48:55], v[98:101], v226, v228 op_sel_hi:[0,0,0]
	v_mfma_scale_f32_16x16x128_f8f6f4 v[78:81], v[8:15], v[56:63], v[78:81], v226, v228 op_sel_hi:[0,0,0]
	v_mfma_scale_f32_16x16x128_f8f6f4 v[74:77], v[0:7], v[56:63], v[74:77], v226, v228 op_sel_hi:[0,0,0]
	s_barrier
	s_mov_b32 s5, 2
	s_mov_b64 s[22:23], 0
	s_mov_b64 s[2:3], -1
	s_and_b64 vcc, exec, s[26:27]
	s_cbranch_vccnz .LBB0_1423

; #define PG8_STAGE_B(bufoff, gbase) do { _Pragma("unroll") for (int _i = 0; _i < 2; ++_i) \
;         __builtin_amdgcn_global_load_lds((const unsigned*)((const char*)(gbase) + voffB[_i]), (LAS unsigned*)(lds + (bufoff) + ldsw + _i * 8192), 16, 0, 0); } while (0)
; #define PG8_STAGE_A(bufoff, gbase, VO, h) do { _Pragma("unroll") for (int _i = 0; _i < 2; ++_i) \
;         __builtin_amdgcn_global_load_lds((const unsigned*)((const char*)(gbase) + (VO)[h][_i]), (LAS unsigned*)(lds + (bufoff) + ldsw + _i * 8192), 16, 0, 0); } while (0)
; #define PG8_WAIT_L(n) asm volatile("s_waitcnt lgkmcnt(" #n ")" ::: "memory")
; #define PG8_WAIT_VX(rx) do { if (rx) asm volatile("s_waitcnt vmcnt(%0)" :: "n"(8 + Epi::NVM) : "memory"); else asm volatile("s_waitcnt vmcnt(8)" ::: "memory"); } while (0)
; #define PG8_BAR __builtin_amdgcn_s_barrier()
; #define PG8_SCHED __builtin_amdgcn_sched_barrier(0)
;     ...
;             const bool last = (t == nt - 2); int rxi = (relax && t == 0) ? 1 : 0; asm volatile("" : "+v"(rxi)); const bool rx = __builtin_amdgcn_readfirstlane(rxi) != 0;
;             if constexpr (Epi::HAS_MID) { constexpr int SEGT = (F8 != 0) ? 8 : 16; if (t == SEGT || t == 2 * SEGT) { PG8_SCHED; E.mid(acc, cur, t / SEGT, wr, wc, fr, fq); PG8_SCHED; } }
;             const char* a1 = cA + (size_t)(t + 1) * kstep;
;             const char* a2 = last ? nA : cA + (size_t)(t + 2) * kstep; const char* b2 = last ? nB : cB + (size_t)(t + 2) * kstepB;
;             const char* a3 = a2 + kstep; const char* b3 = b2 + kstepB;
;             unsigned vo2[2][2];
; #pragma unroll
;             for (int h = 0; h < 2; ++h)
; #pragma unroll
;                 for (int i = 0; i < 2; ++i) vo2[h][i] = (GATHER && last) ? voffN[h][i] : voffA[h][i];
;             PG8_LDB(B0, 0, 0); PG8_LDB(B1, 0, 1); PG8_SCHED; PG8_LDA(At, 0, 0); if (!rx) PG8_STAGE_A(PG8_SA(1, 1), a1, voffA, 1);
;             PG8_WAIT_VX(rx); PG8_WAIT_L(0); PG8_BAR; PG8_MMA(0, 0, At, B0); PG8_MMA(0, 1, At, B1); PG8_BAR; PG8_SCHED;
;             PG8_LDA(At, 0, 1); PG8_STAGE_B(PG8_SB(0, 0), b2); PG8_STAGE_B(PG8_SB(0, 1), b2 + hstepB); PG8_STAGE_A(PG8_SA(0, 0), a2, vo2, 0);
.LBB0_1415:
	s_add_u32 s7, s24, 0x100
	s_addc_u32 s26, s25, 0
	s_and_b64 s[24:25], s[2:3], exec
	s_cselect_b32 s27, s11, s26
	s_cselect_b32 s26, s10, s7
	s_lshl_b32 s5, s5, 18
	s_add_u32 s5, s14, s5
	s_addc_u32 s7, s15, 0
	s_add_u32 s5, s5, 0x80000
	s_addc_u32 s7, s7, 0
	s_waitcnt lgkmcnt(0)
	s_and_b64 s[2:3], s[2:3], exec
	s_cselect_b32 s25, s9, s7
	s_cselect_b32 s24, s8, s5
	s_barrier
	s_waitcnt lgkmcnt(0)
	v_mfma_scale_f32_16x16x128_f8f6f4 v[190:193], v[24:31], v[56:63], v[190:193], v226, v228 op_sel_hi:[0,0,0]
	v_mfma_scale_f32_16x16x128_f8f6f4 v[186:189], v[16:23], v[56:63], v[186:189], v226, v228 op_sel_hi:[0,0,0]
	v_mfma_scale_f32_16x16x128_f8f6f4 v[178:181], v[24:31], v[48:55], v[178:181], v226, v228 op_sel_hi:[0,0,0]
	v_mfma_scale_f32_16x16x128_f8f6f4 v[170:173], v[16:23], v[48:55], v[170:173], v226, v228 op_sel_hi:[0,0,0]
	v_mfma_scale_f32_16x16x128_f8f6f4 v[162:165], v[24:31], v[40:47], v[162:165], v226, v228 op_sel_hi:[0,0,0]
	v_mfma_scale_f32_16x16x128_f8f6f4 v[154:157], v[16:23], v[40:47], v[154:157], v226, v228 op_sel_hi:[0,0,0]
	v_mfma_scale_f32_16x16x128_f8f6f4 v[146:149], v[24:31], v[32:39], v[146:149], v226, v228 op_sel_hi:[0,0,0]
	v_mfma_scale_f32_16x16x128_f8f6f4 v[138:141], v[16:23], v[32:39], v[138:141], v226, v228 op_sel_hi:[0,0,0]
	v_mfma_scale_f32_16x16x128_f8f6f4 v[182:185], v[8:15], v[56:63], v[182:185], v226, v228 op_sel_hi:[0,0,0]
	v_mfma_scale_f32_16x16x128_f8f6f4 v[174:177], v[0:7], v[56:63], v[174:177], v226, v228 op_sel_hi:[0,0,0]
	v_mfma_scale_f32_16x16x128_f8f6f4 v[166:169], v[8:15], v[48:55], v[166:169], v226, v228 op_sel_hi:[0,0,0]
	v_mfma_scale_f32_16x16x128_f8f6f4 v[158:161], v[0:7], v[48:55], v[158:161], v226, v228 op_sel_hi:[0,0,0]
	v_mfma_scale_f32_16x16x128_f8f6f4 v[150:153], v[8:15], v[40:47], v[150:153], v226, v228 op_sel_hi:[0,0,0]
	v_mfma_scale_f32_16x16x128_f8f6f4 v[142:145], v[0:7], v[40:47], v[142:145], v226, v228 op_sel_hi:[0,0,0]
	v_mfma_scale_f32_16x16x128_f8f6f4 v[134:137], v[8:15], v[32:39], v[134:137], v226, v228 op_sel_hi:[0,0,0]
	v_mfma_scale_f32_16x16x128_f8f6f4 v[130:133], v[0:7], v[32:39], v[130:133], v226, v228 op_sel_hi:[0,0,0]
	s_barrier
	s_mov_b32 m0, s35
	v_lshl_add_u64 v[206:207], s[24:25], 0, v[64:65]
	s_add_u32 s2, s24, 0x200
	ds_read_b128 v[56:59], v212 offset:16384
	ds_read_b128 v[60:63], v212 offset:17408
	ds_read_b128 v[48:51], v212 offset:18432
	ds_read_b128 v[52:55], v212 offset:19456
	ds_read_b128 v[40:43], v212 offset:20480
	ds_read_b128 v[44:47], v212 offset:21504
	ds_read_b128 v[32:35], v212 offset:22528
	ds_read_b128 v[36:39], v212 offset:23552
	global_load_lds_dwordx4 v[206:207], off
	v_lshl_add_u64 v[206:207], s[24:25], 0, v[198:199]
	s_mov_b32 m0, s36
	s_addc_u32 s3, s25, 0
	global_load_lds_dwordx4 v[206:207], off
	v_lshl_add_u64 v[206:207], s[2:3], 0, v[64:65]
	s_mov_b32 m0, s37
	v_lshl_add_u64 v[208:209], s[26:27], 0, v[196:197]
	global_load_lds_dwordx4 v[206:207], off
	v_lshl_add_u64 v[206:207], s[2:3], 0, v[198:199]
	s_mov_b32 m0, s38
	v_cndmask_b32_e64 v213, 0, 1, s[28:29]
	global_load_lds_dwordx4 v[206:207], off
	v_lshl_add_u64 v[206:207], s[26:27], 0, v[202:203]
	s_mov_b32 m0, s13
	v_cmp_ne_u32_e64 s[2:3], 1, v213
	global_load_lds_dwordx4 v[206:207], off
	s_mov_b32 m0, s39
	s_andn2_b64 vcc, exec, s[28:29]
	global_load_lds_dwordx4 v[208:209], off
	s_cbranch_vccnz .LBB0_1420
	s_waitcnt vmcnt(16)
	s_cbranch_execnz .LBB0_1418

; #define PG8_STAGE_A(bufoff, gbase, VO, h) do { _Pragma("unroll") for (int _i = 0; _i < 2; ++_i) \
;         __builtin_amdgcn_global_load_lds((const unsigned*)((const char*)(gbase) + (VO)[h][_i]), (LAS unsigned*)(lds + (bufoff) + ldsw + _i * 8192), 16, 0, 0); } while (0)
; #define PG8_WAIT_L(n) asm volatile("s_waitcnt lgkmcnt(" #n ")" ::: "memory")
; #define PG8_WAIT_VX(rx) do { if (rx) asm volatile("s_waitcnt vmcnt(%0)" :: "n"(8 + Epi::NVM) : "memory"); else asm volatile("s_waitcnt vmcnt(8)" ::: "memory"); } while (0)
; #define PG8_BAR __builtin_amdgcn_s_barrier()
; #define PG8_SCHED __builtin_amdgcn_sched_barrier(0)
;     ...
;             PG8_WAIT_VX(rx); PG8_WAIT_L(0); PG8_BAR; PG8_MMA(1, 0, At, B0); PG8_MMA(1, 1, At, B1); PG8_BAR; PG8_SCHED;
;             PG8_LDB(B0, 1, 0); PG8_LDB(B1, 1, 1); PG8_SCHED; PG8_LDA(At, 1, 0); PG8_STAGE_A(PG8_SA(0, 1), a2, vo2, 1);
.LBB0_1418:
	s_waitcnt lgkmcnt(0)
	s_barrier
	s_waitcnt lgkmcnt(0)
	v_mfma_scale_f32_16x16x128_f8f6f4 v[126:129], v[24:31], v[56:63], v[126:129], v226, v228 op_sel_hi:[0,0,0]
	v_mfma_scale_f32_16x16x128_f8f6f4 v[122:125], v[16:23], v[56:63], v[122:125], v226, v228 op_sel_hi:[0,0,0]
	v_mfma_scale_f32_16x16x128_f8f6f4 v[114:117], v[24:31], v[48:55], v[114:117], v226, v228 op_sel_hi:[0,0,0]
	v_mfma_scale_f32_16x16x128_f8f6f4 v[106:109], v[16:23], v[48:55], v[106:109], v226, v228 op_sel_hi:[0,0,0]
	v_mfma_scale_f32_16x16x128_f8f6f4 v[90:93], v[24:31], v[40:47], v[90:93], v226, v228 op_sel_hi:[0,0,0]
	v_mfma_scale_f32_16x16x128_f8f6f4 v[82:85], v[16:23], v[40:47], v[82:85], v226, v228 op_sel_hi:[0,0,0]
	v_mfma_scale_f32_16x16x128_f8f6f4 v[70:73], v[24:31], v[32:39], v[70:73], v226, v228 op_sel_hi:[0,0,0]
	v_mfma_scale_f32_16x16x128_f8f6f4 v[66:69], v[16:23], v[32:39], v[66:69], v226, v228 op_sel_hi:[0,0,0]
	v_mfma_scale_f32_16x16x128_f8f6f4 v[118:121], v[8:15], v[56:63], v[118:121], v226, v228 op_sel_hi:[0,0,0]
	v_mfma_scale_f32_16x16x128_f8f6f4 v[110:113], v[0:7], v[56:63], v[110:113], v226, v228 op_sel_hi:[0,0,0]
	v_mfma_scale_f32_16x16x128_f8f6f4 v[94:97], v[8:15], v[48:55], v[94:97], v226, v228 op_sel_hi:[0,0,0]
	v_mfma_scale_f32_16x16x128_f8f6f4 v[86:89], v[0:7], v[48:55], v[86:89], v226, v228 op_sel_hi:[0,0,0]
	v_mfma_scale_f32_16x16x128_f8f6f4 v[102:105], v[8:15], v[40:47], v[102:105], v226, v228 op_sel_hi:[0,0,0]
	v_mfma_scale_f32_16x16x128_f8f6f4 v[98:101], v[0:7], v[40:47], v[98:101], v226, v228 op_sel_hi:[0,0,0]
	v_mfma_scale_f32_16x16x128_f8f6f4 v[78:81], v[8:15], v[32:39], v[78:81], v226, v228 op_sel_hi:[0,0,0]
	v_mfma_scale_f32_16x16x128_f8f6f4 v[74:77], v[0:7], v[32:39], v[74:77], v226, v228 op_sel_hi:[0,0,0]
	s_barrier
	v_add_u32_e32 v0, 0x18000, v211
	v_add_u32_e32 v4, 0x1c000, v211
	ds_read_b128 v[24:27], v0
	ds_read_b128 v[28:31], v0 offset:1024
	ds_read_b128 v[16:19], v0 offset:2048
	ds_read_b128 v[20:23], v0 offset:3072
	ds_read_b128 v[8:11], v4
	ds_read_b128 v[12:15], v4 offset:1024
	ds_read_b128 v[0:3], v4 offset:2048
	ds_read_b128 v[4:7], v4 offset:3072
	s_mov_b32 m0, s40
	v_lshl_add_u64 v[214:215], s[26:27], 0, v[200:201]
	ds_read_b128 v[56:59], v212 offset:32768
	ds_read_b128 v[60:63], v212 offset:33792
	ds_read_b128 v[48:51], v212 offset:34816
	ds_read_b128 v[52:55], v212 offset:35840
	ds_read_b128 v[40:43], v212 offset:36864
	ds_read_b128 v[44:47], v212 offset:37888
	ds_read_b128 v[32:35], v212 offset:38912
	ds_read_b128 v[36:39], v212 offset:39936
	global_load_lds_dwordx4 v[214:215], off
	v_lshl_add_u64 v[214:215], s[26:27], 0, v[194:195]
	s_mov_b32 m0, s41
	s_and_b64 vcc, exec, s[2:3]
	global_load_lds_dwordx4 v[214:215], off
	s_cbranch_vccnz .LBB0_1421
	s_waitcnt vmcnt(16)
	s_cbranch_execnz .LBB0_1410
	s_branch .LBB0_1422
